# baseline (speedup 1.0000x reference)
_Z8k_stageAPKfS0_S0_S0_PDF16_PKDF16_S0_S1_ii:
	s_load_dwordx2 s[64:65], s[0:1], 0x40
	v_readfirstlane_b32 s94, v0
	s_nop 0
	s_lshr_b32 s94, s94, 6
	s_load_dwordx8 s[4:11], s[0:1], 0x0
	v_readfirstlane_b32 s14, v0
	s_lshr_b32 s15, s2, 5
	s_lshl_b32 s2, s2, 7
	s_lshr_b32 s20, s14, 6
	s_and_b32 s12, s2, 0xf80
	s_lshl_b32 s13, s15, 12
	s_mov_b32 s18, s3
	s_cmpk_lt_u32 s14, 0x100
	s_waitcnt lgkmcnt(0)
	s_cselect_b32 s2, s4, s6
	s_cselect_b32 s3, s5, s7
	s_cselect_b32 s4, s8, s10
	s_cselect_b32 s5, s9, s11
	s_cmp_eq_u32 s18, 0
	s_cselect_b32 s3, s3, s5
	s_cselect_b32 s2, s2, s4
	s_lshr_b32 s5, s14, 1
	s_lshl_b32 s4, s15, 7
	s_and_b32 s5, s5, 0x60
	v_bfe_u32 v1, v0, 5, 1
	s_or_b32 s4, s5, s4
	v_lshl_or_b32 v82, v1, 3, s4
	v_mov_b32_e32 v83, 0
	v_lshlrev_b64 v[2:3], 14, v[82:83]
	v_lshlrev_b32_e32 v78, 2, v0
	s_mov_b32 s17, 0
	v_lshl_add_u64 v[2:3], s[2:3], 0, v[2:3]
	s_lshl_b32 s16, s12, 2
	v_and_b32_e32 v79, 0x7c, v78
	v_lshl_add_u64 v[2:3], v[2:3], 0, s[16:17]
	v_lshlrev_b32_e32 v82, 2, v79
	v_lshl_add_u64 v[42:43], v[2:3], 0, v[82:83]
	s_movk_i32 s21, 0x4000
	v_add_co_u32_e32 v10, vcc, s21, v42
	s_mov_b32 s2, 0x8000
	s_nop 0
	v_addc_co_u32_e32 v11, vcc, 0, v43, vcc
	v_add_co_u32_e32 v18, vcc, s2, v42
	s_mov_b32 s2, 0xc000
	s_nop 0
	v_addc_co_u32_e32 v19, vcc, 0, v43, vcc
	v_add_co_u32_e32 v20, vcc, s2, v42
	s_mov_b32 s14, 0x10000
	s_nop 0
	v_addc_co_u32_e32 v21, vcc, 0, v43, vcc
	v_add_co_u32_e32 v26, vcc, s14, v42
	s_mov_b32 s2, 0x14000
	s_nop 0
	v_addc_co_u32_e32 v27, vcc, 0, v43, vcc
	v_add_co_u32_e32 v28, vcc, s2, v42
	s_mov_b32 s2, 0x18000
	s_nop 0
	v_addc_co_u32_e32 v29, vcc, 0, v43, vcc
	v_add_co_u32_e32 v34, vcc, s2, v42
	s_mov_b32 s2, 0x1c000
	s_nop 0
	v_addc_co_u32_e32 v35, vcc, 0, v43, vcc
	v_add_co_u32_e32 v36, vcc, s2, v42
	s_mov_b32 s2, 0x40000
	s_nop 0
	v_addc_co_u32_e32 v37, vcc, 0, v43, vcc
	v_add_co_u32_e32 v66, vcc, s2, v42
	s_mov_b32 s2, 0x44000
	s_nop 0
	v_addc_co_u32_e32 v67, vcc, 0, v43, vcc
	v_add_co_u32_e32 v68, vcc, s2, v42
	s_mov_b32 s2, 0x48000
	s_nop 0
	v_addc_co_u32_e32 v69, vcc, 0, v43, vcc
	global_load_dwordx4 v[2:5], v[42:43], off nt
	global_load_dwordx4 v[6:9], v[10:11], off nt
	v_add_co_u32_e32 v44, vcc, s2, v42
	global_load_dwordx4 v[10:13], v[18:19], off nt
	global_load_dwordx4 v[14:17], v[20:21], off nt
	s_nop 0
	global_load_dwordx4 v[18:21], v[26:27], off nt
	global_load_dwordx4 v[22:25], v[28:29], off nt
	s_nop 0
	global_load_dwordx4 v[26:29], v[34:35], off nt
	global_load_dwordx4 v[30:33], v[36:37], off nt
	v_addc_co_u32_e32 v45, vcc, 0, v43, vcc
	s_mov_b32 s2, 0x4c000
	v_add_co_u32_e32 v46, vcc, s2, v42
	s_mov_b32 s2, 0x50000
	s_nop 0
	v_addc_co_u32_e32 v47, vcc, 0, v43, vcc
	v_add_co_u32_e32 v70, vcc, s2, v42
	s_mov_b32 s2, 0x54000
	s_nop 0
	v_addc_co_u32_e32 v71, vcc, 0, v43, vcc
	v_add_co_u32_e32 v72, vcc, s2, v42
	s_mov_b32 s2, 0x58000
	s_nop 0
	v_addc_co_u32_e32 v73, vcc, 0, v43, vcc
	v_add_co_u32_e32 v74, vcc, s2, v42
	s_mov_b32 s2, 0x5c000
	s_nop 0
	v_addc_co_u32_e32 v75, vcc, 0, v43, vcc
	v_add_co_u32_e32 v76, vcc, s2, v42
	global_load_dwordx4 v[34:37], v[44:45], off nt
	global_load_dwordx4 v[38:41], v[46:47], off nt
	v_addc_co_u32_e32 v77, vcc, 0, v43, vcc
	global_load_dwordx4 v[42:45], v[74:75], off nt
	global_load_dwordx4 v[46:49], v[76:77], off nt
	global_load_dwordx4 v[50:53], v[70:71], off nt
	global_load_dwordx4 v[54:57], v[72:73], off nt
	global_load_dwordx4 v[58:61], v[66:67], off nt
	global_load_dwordx4 v[62:65], v[68:69], off nt
	v_lshl_or_b32 v1, s20, 2, v1
	v_lshrrev_b32_e32 v70, 5, v0
	v_or_b32_e32 v141, 0x200, v0
	v_or_b32_e32 v142, 0x600, v0
	s_or_b32 s16, s13, s12
	s_ashr_i32 s19, s18, 31
	s_lshl_b64 s[12:13], s[16:17], 9
	s_mov_b32 s15, 0x20000
	v_or_b32_e32 v144, 0xa00, v0
	v_bfe_u32 v140, v0, 4, 2
	v_and_b32_e32 v145, 15, v0
	v_lshlrev_b32_e32 v220, 9, v145
	s_waitcnt vmcnt(14)
	v_cvt_pk_f16_f32 v66, v2, v6
	v_lshlrev_b32_e32 v6, 9, v79
	v_bitop3_b32 v2, v78, v1, 12 bitop3:0x6c
	s_waitcnt vmcnt(12)
	v_cvt_pk_f16_f32 v67, v10, v14
	s_waitcnt vmcnt(10)
	v_cvt_pk_f16_f32 v68, v18, v22
	s_waitcnt vmcnt(8)
	v_cvt_pk_f16_f32 v69, v26, v30
	v_lshl_add_u32 v2, v2, 4, v6
	ds_write_b128 v2, v[66:69]
	v_cvt_pk_f16_f32 v66, v3, v7
	v_or_b32_e32 v7, 1, v79
	v_lshlrev_b32_e32 v10, 9, v7
	v_bitop3_b32 v2, v7, v1, 13 bitop3:0x6c
	v_cvt_pk_f16_f32 v69, v27, v31
	v_cvt_pk_f16_f32 v68, v19, v23
	v_cvt_pk_f16_f32 v67, v11, v15
	v_lshl_add_u32 v2, v2, 4, v10
	ds_write_b128 v2, v[66:69]
	v_cvt_pk_f16_f32 v66, v4, v8
	v_or_b32_e32 v8, 2, v79
	v_lshlrev_b32_e32 v11, 9, v8
	v_bitop3_b32 v2, v8, v1, 14 bitop3:0x6c
	v_cvt_pk_f16_f32 v69, v28, v32
	v_cvt_pk_f16_f32 v68, v20, v24
	v_cvt_pk_f16_f32 v67, v12, v16
	v_lshl_add_u32 v2, v2, 4, v11
	v_cvt_pk_f16_f32 v12, v5, v9
	v_or_b32_e32 v9, 3, v79
	ds_write_b128 v2, v[66:69]
	v_lshlrev_b32_e32 v16, 9, v9
	v_bitop3_b32 v2, v9, v1, 15 bitop3:0x6c
	v_cvt_pk_f16_f32 v15, v29, v33
	v_cvt_pk_f16_f32 v14, v21, v25
	v_cvt_pk_f16_f32 v13, v13, v17
	v_lshl_add_u32 v2, v2, 4, v16
	v_or_b32_e32 v1, 2, v1
	ds_write_b128 v2, v[12:15]
	v_bitop3_b32 v12, v78, v1, 12 bitop3:0x6c
	s_waitcnt vmcnt(4)
	v_cvt_pk_f16_f32 v5, v42, v46
	s_waitcnt vmcnt(2)
	v_cvt_pk_f16_f32 v4, v50, v54
	v_cvt_pk_f16_f32 v3, v34, v38
	s_waitcnt vmcnt(0)
	v_cvt_pk_f16_f32 v2, v58, v62
	v_lshl_add_u32 v6, v12, 4, v6
	ds_write_b128 v6, v[2:5]
	v_bitop3_b32 v6, v7, v1, 13 bitop3:0x6c
	v_cvt_pk_f16_f32 v5, v43, v47
	v_cvt_pk_f16_f32 v4, v51, v55
	v_cvt_pk_f16_f32 v3, v35, v39
	v_cvt_pk_f16_f32 v2, v59, v63
	v_lshl_add_u32 v6, v6, 4, v10
	ds_write_b128 v6, v[2:5]
	v_bitop3_b32 v6, v8, v1, 14 bitop3:0x6c
	v_cvt_pk_f16_f32 v5, v44, v48
	v_cvt_pk_f16_f32 v4, v52, v56
	v_cvt_pk_f16_f32 v3, v36, v40
	v_cvt_pk_f16_f32 v2, v60, v64
	v_lshl_add_u32 v6, v6, 4, v11
	v_bitop3_b32 v1, v9, v1, 15 bitop3:0x6c
	ds_write_b128 v6, v[2:5]
	v_cvt_pk_f16_f32 v5, v45, v49
	v_cvt_pk_f16_f32 v4, v53, v57
	v_cvt_pk_f16_f32 v3, v37, v41
	v_cvt_pk_f16_f32 v2, v61, v65
	v_lshl_add_u32 v1, v1, 4, v16
	ds_write_b128 v1, v[2:5]
	v_bitop3_b32 v2, v70, v0, 31 bitop3:0x78
	v_lshlrev_b32_e32 v1, 9, v70
	v_lshlrev_b32_e32 v22, 4, v2
	v_or_b32_e32 v10, v22, v1
	s_waitcnt lgkmcnt(0)
	s_barrier
	ds_read_b128 v[2:5], v10
	s_load_dwordx8 s[4:11], s[0:1], 0x20
	s_load_dwordx2 s[2:3], s[0:1], 0x40
	v_lshlrev_b32_e32 v24, 4, v0
	v_and_b32_e32 v25, 0x1e00, v24
	v_or_b32_e32 v26, v22, v25
	s_waitcnt lgkmcnt(0)
	v_pk_max_f16 v6, v5, v5
	v_and_b32_e32 v18, 31, v0
	v_pk_max_f16 v9, v6, 0
	v_pk_max_f16 v6, v4, v4
	v_lshlrev_b32_e32 v29, 4, v18
	v_pk_max_f16 v8, v6, 0
	v_pk_max_f16 v6, v3, v3
	s_lshl_b64 s[0:1], s[18:19], 23
	v_pk_max_f16 v7, v6, 0
	v_pk_max_f16 v6, v2, v2
	s_add_u32 s0, s4, s0
	v_pk_max_f16 v6, v6, 0
	ds_write_b128 v10, v[6:9]
	v_lshlrev_b32_e32 v6, 4, v141
	v_and_b32_e32 v23, 0x3e00, v6
	v_or_b32_e32 v14, v22, v23
	ds_read_b128 v[6:9], v14
	s_addc_u32 s1, s5, s1
	s_add_u32 s12, s0, s12
	s_addc_u32 s0, s1, s13
	s_and_b32 s13, s0, 0xffff
	s_waitcnt lgkmcnt(0)
	v_pk_max_f16 v10, v9, v9
	v_or_b32_e32 v1, v1, v29
	v_pk_max_f16 v13, v10, 0
	v_pk_max_f16 v10, v8, v8
	buffer_store_dwordx4 v[2:5], v1, s[12:15], 0 offen sc1
	v_pk_max_f16 v12, v10, 0
	v_pk_max_f16 v10, v7, v7
	v_or_b32_e32 v1, v23, v29
	v_pk_max_f16 v11, v10, 0
	v_pk_max_f16 v10, v6, v6
	buffer_store_dwordx4 v[6:9], v1, s[12:15], 0 offen sc1
	v_pk_max_f16 v10, v10, 0
	ds_write_b128 v14, v[10:13]
	ds_read_b128 v[10:13], v26 offset:16384
	v_or_b32_e32 v25, v25, v29
	v_or_b32_e32 v6, 0x4000, v25
	s_mov_b32 s0, 0xfe00
	s_waitcnt lgkmcnt(0)
	v_pk_max_f16 v14, v13, v13
	s_nop 0
	v_pk_max_f16 v17, v14, 0
	v_pk_max_f16 v14, v12, v12
	buffer_store_dwordx4 v[10:13], v6, s[12:15], 0 offen sc1
	v_pk_max_f16 v16, v14, 0
	v_pk_max_f16 v14, v11, v11
	s_nop 0
	v_pk_max_f16 v15, v14, 0
	v_pk_max_f16 v14, v10, v10
	s_nop 0
	v_pk_max_f16 v14, v14, 0
	ds_write_b128 v26, v[14:17] offset:16384
	v_lshlrev_b32_e32 v14, 4, v142
	v_and_b32_e32 v27, 0x7e00, v14
	v_or_b32_e32 v28, v22, v27
	ds_read_b128 v[14:17], v28
	v_or_b32_e32 v10, v27, v29
	s_waitcnt lgkmcnt(0)
	v_pk_max_f16 v18, v17, v17
	s_nop 0
	v_pk_max_f16 v21, v18, 0
	v_pk_max_f16 v18, v16, v16
	buffer_store_dwordx4 v[14:17], v10, s[12:15], 0 offen sc1
	v_pk_max_f16 v20, v18, 0
	v_pk_max_f16 v18, v15, v15
	v_or_b32_e32 v10, 0x8000, v25
	v_pk_max_f16 v19, v18, 0
	v_pk_max_f16 v18, v14, v14
	s_nop 0
	v_pk_max_f16 v18, v18, 0
	ds_write_b128 v28, v[18:21]
	ds_read_b128 v[18:21], v26 offset:32768
	s_waitcnt lgkmcnt(0)
	v_pk_max_f16 v1, v21, v21
	s_nop 0
	v_pk_max_f16 v5, v1, 0
	v_pk_max_f16 v1, v20, v20
	buffer_store_dwordx4 v[18:21], v10, s[12:15], 0 offen sc1
	v_pk_max_f16 v4, v1, 0
	v_pk_max_f16 v1, v19, v19
	s_nop 0
	v_pk_max_f16 v3, v1, 0
	v_pk_max_f16 v1, v18, v18
	s_nop 0
	v_pk_max_f16 v2, v1, 0
	v_lshlrev_b32_e32 v1, 4, v144
	v_and_b32_e32 v1, 0xbe00, v1
	ds_write_b128 v26, v[2:5] offset:32768
	v_or_b32_e32 v23, v22, v1
	ds_read_b128 v[2:5], v23
	v_or_b32_e32 v1, v1, v29
	s_waitcnt lgkmcnt(0)
	v_pk_max_f16 v6, v5, v5
	s_nop 0
	v_pk_max_f16 v9, v6, 0
	v_pk_max_f16 v6, v4, v4
	buffer_store_dwordx4 v[2:5], v1, s[12:15], 0 offen sc1
	v_pk_max_f16 v8, v6, 0
	v_pk_max_f16 v6, v3, v3
	v_or_b32_e32 v1, 0xc000, v25
	v_pk_max_f16 v7, v6, 0
	v_pk_max_f16 v6, v2, v2
	s_nop 0
	v_pk_max_f16 v6, v6, 0
	ds_write_b128 v23, v[6:9]
	ds_read_b128 v[6:9], v26 offset:49152
	s_waitcnt lgkmcnt(0)
	v_pk_max_f16 v10, v9, v9
	s_nop 0
	v_pk_max_f16 v13, v10, 0
	v_pk_max_f16 v10, v8, v8
	buffer_store_dwordx4 v[6:9], v1, s[12:15], 0 offen sc1
	v_pk_max_f16 v12, v10, 0
	v_pk_max_f16 v10, v7, v7
	s_nop 0
	v_pk_max_f16 v11, v10, 0
	v_pk_max_f16 v10, v6, v6
	s_nop 0
	v_pk_max_f16 v10, v10, 0
	ds_write_b128 v26, v[10:13] offset:49152
	v_mov_b32_e32 v10, 0xe000
	v_bitop3_b32 v14, v24, s0, v10 bitop3:0xc8
	s_mul_i32 s0, s3, s18
	v_or_b32_e32 v15, v22, v14
	s_add_i32 s0, s0, s2
	ds_read_b128 v[10:13], v15
	s_mul_i32 s2, s0, 0x60000
	s_mul_hi_i32 s1, s0, 0x60000
	s_add_u32 s2, s6, s2
	s_mulk_i32 s0, 0x300
	s_addc_u32 s3, s7, s1
	s_ashr_i32 s1, s0, 31
	s_lshl_b64 s[0:1], s[0:1], 2
	v_or_b32_e32 v1, v14, v29
	s_add_u32 s4, s8, s0
	s_waitcnt lgkmcnt(0)
	buffer_store_dwordx4 v[10:13], v1, s[12:15], 0 offen sc1
	v_pk_max_f16 v1, v13, v13
	s_addc_u32 s5, s9, s1
	s_mul_i32 s0, s18, 0x1800000
	v_pk_max_f16 v5, v1, 0
	v_pk_max_f16 v1, v12, v12
	s_mul_hi_i32 s1, s18, 0x1800000
	s_add_u32 s0, s10, s0
	v_pk_max_f16 v4, v1, 0
	v_pk_max_f16 v1, v11, v11
	s_addc_u32 s1, s11, s1
	v_pk_max_f16 v3, v1, 0
	v_pk_max_f16 v1, v10, v10
	s_and_b32 s1, s1, 0xffff
	s_mul_i32 s7, s20, 0x6000
	v_pk_max_f16 v2, v1, 0
	v_and_b32_e32 v1, 63, v0
	s_mul_hi_u32 s6, s20, 0x6000
	s_add_u32 s2, s2, s7
	s_addc_u32 s3, s3, s6
	v_lshlrev_b32_e32 v82, 4, v1
	v_lshl_add_u64 v[118:119], s[2:3], 0, v[82:83]
	s_movk_i32 s6, 0x1000
	v_add_co_u32_e32 v50, vcc, s6, v118
	s_movk_i32 s6, 0x2000
	s_nop 0
	v_addc_co_u32_e32 v51, vcc, 0, v119, vcc
	ds_write_b128 v15, v[2:5]
	v_add_co_u32_e32 v52, vcc, s6, v118
	global_load_dwordx4 v[2:5], v82, s[2:3] offset:1024
	global_load_dwordx4 v[6:9], v82, s[2:3] offset:2048
	v_addc_co_u32_e32 v53, vcc, 0, v119, vcc
	global_load_dwordx4 v[10:13], v82, s[2:3] offset:3072
	global_load_dwordx4 v[14:17], v[52:53], off offset:-4096
	global_load_dwordx4 v[18:21], v[50:51], off offset:1024
	global_load_dwordx4 v[22:25], v[50:51], off offset:2048
	global_load_dwordx4 v[26:29], v82, s[2:3]
	global_load_dwordx4 v[30:33], v[50:51], off offset:3072
	global_load_dwordx4 v[34:37], v[52:53], off
	global_load_dwordx4 v[38:41], v[52:53], off offset:1024
	global_load_dwordx4 v[42:45], v[52:53], off offset:2048
	global_load_dwordx4 v[46:49], v[52:53], off offset:3072
	s_movk_i32 s2, 0x3000
	v_add_co_u32_e32 v116, vcc, s2, v118
	s_waitcnt lgkmcnt(0)
	s_nop 0
	v_addc_co_u32_e32 v117, vcc, 0, v119, vcc
	v_add_co_u32_e32 v132, vcc, s21, v118
	s_barrier
	s_nop 0
	v_addc_co_u32_e32 v133, vcc, 0, v119, vcc
	global_load_dwordx4 v[50:53], v[132:133], off offset:-4096
	global_load_dwordx4 v[54:57], v[116:117], off offset:1024
	global_load_dwordx4 v[58:61], v[116:117], off offset:2048
	v_bitop3_b32 v1, v140, v0, 15 bitop3:0x78
	v_lshl_or_b32 v134, v1, 4, v220
	ds_read_b128 v[62:65], v134
	ds_read_b128 v[66:69], v134 offset:8192
	ds_read_b128 v[70:73], v134 offset:16384
	ds_read_b128 v[74:77], v134 offset:24576
	ds_read_b128 v[78:81], v134 offset:32768
	ds_read_b128 v[84:87], v134 offset:40960
	ds_read_b128 v[88:91], v134 offset:49152
	ds_read_b128 v[92:95], v134 offset:57344
	s_mul_i32 s7, s20, 48
	v_lshl_or_b32 v82, v140, 2, s7
	s_mul_i32 s7, s20, 0x60
	s_add_i32 s7, s7, 0x10000
	v_mul_u32_u24_e32 v1, 0x556, v0
	v_lshl_or_b32 v250, v140, 3, s7
	s_or_b32 s7, s16, 64
	v_lshrrev_b32_e32 v143, 16, v1
	s_movk_i32 s6, 0x600
	s_mov_b32 s2, 0x1800000
	s_mov_b32 s3, s15
	v_or_b32_e32 v139, s7, v143
	s_waitcnt vmcnt(8) lgkmcnt(7)
	v_mfma_f32_16x16x32_f16 v[96:99], v[26:29], v[62:65], 0
	s_waitcnt lgkmcnt(6)
	v_mfma_f32_16x16x32_f16 v[100:103], v[26:29], v[66:69], 0
	s_waitcnt lgkmcnt(5)
	v_mfma_f32_16x16x32_f16 v[104:107], v[26:29], v[70:73], 0
	s_waitcnt lgkmcnt(4)
	v_mfma_f32_16x16x32_f16 v[108:111], v[26:29], v[74:77], 0
	s_waitcnt lgkmcnt(3)
	v_mfma_f32_16x16x32_f16 v[112:115], v[26:29], v[78:81], 0
	s_waitcnt lgkmcnt(2)
	v_mfma_f32_16x16x32_f16 v[120:123], v[26:29], v[84:87], 0
	s_waitcnt lgkmcnt(1)
	v_mfma_f32_16x16x32_f16 v[124:127], v[26:29], v[88:91], 0
	s_waitcnt lgkmcnt(0)
	v_mfma_f32_16x16x32_f16 v[26:29], v[26:29], v[92:95], 0
	v_mfma_f32_16x16x32_f16 v[128:131], v[2:5], v[62:65], 0
	v_mfma_f32_16x16x32_f16 v[146:149], v[2:5], v[66:69], 0
	v_mfma_f32_16x16x32_f16 v[150:153], v[2:5], v[70:73], 0
	v_mfma_f32_16x16x32_f16 v[154:157], v[2:5], v[74:77], 0
	v_mfma_f32_16x16x32_f16 v[158:161], v[2:5], v[78:81], 0
	v_mfma_f32_16x16x32_f16 v[162:165], v[2:5], v[84:87], 0
	v_mfma_f32_16x16x32_f16 v[166:169], v[2:5], v[88:91], 0
	v_mfma_f32_16x16x32_f16 v[2:5], v[2:5], v[92:95], 0
	v_mfma_f32_16x16x32_f16 v[62:65], v[6:9], v[62:65], 0
	v_mfma_f32_16x16x32_f16 v[66:69], v[6:9], v[66:69], 0
	v_mfma_f32_16x16x32_f16 v[70:73], v[6:9], v[70:73], 0
	v_mfma_f32_16x16x32_f16 v[74:77], v[6:9], v[74:77], 0
	v_mfma_f32_16x16x32_f16 v[78:81], v[6:9], v[78:81], 0
	v_mfma_f32_16x16x32_f16 v[84:87], v[6:9], v[84:87], 0
	v_mfma_f32_16x16x32_f16 v[88:91], v[6:9], v[88:91], 0
	v_mfma_f32_16x16x32_f16 v[6:9], v[6:9], v[92:95], 0
	global_load_dwordx4 v[92:95], v[116:117], off offset:3072
	global_load_dwordx4 v[170:173], v[132:133], off
	global_load_dwordx4 v[174:177], v[132:133], off offset:1024
	v_bitop3_b32 v1, v140, v145, 4 bitop3:0x36
	v_lshl_or_b32 v1, v1, 4, v220
	ds_read_b128 v[178:181], v1
	ds_read_b128 v[182:185], v1 offset:8192
	ds_read_b128 v[186:189], v1 offset:16384
	ds_read_b128 v[190:193], v1 offset:24576
	ds_read_b128 v[194:197], v1 offset:32768
	ds_read_b128 v[198:201], v1 offset:40960
	ds_read_b128 v[202:205], v1 offset:49152
	ds_read_b128 v[206:209], v1 offset:57344
	s_waitcnt lgkmcnt(7)
	v_mfma_f32_16x16x32_f16 v[96:99], v[10:13], v[178:181], v[96:99]
	s_waitcnt lgkmcnt(6)
	v_mfma_f32_16x16x32_f16 v[100:103], v[10:13], v[182:185], v[100:103]
	s_waitcnt lgkmcnt(5)
	v_mfma_f32_16x16x32_f16 v[104:107], v[10:13], v[186:189], v[104:107]
	s_waitcnt lgkmcnt(4)
	v_mfma_f32_16x16x32_f16 v[108:111], v[10:13], v[190:193], v[108:111]
	s_waitcnt lgkmcnt(3)
	v_mfma_f32_16x16x32_f16 v[112:115], v[10:13], v[194:197], v[112:115]
	s_waitcnt lgkmcnt(2)
	v_mfma_f32_16x16x32_f16 v[120:123], v[10:13], v[198:201], v[120:123]
	s_waitcnt lgkmcnt(1)
	v_mfma_f32_16x16x32_f16 v[124:127], v[10:13], v[202:205], v[124:127]
	s_waitcnt lgkmcnt(0)
	v_mfma_f32_16x16x32_f16 v[10:13], v[10:13], v[206:209], v[26:29]
	v_mfma_f32_16x16x32_f16 v[26:29], v[14:17], v[178:181], v[128:131]
	v_mfma_f32_16x16x32_f16 v[128:131], v[14:17], v[182:185], v[146:149]
	v_mfma_f32_16x16x32_f16 v[146:149], v[14:17], v[186:189], v[150:153]
	v_mfma_f32_16x16x32_f16 v[150:153], v[14:17], v[190:193], v[154:157]
	v_mfma_f32_16x16x32_f16 v[154:157], v[14:17], v[194:197], v[158:161]
	v_mfma_f32_16x16x32_f16 v[158:161], v[14:17], v[198:201], v[162:165]
	v_mfma_f32_16x16x32_f16 v[162:165], v[14:17], v[202:205], v[166:169]
	v_mfma_f32_16x16x32_f16 v[2:5], v[14:17], v[206:209], v[2:5]
	v_mfma_f32_16x16x32_f16 v[14:17], v[18:21], v[178:181], v[62:65]
	v_mfma_f32_16x16x32_f16 v[62:65], v[18:21], v[182:185], v[66:69]
	v_mfma_f32_16x16x32_f16 v[66:69], v[18:21], v[186:189], v[70:73]
	v_mfma_f32_16x16x32_f16 v[70:73], v[18:21], v[190:193], v[74:77]
	v_mfma_f32_16x16x32_f16 v[74:77], v[18:21], v[194:197], v[78:81]
	v_mfma_f32_16x16x32_f16 v[78:81], v[18:21], v[198:201], v[84:87]
	v_mfma_f32_16x16x32_f16 v[84:87], v[18:21], v[202:205], v[88:91]
	v_mfma_f32_16x16x32_f16 v[6:9], v[18:21], v[206:209], v[6:9]
	s_movk_i32 s8, 0x5000
	v_add_co_u32_e32 v116, vcc, s8, v118
	global_load_dwordx4 v[88:91], v[132:133], off offset:2048
	global_load_dwordx4 v[166:169], v[132:133], off offset:3072
	v_addc_co_u32_e32 v117, vcc, 0, v119, vcc
	global_load_dwordx4 v[178:181], v[116:117], off
	v_bitop3_b32 v18, v140, v145, 8 bitop3:0x36
	v_lshl_or_b32 v133, v18, 4, v220
	ds_read_b128 v[18:21], v133
	ds_read_b128 v[182:185], v133 offset:8192
	ds_read_b128 v[186:189], v133 offset:16384
	ds_read_b128 v[190:193], v133 offset:24576
	ds_read_b128 v[194:197], v133 offset:32768
	ds_read_b128 v[198:201], v133 offset:40960
	ds_read_b128 v[202:205], v133 offset:49152
	ds_read_b128 v[206:209], v133 offset:57344
	s_waitcnt lgkmcnt(7)
	v_mfma_f32_16x16x32_f16 v[96:99], v[22:25], v[18:21], v[96:99]
	s_waitcnt lgkmcnt(6)
	v_mfma_f32_16x16x32_f16 v[100:103], v[22:25], v[182:185], v[100:103]
	s_waitcnt lgkmcnt(5)
	v_mfma_f32_16x16x32_f16 v[104:107], v[22:25], v[186:189], v[104:107]
	s_waitcnt lgkmcnt(4)
	v_mfma_f32_16x16x32_f16 v[108:111], v[22:25], v[190:193], v[108:111]
	s_waitcnt lgkmcnt(3)
	v_mfma_f32_16x16x32_f16 v[112:115], v[22:25], v[194:197], v[112:115]
	s_waitcnt lgkmcnt(2)
	v_mfma_f32_16x16x32_f16 v[120:123], v[22:25], v[198:201], v[120:123]
	s_waitcnt lgkmcnt(1)
	v_mfma_f32_16x16x32_f16 v[124:127], v[22:25], v[202:205], v[124:127]
	s_waitcnt lgkmcnt(0)
	v_mfma_f32_16x16x32_f16 v[10:13], v[22:25], v[206:209], v[10:13]
	s_waitcnt vmcnt(13)
	v_mfma_f32_16x16x32_f16 v[22:25], v[30:33], v[18:21], v[26:29]
	v_mfma_f32_16x16x32_f16 v[26:29], v[30:33], v[182:185], v[128:131]
	v_mfma_f32_16x16x32_f16 v[128:131], v[30:33], v[186:189], v[146:149]
	v_mfma_f32_16x16x32_f16 v[146:149], v[30:33], v[190:193], v[150:153]
	v_mfma_f32_16x16x32_f16 v[150:153], v[30:33], v[194:197], v[154:157]
	v_mfma_f32_16x16x32_f16 v[154:157], v[30:33], v[198:201], v[158:161]
	v_mfma_f32_16x16x32_f16 v[158:161], v[30:33], v[202:205], v[162:165]
	v_mfma_f32_16x16x32_f16 v[2:5], v[30:33], v[206:209], v[2:5]
	s_waitcnt vmcnt(12)
	v_mfma_f32_16x16x32_f16 v[14:17], v[34:37], v[18:21], v[14:17]
	v_mfma_f32_16x16x32_f16 v[18:21], v[34:37], v[182:185], v[62:65]
	v_mfma_f32_16x16x32_f16 v[30:33], v[34:37], v[186:189], v[66:69]
	v_mfma_f32_16x16x32_f16 v[62:65], v[34:37], v[190:193], v[70:73]
	v_mfma_f32_16x16x32_f16 v[66:69], v[34:37], v[194:197], v[74:77]
	v_mfma_f32_16x16x32_f16 v[70:73], v[34:37], v[198:201], v[78:81]
	v_mfma_f32_16x16x32_f16 v[74:77], v[34:37], v[202:205], v[84:87]
	v_mfma_f32_16x16x32_f16 v[6:9], v[34:37], v[206:209], v[6:9]
	s_nop 0
	global_load_dwordx4 v[78:81], v[116:117], off offset:1024
	global_load_dwordx4 v[162:165], v[116:117], off offset:2048
	global_load_dwordx4 v[182:185], v[116:117], off offset:3072
	v_bitop3_b32 v34, v140, v145, 12 bitop3:0x36
	v_lshl_or_b32 v135, v34, 4, v220
	ds_read_b128 v[34:37], v135
	ds_read_b128 v[84:87], v135 offset:8192
	ds_read_b128 v[186:189], v135 offset:16384
	ds_read_b128 v[190:193], v135 offset:24576
	ds_read_b128 v[194:197], v135 offset:32768
	ds_read_b128 v[198:201], v135 offset:40960
	ds_read_b128 v[202:205], v135 offset:49152
	ds_read_b128 v[206:209], v135 offset:57344
	s_waitcnt vmcnt(14) lgkmcnt(7)
	v_mfma_f32_16x16x32_f16 v[96:99], v[38:41], v[34:37], v[96:99]
	s_waitcnt lgkmcnt(6)
	v_mfma_f32_16x16x32_f16 v[100:103], v[38:41], v[84:87], v[100:103]
	s_waitcnt lgkmcnt(5)
	v_mfma_f32_16x16x32_f16 v[104:107], v[38:41], v[186:189], v[104:107]
	s_waitcnt lgkmcnt(4)
	v_mfma_f32_16x16x32_f16 v[108:111], v[38:41], v[190:193], v[108:111]
	s_waitcnt lgkmcnt(3)
	v_mfma_f32_16x16x32_f16 v[112:115], v[38:41], v[194:197], v[112:115]
	s_waitcnt lgkmcnt(2)
	v_mfma_f32_16x16x32_f16 v[120:123], v[38:41], v[198:201], v[120:123]
	s_waitcnt lgkmcnt(1)
	v_mfma_f32_16x16x32_f16 v[124:127], v[38:41], v[202:205], v[124:127]
	s_waitcnt lgkmcnt(0)
	v_mfma_f32_16x16x32_f16 v[210:213], v[38:41], v[206:209], v[10:13]
	s_waitcnt vmcnt(13)
	v_mfma_f32_16x16x32_f16 v[22:25], v[42:45], v[34:37], v[22:25]
	v_mfma_f32_16x16x32_f16 v[214:217], v[42:45], v[84:87], v[26:29]
	v_mfma_f32_16x16x32_f16 v[128:131], v[42:45], v[186:189], v[128:131]
	v_mfma_f32_16x16x32_f16 v[146:149], v[42:45], v[190:193], v[146:149]
	v_mfma_f32_16x16x32_f16 v[150:153], v[42:45], v[194:197], v[150:153]
	v_mfma_f32_16x16x32_f16 v[154:157], v[42:45], v[198:201], v[154:157]
	v_mfma_f32_16x16x32_f16 v[158:161], v[42:45], v[202:205], v[158:161]
	v_mfma_f32_16x16x32_f16 v[2:5], v[42:45], v[206:209], v[2:5]
	s_waitcnt vmcnt(12)
	v_mfma_f32_16x16x32_f16 v[14:17], v[46:49], v[34:37], v[14:17]
	v_mfma_f32_16x16x32_f16 v[18:21], v[46:49], v[84:87], v[18:21]
	v_mfma_f32_16x16x32_f16 v[30:33], v[46:49], v[186:189], v[30:33]
	v_mfma_f32_16x16x32_f16 v[34:37], v[46:49], v[190:193], v[62:65]
	v_mfma_f32_16x16x32_f16 v[42:45], v[46:49], v[194:197], v[66:69]
	v_mfma_f32_16x16x32_f16 v[62:65], v[46:49], v[198:201], v[70:73]
	v_mfma_f32_16x16x32_f16 v[66:69], v[46:49], v[202:205], v[74:77]
	v_mfma_f32_16x16x32_f16 v[6:9], v[46:49], v[206:209], v[6:9]
	s_mov_b32 s8, 0x30000
	v_add_co_u32_e32 v116, vcc, s8, v118
	s_mov_b32 s8, 0x31000
	s_nop 0
	v_addc_co_u32_e32 v117, vcc, 0, v119, vcc
	v_add_co_u32_e32 v218, vcc, s8, v118
	v_bitop3_b32 v46, v140, v145, 16 bitop3:0x36
	s_nop 0
	v_addc_co_u32_e32 v219, vcc, 0, v119, vcc
	global_load_dwordx4 v[38:41], v[218:219], off offset:-4096
	global_load_dwordx4 v[26:29], v[116:117], off offset:1024
	global_load_dwordx4 v[10:13], v[116:117], off offset:2048
	v_lshl_or_b32 v136, v46, 4, v220
	ds_read_b128 v[46:49], v136
	ds_read_b128 v[70:73], v136 offset:8192
	ds_read_b128 v[74:77], v136 offset:16384
	ds_read_b128 v[84:87], v136 offset:24576
	ds_read_b128 v[186:189], v136 offset:32768
	ds_read_b128 v[190:193], v136 offset:40960
	ds_read_b128 v[194:197], v136 offset:49152
	ds_read_b128 v[198:201], v136 offset:57344
	s_waitcnt vmcnt(14) lgkmcnt(7)
	v_mfma_f32_16x16x32_f16 v[96:99], v[50:53], v[46:49], v[96:99]
	s_waitcnt lgkmcnt(6)
	v_mfma_f32_16x16x32_f16 v[100:103], v[50:53], v[70:73], v[100:103]
	s_waitcnt lgkmcnt(5)
	v_mfma_f32_16x16x32_f16 v[104:107], v[50:53], v[74:77], v[104:107]
	s_waitcnt lgkmcnt(4)
	v_mfma_f32_16x16x32_f16 v[108:111], v[50:53], v[84:87], v[108:111]
	s_waitcnt lgkmcnt(3)
	v_mfma_f32_16x16x32_f16 v[112:115], v[50:53], v[186:189], v[112:115]
	s_waitcnt lgkmcnt(2)
	v_mfma_f32_16x16x32_f16 v[120:123], v[50:53], v[190:193], v[120:123]
	s_waitcnt lgkmcnt(1)
	v_mfma_f32_16x16x32_f16 v[124:127], v[50:53], v[194:197], v[124:127]
	s_waitcnt lgkmcnt(0)
	v_mfma_f32_16x16x32_f16 v[50:53], v[50:53], v[198:201], v[210:213]
	s_waitcnt vmcnt(13)
	v_mfma_f32_16x16x32_f16 v[202:205], v[54:57], v[46:49], v[22:25]
	v_mfma_f32_16x16x32_f16 v[206:209], v[54:57], v[70:73], v[214:217]
	v_mfma_f32_16x16x32_f16 v[128:131], v[54:57], v[74:77], v[128:131]
	v_mfma_f32_16x16x32_f16 v[146:149], v[54:57], v[84:87], v[146:149]
	v_mfma_f32_16x16x32_f16 v[150:153], v[54:57], v[186:189], v[150:153]
	v_mfma_f32_16x16x32_f16 v[154:157], v[54:57], v[190:193], v[154:157]
	v_mfma_f32_16x16x32_f16 v[158:161], v[54:57], v[194:197], v[158:161]
	v_mfma_f32_16x16x32_f16 v[54:57], v[54:57], v[198:201], v[2:5]
	s_waitcnt vmcnt(12)
	v_mfma_f32_16x16x32_f16 v[14:17], v[58:61], v[46:49], v[14:17]
	v_mfma_f32_16x16x32_f16 v[18:21], v[58:61], v[70:73], v[18:21]
	v_mfma_f32_16x16x32_f16 v[30:33], v[58:61], v[74:77], v[30:33]
	v_mfma_f32_16x16x32_f16 v[34:37], v[58:61], v[84:87], v[34:37]
	v_mfma_f32_16x16x32_f16 v[42:45], v[58:61], v[186:189], v[42:45]
	v_mfma_f32_16x16x32_f16 v[46:49], v[58:61], v[190:193], v[62:65]
	v_mfma_f32_16x16x32_f16 v[62:65], v[58:61], v[194:197], v[66:69]
	v_mfma_f32_16x16x32_f16 v[58:61], v[58:61], v[198:201], v[6:9]
	global_load_dwordx4 v[22:25], v[116:117], off offset:3072
	s_nop 1
	global_load_dwordx4 v[6:9], v[218:219], off
	global_load_dwordx4 v[2:5], v[218:219], off offset:1024
	v_bitop3_b32 v66, v140, v145, 20 bitop3:0x36
	v_lshl_or_b32 v137, v66, 4, v220
	ds_read_b128 v[66:69], v137
	ds_read_b128 v[70:73], v137 offset:8192
	ds_read_b128 v[74:77], v137 offset:16384
	ds_read_b128 v[84:87], v137 offset:24576
	ds_read_b128 v[186:189], v137 offset:32768
	ds_read_b128 v[190:193], v137 offset:40960
	ds_read_b128 v[194:197], v137 offset:49152
	ds_read_b128 v[198:201], v137 offset:57344
	s_waitcnt vmcnt(14) lgkmcnt(7)
	v_mfma_f32_16x16x32_f16 v[96:99], v[92:95], v[66:69], v[96:99]
	s_waitcnt lgkmcnt(6)
	v_mfma_f32_16x16x32_f16 v[100:103], v[92:95], v[70:73], v[100:103]
	s_waitcnt lgkmcnt(5)
	v_mfma_f32_16x16x32_f16 v[104:107], v[92:95], v[74:77], v[104:107]
	s_waitcnt lgkmcnt(4)
	v_mfma_f32_16x16x32_f16 v[108:111], v[92:95], v[84:87], v[108:111]
	s_waitcnt lgkmcnt(3)
	v_mfma_f32_16x16x32_f16 v[112:115], v[92:95], v[186:189], v[112:115]
	s_waitcnt lgkmcnt(2)
	v_mfma_f32_16x16x32_f16 v[210:213], v[92:95], v[190:193], v[120:123]
	s_waitcnt lgkmcnt(1)
	v_mfma_f32_16x16x32_f16 v[124:127], v[92:95], v[194:197], v[124:127]
	s_waitcnt lgkmcnt(0)
	v_mfma_f32_16x16x32_f16 v[50:53], v[92:95], v[198:201], v[50:53]
	s_waitcnt vmcnt(13)
	v_mfma_f32_16x16x32_f16 v[92:95], v[170:173], v[66:69], v[202:205]
	v_mfma_f32_16x16x32_f16 v[202:205], v[170:173], v[70:73], v[206:209]
	v_mfma_f32_16x16x32_f16 v[128:131], v[170:173], v[74:77], v[128:131]
	v_mfma_f32_16x16x32_f16 v[146:149], v[170:173], v[84:87], v[146:149]
	v_mfma_f32_16x16x32_f16 v[150:153], v[170:173], v[186:189], v[150:153]
	v_mfma_f32_16x16x32_f16 v[154:157], v[170:173], v[190:193], v[154:157]
	v_mfma_f32_16x16x32_f16 v[158:161], v[170:173], v[194:197], v[158:161]
	v_mfma_f32_16x16x32_f16 v[54:57], v[170:173], v[198:201], v[54:57]
	s_waitcnt vmcnt(12)
	v_mfma_f32_16x16x32_f16 v[66:69], v[174:177], v[66:69], v[14:17]
	v_mfma_f32_16x16x32_f16 v[70:73], v[174:177], v[70:73], v[18:21]
	v_mfma_f32_16x16x32_f16 v[74:77], v[174:177], v[74:77], v[30:33]
	v_mfma_f32_16x16x32_f16 v[34:37], v[174:177], v[84:87], v[34:37]
	v_mfma_f32_16x16x32_f16 v[42:45], v[174:177], v[186:189], v[42:45]
	v_mfma_f32_16x16x32_f16 v[46:49], v[174:177], v[190:193], v[46:49]
	v_mfma_f32_16x16x32_f16 v[62:65], v[174:177], v[194:197], v[62:65]
	v_mfma_f32_16x16x32_f16 v[58:61], v[174:177], v[198:201], v[58:61]
	s_mov_b32 s8, 0x33000
	v_add_co_u32_e32 v122, vcc, s8, v118
	global_load_dwordx4 v[30:33], v[218:219], off offset:2048
	global_load_dwordx4 v[14:17], v[218:219], off offset:3072
	v_addc_co_u32_e32 v123, vcc, 0, v119, vcc
	global_load_dwordx4 v[18:21], v[122:123], off offset:-4096
	v_bitop3_b32 v84, v140, v145, 24 bitop3:0x36
	v_lshl_or_b32 v138, v84, 4, v220
	ds_read_b128 v[84:87], v138
	ds_read_b128 v[170:173], v138 offset:8192
	ds_read_b128 v[174:177], v138 offset:16384
	ds_read_b128 v[186:189], v138 offset:24576
	ds_read_b128 v[190:193], v138 offset:32768
	ds_read_b128 v[194:197], v138 offset:40960
	ds_read_b128 v[198:201], v138 offset:49152
	ds_read_b128 v[206:209], v138 offset:57344
	s_mov_b32 s8, 0x32000
	v_add_co_u32_e32 v116, vcc, s8, v118
	s_nop 1
	v_addc_co_u32_e32 v117, vcc, 0, v119, vcc
	s_waitcnt vmcnt(14) lgkmcnt(7)
	v_mfma_f32_16x16x32_f16 v[96:99], v[88:91], v[84:87], v[96:99]
	s_waitcnt lgkmcnt(6)
	v_mfma_f32_16x16x32_f16 v[100:103], v[88:91], v[170:173], v[100:103]
	s_waitcnt lgkmcnt(5)
	v_mfma_f32_16x16x32_f16 v[104:107], v[88:91], v[174:177], v[104:107]
	s_waitcnt lgkmcnt(4)
	v_mfma_f32_16x16x32_f16 v[108:111], v[88:91], v[186:189], v[108:111]
	s_waitcnt lgkmcnt(3)
	v_mfma_f32_16x16x32_f16 v[112:115], v[88:91], v[190:193], v[112:115]
	s_waitcnt lgkmcnt(2)
	v_mfma_f32_16x16x32_f16 v[210:213], v[88:91], v[194:197], v[210:213]
	s_waitcnt lgkmcnt(1)
	v_mfma_f32_16x16x32_f16 v[124:127], v[88:91], v[198:201], v[124:127]
	s_waitcnt lgkmcnt(0)
	v_mfma_f32_16x16x32_f16 v[50:53], v[88:91], v[206:209], v[50:53]
	s_waitcnt vmcnt(13)
	v_mfma_f32_16x16x32_f16 v[90:93], v[166:169], v[84:87], v[92:95]
	v_mfma_f32_16x16x32_f16 v[202:205], v[166:169], v[170:173], v[202:205]
	v_mfma_f32_16x16x32_f16 v[128:131], v[166:169], v[174:177], v[128:131]
	v_mfma_f32_16x16x32_f16 v[146:149], v[166:169], v[186:189], v[146:149]
	v_mfma_f32_16x16x32_f16 v[150:153], v[166:169], v[190:193], v[150:153]
	v_mfma_f32_16x16x32_f16 v[154:157], v[166:169], v[194:197], v[154:157]
	v_mfma_f32_16x16x32_f16 v[158:161], v[166:169], v[198:201], v[158:161]
	v_mfma_f32_16x16x32_f16 v[54:57], v[166:169], v[206:209], v[54:57]
	s_waitcnt vmcnt(12)
	v_mfma_f32_16x16x32_f16 v[166:169], v[178:181], v[84:87], v[66:69]
	v_mfma_f32_16x16x32_f16 v[170:173], v[178:181], v[170:173], v[70:73]
	v_mfma_f32_16x16x32_f16 v[174:177], v[178:181], v[174:177], v[74:77]
	v_mfma_f32_16x16x32_f16 v[186:189], v[178:181], v[186:189], v[34:37]
	v_mfma_f32_16x16x32_f16 v[190:193], v[178:181], v[190:193], v[42:45]
	v_mfma_f32_16x16x32_f16 v[194:197], v[178:181], v[194:197], v[46:49]
	v_mfma_f32_16x16x32_f16 v[198:201], v[178:181], v[198:201], v[62:65]
	v_mfma_f32_16x16x32_f16 v[178:181], v[178:181], v[206:209], v[58:61]
	s_nop 0
	global_load_dwordx4 v[46:49], v[116:117], off offset:1024
	global_load_dwordx4 v[42:45], v[116:117], off offset:2048
	global_load_dwordx4 v[34:37], v[116:117], off offset:3072
	v_bitop3_b32 v58, v140, v145, 28 bitop3:0x36
	v_lshl_or_b32 v140, v58, 4, v220
	ds_read_b128 v[58:61], v140
	ds_read_b128 v[62:65], v140 offset:8192
	ds_read_b128 v[206:209], v140 offset:16384
	ds_read_b128 v[214:217], v140 offset:24576
	ds_read_b128 v[218:221], v140 offset:32768
	ds_read_b128 v[222:225], v140 offset:40960
	ds_read_b128 v[226:229], v140 offset:49152
	ds_read_b128 v[230:233], v140 offset:57344
	s_waitcnt vmcnt(14) lgkmcnt(7)
	v_mfma_f32_16x16x32_f16 v[234:237], v[78:81], v[58:61], v[96:99]
	s_waitcnt lgkmcnt(6)
	v_mfma_f32_16x16x32_f16 v[238:241], v[78:81], v[62:65], v[100:103]
	s_waitcnt lgkmcnt(5)
	v_mfma_f32_16x16x32_f16 v[242:245], v[78:81], v[206:209], v[104:107]
	s_waitcnt lgkmcnt(4)
	v_mfma_f32_16x16x32_f16 v[246:249], v[78:81], v[214:217], v[108:111]
	s_waitcnt lgkmcnt(3)
	v_mfma_f32_16x16x32_f16 v[106:109], v[78:81], v[218:221], v[112:115]
	s_waitcnt lgkmcnt(2)
	v_mfma_f32_16x16x32_f16 v[102:105], v[78:81], v[222:225], v[210:213]
	s_waitcnt lgkmcnt(1)
	v_mfma_f32_16x16x32_f16 v[94:97], v[78:81], v[226:229], v[124:127]
	s_waitcnt lgkmcnt(0)
	v_mfma_f32_16x16x32_f16 v[86:89], v[78:81], v[230:233], v[50:53]
	s_waitcnt vmcnt(13)
	v_mfma_f32_16x16x32_f16 v[124:127], v[162:165], v[58:61], v[90:93]
	v_mfma_f32_16x16x32_f16 v[202:205], v[162:165], v[62:65], v[202:205]
	v_mfma_f32_16x16x32_f16 v[210:213], v[162:165], v[206:209], v[128:131]
	v_mfma_f32_16x16x32_f16 v[146:149], v[162:165], v[214:217], v[146:149]
	v_mfma_f32_16x16x32_f16 v[78:81], v[162:165], v[218:221], v[150:153]
	v_mfma_f32_16x16x32_f16 v[74:77], v[162:165], v[222:225], v[154:157]
	v_mfma_f32_16x16x32_f16 v[70:73], v[162:165], v[226:229], v[158:161]
	v_mfma_f32_16x16x32_f16 v[66:69], v[162:165], v[230:233], v[54:57]
	s_waitcnt vmcnt(12)
	v_mfma_f32_16x16x32_f16 v[150:153], v[182:185], v[58:61], v[166:169]
	v_mfma_f32_16x16x32_f16 v[154:157], v[182:185], v[62:65], v[170:173]
	v_mfma_f32_16x16x32_f16 v[114:117], v[182:185], v[206:209], v[174:177]
	v_mfma_f32_16x16x32_f16 v[110:113], v[182:185], v[214:217], v[186:189]
	v_mfma_f32_16x16x32_f16 v[62:65], v[182:185], v[218:221], v[190:193]
	v_mfma_f32_16x16x32_f16 v[58:61], v[182:185], v[222:225], v[194:197]
	v_mfma_f32_16x16x32_f16 v[54:57], v[182:185], v[226:229], v[198:201]
	v_mfma_f32_16x16x32_f16 v[50:53], v[182:185], v[230:233], v[178:181]
	v_lshl_add_u64 v[120:121], v[82:83], 2, s[4:5]
	global_load_dwordx4 v[98:101], v[120:121], off
	global_load_dwordx4 v[90:93], v[120:121], off offset:64
	global_load_dwordx4 v[82:85], v[120:121], off offset:128
	s_movk_i32 s5, 0x310
	v_mad_u32_u24 v130, v145, s5, v250
	v_mov_b32_e32 v158, v239
	v_mov_b32_e32 v159, v240
	v_mov_b32_e32 v160, v243
	v_mov_b32_e32 v161, v244
	v_mov_b32_e32 v162, v247
	v_mov_b32_e32 v163, v248
	v_mov_b32_e32 v164, v203
	v_mov_b32_e32 v165, v204
	v_mov_b32_e32 v169, v148
	v_mov_b32_e32 v166, v211
	v_mov_b32_e32 v167, v212
	v_mov_b32_e32 v168, v147
	s_barrier
	v_add_u32_e32 v132, 0x3000, v130
	v_add_u32_e32 v131, 0x6000, v130
	s_mov_b32 s4, 0xfffffd0
	v_mul_i32_i24_e32 v176, s4, v143
	s_waitcnt vmcnt(2)
	v_pk_add_f32 v[170:171], v[234:235], v[98:99]
	v_pk_add_f32 v[172:173], v[236:237], v[100:101]
	v_add_f32_e32 v145, v238, v98
	v_pk_mov_b32 v[128:129], v[98:99], v[100:101] op_sel:[1,0]
	v_add_f32_e32 v99, v241, v101
	s_waitcnt vmcnt(1)
	v_pk_add_f32 v[124:125], v[124:125], v[90:91]
	v_pk_add_f32 v[174:175], v[126:127], v[92:93]
	v_add_f32_e32 v180, v202, v90
	v_pk_mov_b32 v[126:127], v[90:91], v[92:93] op_sel:[1,0]
	v_add_f32_e32 v91, v205, v93
	v_add_f32_e32 v100, v242, v98
	v_add_f32_e32 v177, v245, v101
	v_add_f32_e32 v92, v210, v90
	v_add_f32_e32 v181, v213, v93
	v_add_f32_e32 v183, v149, v93
	v_cvt_pk_f16_f32 v149, v172, v173
	v_cvt_f16_f32_e32 v145, v145
	v_cvt_f16_f32_e32 v99, v99
	v_cvt_f16_f32_e32 v173, v180
	v_cvt_f16_f32_e32 v91, v91
	v_cvt_pk_f16_f32 v148, v170, v171
	v_cvt_f16_f32_e32 v100, v100
	v_cvt_f16_f32_e32 v170, v177
	v_cvt_pk_f16_f32 v124, v124, v125
	v_cvt_pk_f16_f32 v125, v174, v175
	v_cvt_f16_f32_e32 v92, v92
	v_cvt_f16_f32_e32 v174, v181
	v_add_f32_e32 v182, v146, v90
	s_waitcnt vmcnt(0)
	v_pk_add_f32 v[146:147], v[150:151], v[82:83]
	v_pk_add_f32 v[150:151], v[158:159], v[128:129]
	v_pk_add_f32 v[158:159], v[160:161], v[128:129]
	v_pk_add_f32 v[160:161], v[162:163], v[128:129]
	v_pk_add_f32 v[162:163], v[164:165], v[126:127]
	v_pk_add_f32 v[164:165], v[166:167], v[126:127]
	v_cvt_pk_f16_f32 v146, v146, v147
	v_cvt_pk_f16_f32 v147, v150, v151
	v_cvt_pk_f16_f32 v150, v158, v159
	v_cvt_pk_f16_f32 v159, v162, v163
	v_cvt_pk_f16_f32 v151, v160, v161
	v_cvt_pk_f16_f32 v161, v164, v165
	ds_write2_b64 v130, v[148:149], v[124:125] offset1:4
	v_pack_b32_f16 v124, v145, v147
	v_alignbit_b32 v125, v99, v147, 16
	v_pack_b32_f16 v158, v173, v159
	v_alignbit_b32 v159, v91, v159, 16
	v_pack_b32_f16 v148, v100, v150
	v_alignbit_b32 v149, v170, v150, 16
	v_pack_b32_f16 v160, v92, v161
	v_alignbit_b32 v161, v174, v161, 16
	ds_write2_b64 v132, v[124:125], v[158:159] offset0:32 offset1:36
	ds_write2_b64 v131, v[148:149], v[160:161] offset0:64 offset1:68
	v_pk_add_f32 v[124:125], v[152:153], v[84:85]
	v_add_f32_e32 v92, v154, v82
	v_cvt_pk_f16_f32 v147, v124, v125
	v_pk_mov_b32 v[124:125], v[82:83], v[84:85] op_sel:[1,0]
	v_add_f32_e32 v83, v157, v85
	v_cvt_f16_f32_e32 v92, v92
	v_cvt_f16_f32_e32 v83, v83
	ds_write_b64 v130, v[146:147] offset:64
	v_mov_b32_e32 v146, v155
	v_mov_b32_e32 v147, v156
	v_pk_add_f32 v[146:147], v[146:147], v[124:125]
	v_add_f32_e32 v178, v246, v98
	v_cvt_pk_f16_f32 v84, v146, v147
	v_pack_b32_f16 v146, v92, v84
	v_alignbit_b32 v147, v83, v84, 16
	v_add_f32_e32 v83, v114, v82
	v_add_f32_e32 v84, v117, v85
	v_cvt_f16_f32_e32 v83, v83
	v_cvt_f16_f32_e32 v84, v84
	v_mov_b32_e32 v114, v115
	v_mov_b32_e32 v115, v116
	v_pk_add_f32 v[114:115], v[114:115], v[124:125]
	v_add_f32_e32 v179, v249, v101
	v_cvt_pk_f16_f32 v92, v114, v115
	v_pack_b32_f16 v114, v83, v92
	v_alignbit_b32 v115, v84, v92, 16
	v_add_f32_e32 v83, v110, v82
	v_add_f32_e32 v84, v113, v85
	v_cvt_f16_f32_e32 v83, v83
	v_cvt_f16_f32_e32 v84, v84
	v_mov_b32_e32 v110, v111
	v_mov_b32_e32 v111, v112
	v_cvt_f16_f32_e32 v171, v178
	v_cvt_f16_f32_e32 v172, v179
	v_cvt_f16_f32_e32 v175, v182
	v_pk_add_f32 v[166:167], v[168:169], v[126:127]
	v_cvt_f16_f32_e32 v168, v183
	v_pk_add_f32 v[110:111], v[110:111], v[124:125]
	v_cvt_pk_f16_f32 v163, v166, v167
	v_cvt_pk_f16_f32 v92, v110, v111
	v_pack_b32_f16 v110, v83, v92
	v_alignbit_b32 v111, v84, v92, 16
	v_or_b32_e32 v83, s16, v143
	ds_write_b64 v130, v[110:111] offset:37696
	v_add_lshl_u32 v111, v176, v0, 4
	v_mul_u32_u24_e32 v112, s6, v83
	v_mul_u32_u24_e32 v83, 0x310, v143
	v_mul_u32_u24_e32 v84, 0x556, v141
	v_pack_b32_f16 v150, v171, v151
	v_alignbit_b32 v151, v172, v151, 16
	v_pack_b32_f16 v162, v175, v163
	v_alignbit_b32 v163, v168, v163, 16
	v_add_u32_e32 v91, 0x9000, v130
	v_add3_u32 v83, v111, v83, s14
	v_lshrrev_b32_e32 v154, 16, v84
	ds_write2_b64 v91, v[150:151], v[162:163] offset0:96 offset1:100
	ds_write_b64 v130, v[146:147] offset:12608
	ds_write_b64 v130, v[114:115] offset:25152
	s_waitcnt lgkmcnt(0)
	s_barrier
	ds_read_b128 v[114:117], v83
	v_mul_i32_i24_e32 v84, s4, v154
	v_add_lshl_u32 v113, v84, v141, 4
	v_mul_u32_u24_e32 v84, 0x310, v154
	v_add3_u32 v84, v113, v84, s14
	ds_read_b128 v[146:149], v84
	v_add_u32_e32 v92, v111, v112
	s_waitcnt lgkmcnt(1)
	buffer_store_dwordx4 v[114:117], v92, s[0:3], 0 offen sc1
	v_or_b32_e32 v92, s16, v154
	s_nop 0
	v_mul_u32_u24_e32 v114, s6, v92
	v_add_u32_e32 v92, v113, v114
	s_waitcnt lgkmcnt(0)
	buffer_store_dwordx4 v[146:149], v92, s[0:3], 0 offen sc1
	v_or_b32_e32 v92, 0x400, v0
	v_mul_u32_u24_e32 v99, 0x556, v92
	v_lshrrev_b32_e32 v155, 16, v99
	v_mul_i32_i24_e32 v99, s4, v155
	v_add_lshl_u32 v115, v99, v92, 4
	v_mul_u32_u24_e32 v92, 0x310, v155
	v_mul_u32_u24_e32 v99, 0x556, v142
	v_add3_u32 v92, v115, v92, s14
	v_lshrrev_b32_e32 v156, 16, v99
	ds_read_b128 v[146:149], v92
	v_mul_i32_i24_e32 v99, s4, v156
	v_add_lshl_u32 v117, v99, v142, 4
	v_mul_u32_u24_e32 v99, 0x310, v156
	v_or_b32_e32 v100, s16, v155
	v_add3_u32 v99, v117, v99, s14
	v_mul_u32_u24_e32 v116, s6, v100
	ds_read_b128 v[150:153], v99
	v_add_u32_e32 v100, v115, v116
	s_waitcnt lgkmcnt(1)
	buffer_store_dwordx4 v[146:149], v100, s[0:3], 0 offen sc1
	v_or_b32_e32 v100, s16, v156
	v_mul_u32_u24_e32 v142, s6, v100
	v_add_u32_e32 v100, v117, v142
	v_or_b32_e32 v0, 0x800, v0
	s_waitcnt lgkmcnt(0)
	buffer_store_dwordx4 v[150:153], v100, s[0:3], 0 offen sc1
	v_mul_u32_u24_e32 v100, 0xaab, v0
	v_lshrrev_b32_e32 v157, 17, v100
	v_mul_i32_i24_e32 v100, s4, v157
	v_or_b32_e32 v110, s16, v157
	v_add_lshl_u32 v143, v100, v0, 4
	v_mul_u32_u24_e32 v141, s6, v110
	v_mul_u32_u24_e32 v100, 0x310, v157
	v_mul_u32_u24_e32 v110, 0xaab, v144
	v_add3_u32 v100, v100, v143, s14
	v_lshrrev_b32_e32 v158, 17, v110
	ds_read_b128 v[146:149], v100
	v_mul_i32_i24_e32 v110, s4, v158
	v_add_lshl_u32 v144, v110, v144, 4
	v_mul_u32_u24_e32 v110, 0x310, v158
	v_add3_u32 v110, v110, v144, s14
	ds_read_b128 v[150:153], v110
	v_add_u32_e32 v0, v143, v141
	s_waitcnt lgkmcnt(1)
	buffer_store_dwordx4 v[146:149], v0, s[0:3], 0 offen sc1
	v_or_b32_e32 v0, s16, v158
	v_mul_u32_u24_e32 v145, s6, v0
	v_add_u32_e32 v0, v144, v145
	s_waitcnt lgkmcnt(0)
	buffer_store_dwordx4 v[150:153], v0, s[0:3], 0 offen sc1
	v_add_f32_e32 v0, v106, v98
	v_cvt_f16_f32_e32 v0, v0
	v_mov_b32_e32 v106, v107
	v_mov_b32_e32 v107, v108
	v_pk_add_f32 v[106:107], v[106:107], v[128:129]
	v_add_f32_e32 v108, v109, v101
	v_cvt_pk_f16_f32 v107, v106, v107
	v_pack_b32_f16 v106, v0, v107
	v_add_f32_e32 v0, v102, v98
	v_cvt_f16_f32_e32 v0, v0
	v_mov_b32_e32 v102, v103
	v_mov_b32_e32 v103, v104
	v_pk_add_f32 v[102:103], v[102:103], v[128:129]
	v_add_f32_e32 v104, v105, v101
	v_cvt_pk_f16_f32 v103, v102, v103
	v_pack_b32_f16 v102, v0, v103
	v_add_f32_e32 v0, v94, v98
	v_cvt_f16_f32_e32 v0, v0
	v_mov_b32_e32 v94, v95
	v_mov_b32_e32 v95, v96
	v_pk_add_f32 v[94:95], v[94:95], v[128:129]
	v_add_f32_e32 v96, v97, v101
	v_cvt_pk_f16_f32 v95, v94, v95
	v_pack_b32_f16 v94, v0, v95
	v_add_f32_e32 v0, v86, v98
	v_cvt_f16_f32_e32 v0, v0
	v_mov_b32_e32 v86, v87
	v_mov_b32_e32 v87, v88
	v_pk_add_f32 v[86:87], v[86:87], v[128:129]
	v_add_f32_e32 v88, v89, v101
	v_cvt_pk_f16_f32 v87, v86, v87
	v_pack_b32_f16 v86, v0, v87
	v_add_f32_e32 v0, v78, v90
	v_cvt_f16_f32_e32 v0, v0
	v_mov_b32_e32 v78, v79
	v_mov_b32_e32 v79, v80
	v_pk_add_f32 v[78:79], v[78:79], v[126:127]
	v_add_f32_e32 v80, v81, v93
	v_cvt_pk_f16_f32 v79, v78, v79
	v_pack_b32_f16 v78, v0, v79
	v_add_f32_e32 v0, v74, v90
	v_cvt_f16_f32_e32 v0, v0
	v_mov_b32_e32 v74, v75
	v_mov_b32_e32 v75, v76
	v_pk_add_f32 v[74:75], v[74:75], v[126:127]
	v_add_f32_e32 v76, v77, v93
	v_cvt_pk_f16_f32 v75, v74, v75
	v_pack_b32_f16 v74, v0, v75
	v_add_f32_e32 v0, v70, v90
	v_cvt_f16_f32_e32 v0, v0
	v_mov_b32_e32 v70, v71
	v_mov_b32_e32 v71, v72
	v_pk_add_f32 v[70:71], v[70:71], v[126:127]
	v_add_f32_e32 v72, v73, v93
	v_cvt_pk_f16_f32 v71, v70, v71
	v_pack_b32_f16 v70, v0, v71
	v_add_f32_e32 v0, v66, v90
	v_cvt_f16_f32_e32 v0, v0
	v_mov_b32_e32 v66, v67
	v_mov_b32_e32 v67, v68
	v_pk_add_f32 v[66:67], v[66:67], v[126:127]
	v_add_f32_e32 v68, v69, v93
	v_cvt_pk_f16_f32 v67, v66, v67
	v_pack_b32_f16 v66, v0, v67
	v_add_f32_e32 v0, v62, v82
	v_cvt_f16_f32_e32 v0, v0
	v_mov_b32_e32 v62, v63
	v_mov_b32_e32 v63, v64
	v_pk_add_f32 v[62:63], v[62:63], v[124:125]
	v_add_f32_e32 v64, v65, v85
	v_cvt_pk_f16_f32 v63, v62, v63
	v_pack_b32_f16 v62, v0, v63
	v_add_f32_e32 v0, v58, v82
	v_cvt_f16_f32_e32 v0, v0
	v_mov_b32_e32 v58, v59
	v_mov_b32_e32 v59, v60
	v_pk_add_f32 v[58:59], v[58:59], v[124:125]
	v_add_f32_e32 v60, v61, v85
	v_cvt_pk_f16_f32 v59, v58, v59
	v_pack_b32_f16 v58, v0, v59
	v_add_f32_e32 v0, v54, v82
	v_cvt_f16_f32_e32 v0, v0
	v_mov_b32_e32 v54, v55
	v_mov_b32_e32 v55, v56
	v_pk_add_f32 v[54:55], v[54:55], v[124:125]
	v_add_f32_e32 v56, v57, v85
	v_cvt_pk_f16_f32 v55, v54, v55
	v_pack_b32_f16 v54, v0, v55
	v_add_f32_e32 v0, v50, v82
	v_mov_b32_e32 v50, v51
	v_mov_b32_e32 v51, v52
	v_add_f32_e32 v52, v53, v85
	v_cvt_f16_f32_e32 v108, v108
	v_cvt_f16_f32_e32 v104, v104
	v_cvt_f16_f32_e32 v96, v96
	v_cvt_f16_f32_e32 v88, v88
	v_cvt_f16_f32_e32 v80, v80
	v_cvt_f16_f32_e32 v76, v76
	v_cvt_f16_f32_e32 v72, v72
	v_cvt_f16_f32_e32 v68, v68
	v_cvt_f16_f32_e32 v64, v64
	v_cvt_f16_f32_e32 v60, v60
	v_cvt_f16_f32_e32 v56, v56
	v_cvt_f16_f32_e32 v0, v0
	v_cvt_f16_f32_e32 v52, v52
	v_pk_add_f32 v[50:51], v[50:51], v[124:125]
	v_alignbit_b32 v107, v108, v107, 16
	v_cvt_pk_f16_f32 v51, v50, v51
	v_alignbit_b32 v103, v104, v103, 16
	v_alignbit_b32 v95, v96, v95, 16
	v_alignbit_b32 v87, v88, v87, 16
	v_alignbit_b32 v79, v80, v79, 16
	v_alignbit_b32 v75, v76, v75, 16
	v_alignbit_b32 v71, v72, v71, 16
	v_alignbit_b32 v67, v68, v67, 16
	v_alignbit_b32 v63, v64, v63, 16
	v_alignbit_b32 v59, v60, v59, 16
	v_alignbit_b32 v55, v56, v55, 16
	v_pack_b32_f16 v50, v0, v51
	v_alignbit_b32 v51, v52, v51, 16
	s_barrier
	ds_write2_b64 v130, v[106:107], v[78:79] offset1:4
	ds_write2_b64 v132, v[102:103], v[74:75] offset0:32 offset1:36
	ds_write2_b64 v131, v[94:95], v[70:71] offset0:64 offset1:68
	ds_write2_b64 v91, v[86:87], v[66:67] offset0:96 offset1:100
	ds_write_b64 v130, v[62:63] offset:64
	ds_write_b64 v130, v[58:59] offset:12608
	ds_write_b64 v130, v[54:55] offset:25152
	ds_write_b64 v130, v[50:51] offset:37696
	s_waitcnt lgkmcnt(0)
	s_barrier
	global_load_dwordx4 v[50:53], v[122:123], off
	global_load_dwordx4 v[54:57], v[122:123], off offset:1024
	global_load_dwordx4 v[58:61], v[122:123], off offset:2048
	ds_read_b128 v[62:65], v83
	ds_read_b128 v[70:73], v84
	v_mul_u32_u24_e32 v68, s6, v139
	v_add_u32_e32 v0, v68, v111
	ds_read_b128 v[74:77], v99
	s_waitcnt lgkmcnt(2)
	buffer_store_dwordx4 v[62:65], v0, s[0:3], 0 offen sc1
	v_or_b32_e32 v0, s7, v154
	v_mul_u32_u24_e32 v69, s6, v0
	ds_read_b128 v[62:65], v92
	v_add_u32_e32 v0, v113, v69
	s_waitcnt lgkmcnt(2)
	buffer_store_dwordx4 v[70:73], v0, s[0:3], 0 offen sc1
	v_or_b32_e32 v0, s7, v155
	s_nop 0
	v_mul_u32_u24_e32 v72, s6, v0
	v_add_u32_e32 v0, v115, v72
	s_waitcnt lgkmcnt(0)
	buffer_store_dwordx4 v[62:65], v0, s[0:3], 0 offen sc1
	v_or_b32_e32 v0, s7, v156
	v_mul_u32_u24_e32 v70, s6, v0
	ds_read_b128 v[62:65], v100
	v_add_u32_e32 v0, v117, v70
	buffer_store_dwordx4 v[74:77], v0, s[0:3], 0 offen sc1
	v_or_b32_e32 v0, s7, v157
	v_mul_u32_u24_e32 v71, s6, v0
	v_add_u32_e32 v0, v143, v71
	ds_read_b128 v[74:77], v110
	s_waitcnt lgkmcnt(1)
	buffer_store_dwordx4 v[62:65], v0, s[0:3], 0 offen sc1
	ds_read_b128 v[62:65], v134
	ds_read_b128 v[78:81], v134 offset:8192
	ds_read_b128 v[86:89], v134 offset:16384
	ds_read_b128 v[94:97], v134 offset:24576
	ds_read_b128 v[102:105], v134 offset:32768
	ds_read_b128 v[106:109], v134 offset:40960
	ds_read_b128 v[124:127], v134 offset:49152
	ds_read_b128 v[146:149], v134 offset:57344
	v_or_b32_e32 v0, s7, v158
	v_mul_u32_u24_e32 v73, s6, v0
	v_add_u32_e32 v0, v144, v73
	s_waitcnt lgkmcnt(8)
	buffer_store_dwordx4 v[74:77], v0, s[0:3], 0 offen sc1
	s_waitcnt lgkmcnt(7)
	s_nop 0
	v_mfma_f32_16x16x32_f16 v[74:77], v[38:41], v[62:65], 0
	s_waitcnt lgkmcnt(6)
	v_mfma_f32_16x16x32_f16 v[150:153], v[38:41], v[78:81], 0
	s_waitcnt lgkmcnt(5)
	v_mfma_f32_16x16x32_f16 v[154:157], v[38:41], v[86:89], 0
	s_waitcnt lgkmcnt(4)
	v_mfma_f32_16x16x32_f16 v[158:161], v[38:41], v[94:97], 0
	s_waitcnt lgkmcnt(3)
	v_mfma_f32_16x16x32_f16 v[162:165], v[38:41], v[102:105], 0
	s_waitcnt lgkmcnt(2)
	v_mfma_f32_16x16x32_f16 v[166:169], v[38:41], v[106:109], 0
	s_waitcnt lgkmcnt(1)
	v_mfma_f32_16x16x32_f16 v[170:173], v[38:41], v[124:127], 0
	s_waitcnt lgkmcnt(0)
	v_mfma_f32_16x16x32_f16 v[38:41], v[38:41], v[146:149], 0
	v_mfma_f32_16x16x32_f16 v[174:177], v[26:29], v[62:65], 0
	v_mfma_f32_16x16x32_f16 v[178:181], v[26:29], v[78:81], 0
	v_mfma_f32_16x16x32_f16 v[182:185], v[26:29], v[86:89], 0
	v_mfma_f32_16x16x32_f16 v[186:189], v[26:29], v[94:97], 0
	v_mfma_f32_16x16x32_f16 v[190:193], v[26:29], v[102:105], 0
	v_mfma_f32_16x16x32_f16 v[194:197], v[26:29], v[106:109], 0
	v_mfma_f32_16x16x32_f16 v[198:201], v[26:29], v[124:127], 0
	v_mfma_f32_16x16x32_f16 v[26:29], v[26:29], v[146:149], 0
	v_mfma_f32_16x16x32_f16 v[62:65], v[10:13], v[62:65], 0
	v_mfma_f32_16x16x32_f16 v[78:81], v[10:13], v[78:81], 0
	v_mfma_f32_16x16x32_f16 v[86:89], v[10:13], v[86:89], 0
	v_mfma_f32_16x16x32_f16 v[94:97], v[10:13], v[94:97], 0
	v_mfma_f32_16x16x32_f16 v[102:105], v[10:13], v[102:105], 0
	v_mfma_f32_16x16x32_f16 v[106:109], v[10:13], v[106:109], 0
	v_mfma_f32_16x16x32_f16 v[124:127], v[10:13], v[124:127], 0
	v_mfma_f32_16x16x32_f16 v[10:13], v[10:13], v[146:149], 0
	s_mov_b32 s4, 0x34000
	v_add_co_u32_e32 v66, vcc, s4, v118
	s_mov_b32 s4, 0x35000
	s_nop 0
	v_addc_co_u32_e32 v67, vcc, 0, v119, vcc
	v_add_co_u32_e32 v118, vcc, s4, v118
	s_nop 1
	v_addc_co_u32_e32 v119, vcc, 0, v119, vcc
	global_load_dwordx4 v[146:149], v[118:119], off offset:-4096
	global_load_dwordx4 v[202:205], v[122:123], off offset:3072
	global_load_dwordx4 v[206:209], v[66:67], off offset:1024
	ds_read_b128 v[210:213], v1
	ds_read_b128 v[214:217], v1 offset:8192
	ds_read_b128 v[218:221], v1 offset:16384
	ds_read_b128 v[222:225], v1 offset:24576
	ds_read_b128 v[226:229], v1 offset:32768
	ds_read_b128 v[230:233], v1 offset:40960
	ds_read_b128 v[234:237], v1 offset:49152
	ds_read_b128 v[238:241], v1 offset:57344
	s_waitcnt lgkmcnt(7)
	v_mfma_f32_16x16x32_f16 v[74:77], v[22:25], v[210:213], v[74:77]
	s_waitcnt lgkmcnt(6)
	v_mfma_f32_16x16x32_f16 v[150:153], v[22:25], v[214:217], v[150:153]
	s_waitcnt lgkmcnt(5)
	v_mfma_f32_16x16x32_f16 v[154:157], v[22:25], v[218:221], v[154:157]
	s_waitcnt lgkmcnt(4)
	v_mfma_f32_16x16x32_f16 v[158:161], v[22:25], v[222:225], v[158:161]
	s_waitcnt lgkmcnt(3)
	v_mfma_f32_16x16x32_f16 v[162:165], v[22:25], v[226:229], v[162:165]
	s_waitcnt lgkmcnt(2)
	v_mfma_f32_16x16x32_f16 v[166:169], v[22:25], v[230:233], v[166:169]
	s_waitcnt lgkmcnt(1)
	v_mfma_f32_16x16x32_f16 v[170:173], v[22:25], v[234:237], v[170:173]
	s_waitcnt lgkmcnt(0)
	v_mfma_f32_16x16x32_f16 v[22:25], v[22:25], v[238:241], v[38:41]
	v_mfma_f32_16x16x32_f16 v[38:41], v[6:9], v[210:213], v[174:177]
	v_mfma_f32_16x16x32_f16 v[174:177], v[6:9], v[214:217], v[178:181]
	v_mfma_f32_16x16x32_f16 v[178:181], v[6:9], v[218:221], v[182:185]
	v_mfma_f32_16x16x32_f16 v[182:185], v[6:9], v[222:225], v[186:189]
	v_mfma_f32_16x16x32_f16 v[186:189], v[6:9], v[226:229], v[190:193]
	v_mfma_f32_16x16x32_f16 v[190:193], v[6:9], v[230:233], v[194:197]
	v_mfma_f32_16x16x32_f16 v[194:197], v[6:9], v[234:237], v[198:201]
	v_mfma_f32_16x16x32_f16 v[6:9], v[6:9], v[238:241], v[26:29]
	v_mfma_f32_16x16x32_f16 v[26:29], v[2:5], v[210:213], v[62:65]
	v_mfma_f32_16x16x32_f16 v[62:65], v[2:5], v[214:217], v[78:81]
	v_mfma_f32_16x16x32_f16 v[78:81], v[2:5], v[218:221], v[86:89]
	v_mfma_f32_16x16x32_f16 v[86:89], v[2:5], v[222:225], v[94:97]
	v_mfma_f32_16x16x32_f16 v[94:97], v[2:5], v[226:229], v[102:105]
	v_mfma_f32_16x16x32_f16 v[102:105], v[2:5], v[230:233], v[106:109]
	v_mfma_f32_16x16x32_f16 v[106:109], v[2:5], v[234:237], v[124:127]
	v_mfma_f32_16x16x32_f16 v[0:3], v[2:5], v[238:241], v[10:13]
	s_nop 2
	global_load_dwordx4 v[10:13], v[66:67], off offset:2048
	global_load_dwordx4 v[122:125], v[66:67], off offset:3072
	global_load_dwordx4 v[126:129], v[118:119], off
	ds_read_b128 v[198:201], v133
	ds_read_b128 v[210:213], v133 offset:8192
	ds_read_b128 v[214:217], v133 offset:16384
	ds_read_b128 v[218:221], v133 offset:24576
	ds_read_b128 v[222:225], v133 offset:32768
	ds_read_b128 v[226:229], v133 offset:40960
	ds_read_b128 v[230:233], v133 offset:49152
	ds_read_b128 v[234:237], v133 offset:57344
	s_waitcnt lgkmcnt(7)
	v_mfma_f32_16x16x32_f16 v[74:77], v[30:33], v[198:201], v[74:77]
	s_waitcnt lgkmcnt(6)
	v_mfma_f32_16x16x32_f16 v[150:153], v[30:33], v[210:213], v[150:153]
	s_waitcnt lgkmcnt(5)
	v_mfma_f32_16x16x32_f16 v[154:157], v[30:33], v[214:217], v[154:157]
	s_waitcnt lgkmcnt(4)
	v_mfma_f32_16x16x32_f16 v[158:161], v[30:33], v[218:221], v[158:161]
	s_waitcnt lgkmcnt(3)
	v_mfma_f32_16x16x32_f16 v[162:165], v[30:33], v[222:225], v[162:165]
	s_waitcnt lgkmcnt(2)
	v_mfma_f32_16x16x32_f16 v[166:169], v[30:33], v[226:229], v[166:169]
	s_waitcnt lgkmcnt(1)
	v_mfma_f32_16x16x32_f16 v[170:173], v[30:33], v[230:233], v[170:173]
	s_waitcnt lgkmcnt(0)
	v_mfma_f32_16x16x32_f16 v[22:25], v[30:33], v[234:237], v[22:25]
	v_mfma_f32_16x16x32_f16 v[30:33], v[14:17], v[198:201], v[38:41]
	v_mfma_f32_16x16x32_f16 v[38:41], v[14:17], v[210:213], v[174:177]
	v_mfma_f32_16x16x32_f16 v[174:177], v[14:17], v[214:217], v[178:181]
	v_mfma_f32_16x16x32_f16 v[178:181], v[14:17], v[218:221], v[182:185]
	v_mfma_f32_16x16x32_f16 v[182:185], v[14:17], v[222:225], v[186:189]
	v_mfma_f32_16x16x32_f16 v[186:189], v[14:17], v[226:229], v[190:193]
	v_mfma_f32_16x16x32_f16 v[190:193], v[14:17], v[230:233], v[194:197]
	v_mfma_f32_16x16x32_f16 v[4:7], v[14:17], v[234:237], v[6:9]
	v_mfma_f32_16x16x32_f16 v[14:17], v[18:21], v[198:201], v[26:29]
	v_mfma_f32_16x16x32_f16 v[26:29], v[18:21], v[210:213], v[62:65]
	v_mfma_f32_16x16x32_f16 v[62:65], v[18:21], v[214:217], v[78:81]
	v_mfma_f32_16x16x32_f16 v[78:81], v[18:21], v[218:221], v[86:89]
	v_mfma_f32_16x16x32_f16 v[86:89], v[18:21], v[222:225], v[94:97]
	v_mfma_f32_16x16x32_f16 v[94:97], v[18:21], v[226:229], v[102:105]
	v_mfma_f32_16x16x32_f16 v[102:105], v[18:21], v[230:233], v[106:109]
	v_mfma_f32_16x16x32_f16 v[0:3], v[18:21], v[234:237], v[0:3]
	global_load_dwordx4 v[18:21], v[118:119], off offset:1024
	s_nop 0
	global_load_dwordx4 v[106:109], v[118:119], off offset:2048
	global_load_dwordx4 v[194:197], v[118:119], off offset:3072
	ds_read_b128 v[198:201], v135
	ds_read_b128 v[210:213], v135 offset:8192
	ds_read_b128 v[214:217], v135 offset:16384
	ds_read_b128 v[218:221], v135 offset:24576
	ds_read_b128 v[222:225], v135 offset:32768
	ds_read_b128 v[226:229], v135 offset:40960
	ds_read_b128 v[230:233], v135 offset:49152
	ds_read_b128 v[234:237], v135 offset:57344
	s_waitcnt lgkmcnt(7)
	v_mfma_f32_16x16x32_f16 v[74:77], v[46:49], v[198:201], v[74:77]
	s_waitcnt lgkmcnt(6)
	v_mfma_f32_16x16x32_f16 v[150:153], v[46:49], v[210:213], v[150:153]
	s_waitcnt lgkmcnt(5)
	v_mfma_f32_16x16x32_f16 v[154:157], v[46:49], v[214:217], v[154:157]
	s_waitcnt lgkmcnt(4)
	v_mfma_f32_16x16x32_f16 v[158:161], v[46:49], v[218:221], v[158:161]
	s_waitcnt lgkmcnt(3)
	v_mfma_f32_16x16x32_f16 v[162:165], v[46:49], v[222:225], v[162:165]
	s_waitcnt lgkmcnt(2)
	v_mfma_f32_16x16x32_f16 v[166:169], v[46:49], v[226:229], v[166:169]
	s_waitcnt lgkmcnt(1)
	v_mfma_f32_16x16x32_f16 v[170:173], v[46:49], v[230:233], v[170:173]
	s_waitcnt lgkmcnt(0)
	v_mfma_f32_16x16x32_f16 v[22:25], v[46:49], v[234:237], v[22:25]
	v_mfma_f32_16x16x32_f16 v[30:33], v[42:45], v[198:201], v[30:33]
	v_mfma_f32_16x16x32_f16 v[38:41], v[42:45], v[210:213], v[38:41]
	v_mfma_f32_16x16x32_f16 v[46:49], v[42:45], v[214:217], v[174:177]
	v_mfma_f32_16x16x32_f16 v[174:177], v[42:45], v[218:221], v[178:181]
	v_mfma_f32_16x16x32_f16 v[178:181], v[42:45], v[222:225], v[182:185]
	v_mfma_f32_16x16x32_f16 v[182:185], v[42:45], v[226:229], v[186:189]
	v_mfma_f32_16x16x32_f16 v[186:189], v[42:45], v[230:233], v[190:193]
	v_mfma_f32_16x16x32_f16 v[4:7], v[42:45], v[234:237], v[4:7]
	v_mfma_f32_16x16x32_f16 v[14:17], v[34:37], v[198:201], v[14:17]
	v_mfma_f32_16x16x32_f16 v[26:29], v[34:37], v[210:213], v[26:29]
	v_mfma_f32_16x16x32_f16 v[42:45], v[34:37], v[214:217], v[62:65]
	v_mfma_f32_16x16x32_f16 v[62:65], v[34:37], v[218:221], v[78:81]
	v_mfma_f32_16x16x32_f16 v[78:81], v[34:37], v[222:225], v[86:89]
	v_mfma_f32_16x16x32_f16 v[86:89], v[34:37], v[226:229], v[94:97]
	v_mfma_f32_16x16x32_f16 v[94:97], v[34:37], v[230:233], v[102:105]
	v_mfma_f32_16x16x32_f16 v[0:3], v[34:37], v[234:237], v[0:3]
	ds_read_b128 v[34:37], v136
	s_nop 0
	ds_read_b128 v[102:105], v136 offset:8192
	ds_read_b128 v[190:193], v136 offset:16384
	ds_read_b128 v[198:201], v136 offset:24576
	ds_read_b128 v[210:213], v136 offset:32768
	ds_read_b128 v[214:217], v136 offset:40960
	ds_read_b128 v[218:221], v136 offset:49152
	ds_read_b128 v[222:225], v136 offset:57344
	s_waitcnt vmcnt(17) lgkmcnt(7)
	v_mfma_f32_16x16x32_f16 v[74:77], v[50:53], v[34:37], v[74:77]
	s_waitcnt lgkmcnt(6)
	v_mfma_f32_16x16x32_f16 v[150:153], v[50:53], v[102:105], v[150:153]
	s_waitcnt lgkmcnt(5)
	v_mfma_f32_16x16x32_f16 v[154:157], v[50:53], v[190:193], v[154:157]
	s_waitcnt lgkmcnt(4)
	v_mfma_f32_16x16x32_f16 v[158:161], v[50:53], v[198:201], v[158:161]
	s_waitcnt lgkmcnt(3)
	v_mfma_f32_16x16x32_f16 v[162:165], v[50:53], v[210:213], v[162:165]
	s_waitcnt lgkmcnt(2)
	v_mfma_f32_16x16x32_f16 v[166:169], v[50:53], v[214:217], v[166:169]
	s_waitcnt lgkmcnt(1)
	v_mfma_f32_16x16x32_f16 v[170:173], v[50:53], v[218:221], v[170:173]
	s_waitcnt lgkmcnt(0)
	v_mfma_f32_16x16x32_f16 v[22:25], v[50:53], v[222:225], v[22:25]
	s_waitcnt vmcnt(16)
	v_mfma_f32_16x16x32_f16 v[30:33], v[54:57], v[34:37], v[30:33]
	v_mfma_f32_16x16x32_f16 v[38:41], v[54:57], v[102:105], v[38:41]
	v_mfma_f32_16x16x32_f16 v[46:49], v[54:57], v[190:193], v[46:49]
	v_mfma_f32_16x16x32_f16 v[50:53], v[54:57], v[198:201], v[174:177]
	v_mfma_f32_16x16x32_f16 v[174:177], v[54:57], v[210:213], v[178:181]
	v_mfma_f32_16x16x32_f16 v[178:181], v[54:57], v[214:217], v[182:185]
	v_mfma_f32_16x16x32_f16 v[182:185], v[54:57], v[218:221], v[186:189]
	v_mfma_f32_16x16x32_f16 v[4:7], v[54:57], v[222:225], v[4:7]
	s_waitcnt vmcnt(15)
	v_mfma_f32_16x16x32_f16 v[14:17], v[58:61], v[34:37], v[14:17]
	v_mfma_f32_16x16x32_f16 v[26:29], v[58:61], v[102:105], v[26:29]
	v_mfma_f32_16x16x32_f16 v[34:37], v[58:61], v[190:193], v[42:45]
	v_mfma_f32_16x16x32_f16 v[42:45], v[58:61], v[198:201], v[62:65]
	v_mfma_f32_16x16x32_f16 v[54:57], v[58:61], v[210:213], v[78:81]
	v_mfma_f32_16x16x32_f16 v[62:65], v[58:61], v[214:217], v[86:89]
	v_mfma_f32_16x16x32_f16 v[78:81], v[58:61], v[218:221], v[94:97]
	v_mfma_f32_16x16x32_f16 v[0:3], v[58:61], v[222:225], v[0:3]
	ds_read_b128 v[58:61], v137
	ds_read_b128 v[86:89], v137 offset:8192
	ds_read_b128 v[94:97], v137 offset:16384
	ds_read_b128 v[102:105], v137 offset:24576
	ds_read_b128 v[186:189], v137 offset:32768
	ds_read_b128 v[190:193], v137 offset:40960
	ds_read_b128 v[198:201], v137 offset:49152
	ds_read_b128 v[134:137], v137 offset:57344
	s_waitcnt vmcnt(7) lgkmcnt(7)
	v_mfma_f32_16x16x32_f16 v[74:77], v[202:205], v[58:61], v[74:77]
	s_waitcnt lgkmcnt(6)
	v_mfma_f32_16x16x32_f16 v[150:153], v[202:205], v[86:89], v[150:153]
	s_waitcnt lgkmcnt(5)
	v_mfma_f32_16x16x32_f16 v[154:157], v[202:205], v[94:97], v[154:157]
	s_waitcnt lgkmcnt(4)
	v_mfma_f32_16x16x32_f16 v[158:161], v[202:205], v[102:105], v[158:161]
	s_waitcnt lgkmcnt(3)
	v_mfma_f32_16x16x32_f16 v[162:165], v[202:205], v[186:189], v[162:165]
	s_waitcnt lgkmcnt(2)
	v_mfma_f32_16x16x32_f16 v[166:169], v[202:205], v[190:193], v[166:169]
	s_waitcnt lgkmcnt(1)
	v_mfma_f32_16x16x32_f16 v[170:173], v[202:205], v[198:201], v[170:173]
	s_waitcnt lgkmcnt(0)
	v_mfma_f32_16x16x32_f16 v[22:25], v[202:205], v[134:137], v[22:25]
	v_mfma_f32_16x16x32_f16 v[30:33], v[146:149], v[58:61], v[30:33]
	v_mfma_f32_16x16x32_f16 v[38:41], v[146:149], v[86:89], v[38:41]
	v_mfma_f32_16x16x32_f16 v[46:49], v[146:149], v[94:97], v[46:49]
	v_mfma_f32_16x16x32_f16 v[50:53], v[146:149], v[102:105], v[50:53]
	v_mfma_f32_16x16x32_f16 v[174:177], v[146:149], v[186:189], v[174:177]
	v_mfma_f32_16x16x32_f16 v[178:181], v[146:149], v[190:193], v[178:181]
	v_mfma_f32_16x16x32_f16 v[182:185], v[146:149], v[198:201], v[182:185]
	v_mfma_f32_16x16x32_f16 v[4:7], v[146:149], v[134:137], v[4:7]
	s_waitcnt vmcnt(6)
	v_mfma_f32_16x16x32_f16 v[14:17], v[206:209], v[58:61], v[14:17]
	v_mfma_f32_16x16x32_f16 v[26:29], v[206:209], v[86:89], v[26:29]
	v_mfma_f32_16x16x32_f16 v[34:37], v[206:209], v[94:97], v[34:37]
	v_mfma_f32_16x16x32_f16 v[42:45], v[206:209], v[102:105], v[42:45]
	v_mfma_f32_16x16x32_f16 v[54:57], v[206:209], v[186:189], v[54:57]
	v_mfma_f32_16x16x32_f16 v[58:61], v[206:209], v[190:193], v[62:65]
	v_mfma_f32_16x16x32_f16 v[62:65], v[206:209], v[198:201], v[78:81]
	v_mfma_f32_16x16x32_f16 v[0:3], v[206:209], v[134:137], v[0:3]
	s_nop 1
	ds_read_b128 v[78:81], v138
	ds_read_b128 v[86:89], v138 offset:8192
	ds_read_b128 v[94:97], v138 offset:16384
	ds_read_b128 v[102:105], v138 offset:24576
	ds_read_b128 v[134:137], v138 offset:32768
	ds_read_b128 v[146:149], v138 offset:40960
	ds_read_b128 v[186:189], v138 offset:49152
	ds_read_b128 v[190:193], v138 offset:57344
	s_waitcnt vmcnt(5) lgkmcnt(7)
	v_mfma_f32_16x16x32_f16 v[74:77], v[10:13], v[78:81], v[74:77]
	s_waitcnt lgkmcnt(6)
	v_mfma_f32_16x16x32_f16 v[150:153], v[10:13], v[86:89], v[150:153]
	s_waitcnt lgkmcnt(5)
	v_mfma_f32_16x16x32_f16 v[154:157], v[10:13], v[94:97], v[154:157]
	s_waitcnt lgkmcnt(4)
	v_mfma_f32_16x16x32_f16 v[158:161], v[10:13], v[102:105], v[158:161]
	s_waitcnt lgkmcnt(3)
	v_mfma_f32_16x16x32_f16 v[162:165], v[10:13], v[134:137], v[162:165]
	s_waitcnt lgkmcnt(2)
	v_mfma_f32_16x16x32_f16 v[166:169], v[10:13], v[146:149], v[166:169]
	s_waitcnt lgkmcnt(1)
	v_mfma_f32_16x16x32_f16 v[170:173], v[10:13], v[186:189], v[170:173]
	s_waitcnt lgkmcnt(0)
	v_mfma_f32_16x16x32_f16 v[8:11], v[10:13], v[190:193], v[22:25]
	s_waitcnt vmcnt(4)
	v_mfma_f32_16x16x32_f16 v[22:25], v[122:125], v[78:81], v[30:33]
	v_mfma_f32_16x16x32_f16 v[30:33], v[122:125], v[86:89], v[38:41]
	v_mfma_f32_16x16x32_f16 v[198:201], v[122:125], v[94:97], v[46:49]
	v_mfma_f32_16x16x32_f16 v[48:51], v[122:125], v[102:105], v[50:53]
	v_mfma_f32_16x16x32_f16 v[174:177], v[122:125], v[134:137], v[174:177]
	v_mfma_f32_16x16x32_f16 v[178:181], v[122:125], v[146:149], v[178:181]
	v_mfma_f32_16x16x32_f16 v[182:185], v[122:125], v[186:189], v[182:185]
	v_mfma_f32_16x16x32_f16 v[4:7], v[122:125], v[190:193], v[4:7]
	s_waitcnt vmcnt(3)
	v_mfma_f32_16x16x32_f16 v[12:15], v[126:129], v[78:81], v[14:17]
	v_mfma_f32_16x16x32_f16 v[78:81], v[126:129], v[86:89], v[26:29]
	v_mfma_f32_16x16x32_f16 v[86:89], v[126:129], v[94:97], v[34:37]
	v_mfma_f32_16x16x32_f16 v[40:43], v[126:129], v[102:105], v[42:45]
	v_mfma_f32_16x16x32_f16 v[94:97], v[126:129], v[134:137], v[54:57]
	v_mfma_f32_16x16x32_f16 v[102:105], v[126:129], v[146:149], v[58:61]
	v_mfma_f32_16x16x32_f16 v[64:67], v[126:129], v[186:189], v[62:65]
	v_mfma_f32_16x16x32_f16 v[0:3], v[126:129], v[190:193], v[0:3]
	s_nop 1
	ds_read_b128 v[60:63], v140
	ds_read_b128 v[122:125], v140 offset:8192
	ds_read_b128 v[126:129], v140 offset:16384
	ds_read_b128 v[134:137], v140 offset:24576
	ds_read_b128 v[146:149], v140 offset:32768
	ds_read_b128 v[186:189], v140 offset:40960
	ds_read_b128 v[190:193], v140 offset:49152
	ds_read_b128 v[202:205], v140 offset:57344
	s_waitcnt vmcnt(2) lgkmcnt(7)
	v_mfma_f32_16x16x32_f16 v[74:77], v[18:21], v[60:63], v[74:77]
	s_waitcnt lgkmcnt(6)
	v_mfma_f32_16x16x32_f16 v[150:153], v[18:21], v[122:125], v[150:153]
	s_waitcnt lgkmcnt(5)
	v_mfma_f32_16x16x32_f16 v[154:157], v[18:21], v[126:129], v[154:157]
	s_waitcnt lgkmcnt(4)
	v_mfma_f32_16x16x32_f16 v[158:161], v[18:21], v[134:137], v[158:161]
	s_waitcnt lgkmcnt(3)
	v_mfma_f32_16x16x32_f16 v[56:59], v[18:21], v[146:149], v[162:165]
	s_waitcnt lgkmcnt(2)
	v_mfma_f32_16x16x32_f16 v[52:55], v[18:21], v[186:189], v[166:169]
	s_waitcnt lgkmcnt(1)
	v_mfma_f32_16x16x32_f16 v[44:47], v[18:21], v[190:193], v[170:173]
	s_waitcnt lgkmcnt(0)
	v_mfma_f32_16x16x32_f16 v[36:39], v[18:21], v[202:205], v[8:11]
	s_waitcnt vmcnt(1)
	v_mfma_f32_16x16x32_f16 v[162:165], v[106:109], v[60:63], v[22:25]
	v_mfma_f32_16x16x32_f16 v[166:169], v[106:109], v[122:125], v[30:33]
	v_mfma_f32_16x16x32_f16 v[170:173], v[106:109], v[126:129], v[198:201]
	v_mfma_f32_16x16x32_f16 v[198:201], v[106:109], v[134:137], v[48:51]
	v_mfma_f32_16x16x32_f16 v[32:35], v[106:109], v[146:149], v[174:177]
	v_mfma_f32_16x16x32_f16 v[24:27], v[106:109], v[186:189], v[178:181]
	v_mfma_f32_16x16x32_f16 v[20:23], v[106:109], v[190:193], v[182:185]
	v_mfma_f32_16x16x32_f16 v[16:19], v[106:109], v[202:205], v[4:7]
	s_waitcnt vmcnt(0)
	v_mfma_f32_16x16x32_f16 v[106:109], v[194:197], v[60:63], v[12:15]
	v_mfma_f32_16x16x32_f16 v[78:81], v[194:197], v[122:125], v[78:81]
	v_mfma_f32_16x16x32_f16 v[86:89], v[194:197], v[126:129], v[86:89]
	v_mfma_f32_16x16x32_f16 v[60:63], v[194:197], v[134:137], v[40:43]
	v_mfma_f32_16x16x32_f16 v[12:15], v[194:197], v[146:149], v[94:97]
	v_mfma_f32_16x16x32_f16 v[8:11], v[194:197], v[186:189], v[102:105]
	v_mfma_f32_16x16x32_f16 v[4:7], v[194:197], v[190:193], v[64:67]
	v_mfma_f32_16x16x32_f16 v[0:3], v[194:197], v[202:205], v[0:3]
	global_load_dwordx4 v[48:51], v[120:121], off offset:1536
	global_load_dwordx4 v[40:43], v[120:121], off offset:1600
	global_load_dwordx4 v[28:31], v[120:121], off offset:1664
	v_mov_b32_e32 v94, v155
	v_mov_b32_e32 v95, v156
	v_mov_b32_e32 v96, v159
	v_mov_b32_e32 v97, v160
	v_mov_b32_e32 v64, v151
	v_mov_b32_e32 v65, v152
	v_mov_b32_e32 v102, v167
	v_mov_b32_e32 v103, v168
	v_mov_b32_e32 v104, v171
	v_mov_b32_e32 v105, v172
	v_mov_b32_e32 v118, v199
	v_mov_b32_e32 v119, v200
	s_barrier
	s_waitcnt vmcnt(2)
	v_pk_add_f32 v[74:75], v[74:75], v[48:49]
	v_add_f32_e32 v82, v150, v48
	v_pk_mov_b32 v[120:121], v[48:49], v[50:51] op_sel:[1,0]
	v_add_f32_e32 v49, v153, v51
	s_waitcnt vmcnt(1)
	v_pk_add_f32 v[122:123], v[162:163], v[40:41]
	v_add_f32_e32 v98, v166, v40
	v_pk_mov_b32 v[66:67], v[40:41], v[42:43] op_sel:[1,0]
	v_add_f32_e32 v41, v169, v43
	v_pk_add_f32 v[76:77], v[76:77], v[50:51]
	v_add_f32_e32 v50, v154, v48
	v_add_f32_e32 v85, v157, v51
	v_add_f32_e32 v90, v158, v48
	v_add_f32_e32 v93, v161, v51
	v_pk_add_f32 v[124:125], v[164:165], v[42:43]
	v_add_f32_e32 v42, v170, v40
	v_add_f32_e32 v101, v173, v43
	v_add_f32_e32 v126, v198, v40
	v_add_f32_e32 v127, v201, v43
	v_cvt_f16_f32_e32 v82, v82
	v_cvt_f16_f32_e32 v49, v49
	v_cvt_f16_f32_e32 v98, v98
	v_cvt_f16_f32_e32 v41, v41
	v_cvt_pk_f16_f32 v74, v74, v75
	v_cvt_pk_f16_f32 v75, v76, v77
	v_cvt_f16_f32_e32 v50, v50
	v_pk_add_f32 v[76:77], v[94:95], v[120:121]
	v_cvt_f16_f32_e32 v85, v85
	v_cvt_f16_f32_e32 v90, v90
	v_pk_add_f32 v[94:95], v[96:97], v[120:121]
	v_cvt_f16_f32_e32 v93, v93
	v_cvt_pk_f16_f32 v96, v122, v123
	v_cvt_f16_f32_e32 v42, v42
	v_cvt_f16_f32_e32 v101, v101
	v_cvt_f16_f32_e32 v122, v126
	v_cvt_f16_f32_e32 v123, v127
	v_pk_add_f32 v[64:65], v[64:65], v[120:121]
	v_pk_add_f32 v[102:103], v[102:103], v[66:67]
	v_pk_add_f32 v[104:105], v[104:105], v[66:67]
	v_pk_add_f32 v[118:119], v[118:119], v[66:67]
	v_cvt_pk_f16_f32 v65, v64, v65
	v_cvt_pk_f16_f32 v76, v76, v77
	v_cvt_pk_f16_f32 v77, v94, v95
	v_cvt_pk_f16_f32 v95, v102, v103
	s_waitcnt vmcnt(0)
	v_pk_add_f32 v[106:107], v[106:107], v[28:29]
	v_pk_add_f32 v[108:109], v[108:109], v[30:31]
	v_cvt_pk_f16_f32 v97, v124, v125
	v_cvt_pk_f16_f32 v102, v104, v105
	v_cvt_pk_f16_f32 v103, v118, v119
	v_pack_b32_f16 v64, v82, v65
	v_alignbit_b32 v65, v49, v65, 16
	v_pack_b32_f16 v94, v98, v95
	v_alignbit_b32 v95, v41, v95, 16
	v_add_f32_e32 v78, v78, v28
	v_cvt_pk_f16_f32 v106, v106, v107
	v_cvt_pk_f16_f32 v107, v108, v109
	ds_write2_b64 v130, v[74:75], v[96:97] offset1:4
	ds_write_b64 v130, v[106:107] offset:64
	v_pack_b32_f16 v74, v50, v76
	v_alignbit_b32 v75, v85, v76, 16
	v_pack_b32_f16 v76, v90, v77
	v_alignbit_b32 v77, v93, v77, 16
	v_pack_b32_f16 v96, v42, v102
	v_alignbit_b32 v97, v101, v102, 16
	v_pack_b32_f16 v102, v122, v103
	v_alignbit_b32 v103, v123, v103, 16
	ds_write2_b64 v132, v[64:65], v[94:95] offset0:32 offset1:36
	ds_write2_b64 v131, v[74:75], v[96:97] offset0:64 offset1:68
	ds_write2_b64 v91, v[76:77], v[102:103] offset0:96 offset1:100
	v_pk_mov_b32 v[64:65], v[28:29], v[30:31] op_sel:[1,0]
	v_add_f32_e32 v29, v81, v31
	v_cvt_f16_f32_e32 v78, v78
	v_cvt_f16_f32_e32 v29, v29
	v_mov_b32_e32 v74, v79
	v_mov_b32_e32 v75, v80
	v_pk_add_f32 v[74:75], v[74:75], v[64:65]
	v_add_f32_e32 v56, v56, v48
	v_cvt_pk_f16_f32 v30, v74, v75
	v_pack_b32_f16 v74, v78, v30
	v_alignbit_b32 v75, v29, v30, 16
	v_add_f32_e32 v29, v86, v28
	v_add_f32_e32 v30, v89, v31
	v_cvt_f16_f32_e32 v29, v29
	v_cvt_f16_f32_e32 v30, v30
	ds_write_b64 v130, v[74:75] offset:12608
	v_mov_b32_e32 v74, v87
	v_mov_b32_e32 v75, v88
	v_pk_add_f32 v[74:75], v[74:75], v[64:65]
	v_add_f32_e32 v52, v52, v48
	v_cvt_pk_f16_f32 v41, v74, v75
	v_pack_b32_f16 v74, v29, v41
	v_alignbit_b32 v75, v30, v41, 16
	v_add_f32_e32 v29, v60, v28
	v_add_f32_e32 v30, v63, v31
	v_cvt_f16_f32_e32 v29, v29
	v_cvt_f16_f32_e32 v30, v30
	v_mov_b32_e32 v60, v61
	v_mov_b32_e32 v61, v62
	v_pk_add_f32 v[60:61], v[60:61], v[64:65]
	ds_write_b64 v130, v[74:75] offset:25152
	v_cvt_pk_f16_f32 v41, v60, v61
	v_pack_b32_f16 v60, v29, v41
	v_alignbit_b32 v61, v30, v41, 16
	ds_write_b64 v130, v[60:61] offset:37696
	s_waitcnt lgkmcnt(0)
	s_barrier
	ds_read_b128 v[60:63], v83
	ds_read_b128 v[74:77], v84
	v_add_u32_e32 v29, 0x300, v111
	v_add_u32_e32 v30, v29, v112
	v_add_f32_e32 v44, v44, v48
	s_waitcnt lgkmcnt(1)
	buffer_store_dwordx4 v[60:63], v30, s[0:3], 0 offen sc1
	v_add_u32_e32 v30, 0x300, v113
	ds_read_b128 v[60:63], v92
	v_add_u32_e32 v41, v30, v114
	s_waitcnt lgkmcnt(1)
	buffer_store_dwordx4 v[74:77], v41, s[0:3], 0 offen sc1
	ds_read_b128 v[74:77], v99
	v_add_u32_e32 v41, 0x300, v115
	v_add_u32_e32 v42, v41, v116
	s_waitcnt lgkmcnt(1)
	buffer_store_dwordx4 v[60:63], v42, s[0:3], 0 offen sc1
	v_add_u32_e32 v42, 0x300, v117
	ds_read_b128 v[60:63], v100
	v_add_u32_e32 v49, v42, v142
	s_waitcnt lgkmcnt(1)
	buffer_store_dwordx4 v[74:77], v49, s[0:3], 0 offen sc1
	ds_read_b128 v[74:77], v110
	v_add_u32_e32 v49, 0x300, v143
	v_add_u32_e32 v50, v49, v141
	s_waitcnt lgkmcnt(1)
	buffer_store_dwordx4 v[60:63], v50, s[0:3], 0 offen sc1
	v_add_u32_e32 v50, 0x300, v144
	v_add_f32_e32 v36, v36, v48
	v_add_u32_e32 v60, v50, v145
	s_waitcnt lgkmcnt(0)
	buffer_store_dwordx4 v[74:77], v60, s[0:3], 0 offen sc1
	v_cvt_f16_f32_e32 v60, v56
	v_mov_b32_e32 v56, v57
	v_mov_b32_e32 v57, v58
	v_add_f32_e32 v58, v59, v51
	v_cvt_f16_f32_e32 v58, v58
	v_pk_add_f32 v[56:57], v[56:57], v[120:121]
	v_add_f32_e32 v32, v32, v40
	v_cvt_pk_f16_f32 v57, v56, v57
	v_pack_b32_f16 v56, v60, v57
	v_alignbit_b32 v57, v58, v57, 16
	v_cvt_f16_f32_e32 v58, v52
	v_mov_b32_e32 v52, v53
	v_mov_b32_e32 v53, v54
	v_add_f32_e32 v54, v55, v51
	v_cvt_f16_f32_e32 v54, v54
	v_pk_add_f32 v[52:53], v[52:53], v[120:121]
	v_add_f32_e32 v24, v24, v40
	v_cvt_pk_f16_f32 v53, v52, v53
	v_pack_b32_f16 v52, v58, v53
	v_alignbit_b32 v53, v54, v53, 16
	v_cvt_f16_f32_e32 v54, v44
	v_mov_b32_e32 v44, v45
	v_mov_b32_e32 v45, v46
	v_add_f32_e32 v46, v47, v51
	v_cvt_f16_f32_e32 v46, v46
	v_pk_add_f32 v[44:45], v[44:45], v[120:121]
	s_nop 0
	v_cvt_pk_f16_f32 v45, v44, v45
	v_pack_b32_f16 v44, v54, v45
	v_alignbit_b32 v45, v46, v45, 16
	v_cvt_f16_f32_e32 v46, v36
	v_mov_b32_e32 v36, v37
	v_mov_b32_e32 v37, v38
	v_add_f32_e32 v38, v39, v51
	v_cvt_f16_f32_e32 v38, v38
	v_pk_add_f32 v[36:37], v[36:37], v[120:121]
	s_barrier
	v_cvt_pk_f16_f32 v37, v36, v37
	v_pack_b32_f16 v36, v46, v37
	v_alignbit_b32 v37, v38, v37, 16
	v_cvt_f16_f32_e32 v38, v32
	v_mov_b32_e32 v32, v33
	v_mov_b32_e32 v33, v34
	v_add_f32_e32 v34, v35, v43
	v_cvt_f16_f32_e32 v34, v34
	v_pk_add_f32 v[32:33], v[32:33], v[66:67]
	s_nop 0
	v_cvt_pk_f16_f32 v33, v32, v33
	v_pack_b32_f16 v32, v38, v33
	v_alignbit_b32 v33, v34, v33, 16
	ds_write2_b64 v130, v[56:57], v[32:33] offset1:4
	v_cvt_f16_f32_e32 v32, v24
	v_mov_b32_e32 v24, v25
	v_mov_b32_e32 v25, v26
	v_add_f32_e32 v26, v27, v43
	v_cvt_f16_f32_e32 v26, v26
	v_pk_add_f32 v[24:25], v[24:25], v[66:67]
	v_add_f32_e32 v20, v20, v40
	v_cvt_pk_f16_f32 v25, v24, v25
	v_pack_b32_f16 v24, v32, v25
	v_alignbit_b32 v25, v26, v25, 16
	ds_write2_b64 v132, v[52:53], v[24:25] offset0:32 offset1:36
	v_cvt_f16_f32_e32 v24, v20
	v_mov_b32_e32 v20, v21
	v_mov_b32_e32 v21, v22
	v_add_f32_e32 v22, v23, v43
	v_cvt_f16_f32_e32 v22, v22
	v_pk_add_f32 v[20:21], v[20:21], v[66:67]
	v_add_f32_e32 v16, v16, v40
	v_cvt_pk_f16_f32 v21, v20, v21
	v_pack_b32_f16 v20, v24, v21
	v_alignbit_b32 v21, v22, v21, 16
	ds_write2_b64 v131, v[44:45], v[20:21] offset0:64 offset1:68
	v_cvt_f16_f32_e32 v20, v16
	v_mov_b32_e32 v16, v17
	v_mov_b32_e32 v17, v18
	v_add_f32_e32 v18, v19, v43
	v_cvt_f16_f32_e32 v18, v18
	v_pk_add_f32 v[16:17], v[16:17], v[66:67]
	v_add_f32_e32 v12, v12, v28
	v_cvt_pk_f16_f32 v17, v16, v17
	v_pack_b32_f16 v16, v20, v17
	v_alignbit_b32 v17, v18, v17, 16
	ds_write2_b64 v91, v[36:37], v[16:17] offset0:96 offset1:100
	v_cvt_f16_f32_e32 v16, v12
	v_mov_b32_e32 v12, v13
	v_mov_b32_e32 v13, v14
	v_add_f32_e32 v14, v15, v31
	v_cvt_f16_f32_e32 v14, v14
	v_pk_add_f32 v[12:13], v[12:13], v[64:65]
	v_add_f32_e32 v8, v8, v28
	v_cvt_pk_f16_f32 v13, v12, v13
	v_pack_b32_f16 v12, v16, v13
	v_alignbit_b32 v13, v14, v13, 16
	ds_write_b64 v130, v[12:13] offset:64
	v_cvt_f16_f32_e32 v12, v8
	v_mov_b32_e32 v8, v9
	v_mov_b32_e32 v9, v10
	v_add_f32_e32 v10, v11, v31
	v_cvt_f16_f32_e32 v10, v10
	v_pk_add_f32 v[8:9], v[8:9], v[64:65]
	v_add_f32_e32 v4, v4, v28
	v_cvt_pk_f16_f32 v9, v8, v9
	v_pack_b32_f16 v8, v12, v9
	v_alignbit_b32 v9, v10, v9, 16
	ds_write_b64 v130, v[8:9] offset:12608
	v_cvt_f16_f32_e32 v8, v4
	v_mov_b32_e32 v4, v5
	v_mov_b32_e32 v5, v6
	v_add_f32_e32 v6, v7, v31
	v_cvt_f16_f32_e32 v6, v6
	v_pk_add_f32 v[4:5], v[4:5], v[64:65]
	v_add_f32_e32 v0, v0, v28
	v_cvt_pk_f16_f32 v5, v4, v5
	v_pack_b32_f16 v4, v8, v5
	v_alignbit_b32 v5, v6, v5, 16
	ds_write_b64 v130, v[4:5] offset:25152
	v_cvt_f16_f32_e32 v4, v0
	v_mov_b32_e32 v0, v1
	v_mov_b32_e32 v1, v2
	v_add_f32_e32 v2, v3, v31
	v_cvt_f16_f32_e32 v2, v2
	v_pk_add_f32 v[0:1], v[0:1], v[64:65]
	v_add_u32_e32 v8, v29, v68
	v_cvt_pk_f16_f32 v1, v0, v1
	v_pack_b32_f16 v0, v4, v1
	v_alignbit_b32 v1, v2, v1, 16
	ds_write_b64 v130, v[0:1] offset:37696
	s_waitcnt lgkmcnt(0)
	s_barrier
	ds_read_b128 v[0:3], v83
	ds_read_b128 v[4:7], v84
	v_add_u32_e32 v12, v42, v70
	s_waitcnt lgkmcnt(1)
	buffer_store_dwordx4 v[0:3], v8, s[0:3], 0 offen sc1
	ds_read_b128 v[0:3], v92
	v_add_u32_e32 v8, v30, v69
	s_waitcnt lgkmcnt(1)
	buffer_store_dwordx4 v[4:7], v8, s[0:3], 0 offen sc1
	v_add_u32_e32 v8, v41, v72
	ds_read_b128 v[4:7], v99
	s_waitcnt lgkmcnt(1)
	buffer_store_dwordx4 v[0:3], v8, s[0:3], 0 offen sc1
	ds_read_b128 v[0:3], v100
	ds_read_b128 v[8:11], v110
	s_waitcnt lgkmcnt(2)
	buffer_store_dwordx4 v[4:7], v12, s[0:3], 0 offen sc1
	s_nop 1
	v_add_u32_e32 v4, v49, v71
	s_waitcnt lgkmcnt(1)
	buffer_store_dwordx4 v[0:3], v4, s[0:3], 0 offen sc1
	s_nop 1
	v_add_u32_e32 v0, v50, v73
	s_waitcnt lgkmcnt(0)
	buffer_store_dwordx4 v[8:11], v0, s[0:3], 0 offen sc1
	s_endpgm

.LBB3_3:
	s_load_dwordx4 s[12:15], s[0:1], 0x70
	s_load_dwordx2 s[20:21], s[0:1], 0x80
	v_and_b32_e32 v1, 15, v0
	s_and_b32 s30, s6, 56
	s_and_b32 s11, s11, 48
	s_andn2_b64 vcc, exec, s[4:5]
	v_bfe_u32 v158, v0, 4, 2
	s_cbranch_vccnz .LBB3_82
	s_bfe_u32 s4, s24, 0x10006
	s_lshl_b32 s5, s4, 4
	s_ashr_i32 s2, s3, 31
	s_mul_i32 s17, s3, 40
	s_mul_hi_i32 s16, s3, 40
	s_add_u32 s22, s0, s17
	s_addc_u32 s23, s1, s16
	s_load_dwordx4 s[16:19], s[22:23], 0x0
	s_load_dwordx2 s[0:1], s[22:23], 0x10
	v_or_b32_e32 v159, s5, v1
	v_lshlrev_b32_e32 v18, 5, v159
	s_waitcnt lgkmcnt(0)
	global_load_dwordx4 v[230:233], v18, s[18:19]
	global_load_dwordx4 v[234:237], v18, s[0:1]
	global_load_dwordx4 v[238:241], v18, s[18:19] offset:16
	global_load_dwordx4 v[242:245], v18, s[0:1] offset:16
	v_bfe_u32 v21, v0, 7, 1
	v_lshrrev_b32_e32 v19, 4, v0
	v_lshrrev_b32_e32 v20, 6, v0
	v_lshlrev_b16_e32 v24, 2, v21
	v_lshrrev_b32_e32 v18, 5, v0
	s_movk_i32 s0, 0x3000
	v_and_b32_e32 v23, 4, v20
	v_and_b32_e32 v25, 3, v19
	v_lshlrev_b32_e32 v20, 12, v20
	v_lshlrev_b32_e32 v21, 11, v21
	v_bitop3_b16 v19, v24, v19, 3 bitop3:0xf8
	s_bitcmp1_b32 s24, 6
	v_and_b32_e32 v18, 4, v18
	v_or3_b32 v163, v20, v21, s0
	v_and_b32_e32 v19, 0xffff, v19
	s_cselect_b64 s[24:25], -1, 0
	s_lshl_b32 s0, s6, 6
	v_or_b32_e32 v161, v18, v158
	v_add_u32_e32 v162, s30, v23
	v_bitop3_b16 v24, v24, 8, v25 bitop3:0xfe
	v_lshlrev_b32_e32 v25, 3, v23
	v_lshl_or_b32 v23, v23, 12, v21
	v_bitop3_b32 v18, v18, v159, v158 bitop3:0x36
	v_bitop3_b32 v19, s5, v19, v1 bitop3:0x36
	s_lshl_b32 s31, s7, 12
	s_and_b32 s0, s0, 0xe00
	s_movk_i32 s1, 0x2000
	v_and_b32_e32 v22, 0x100, v0
	v_lshl_or_b32 v168, v18, 4, v23
	v_lshlrev_b32_e32 v18, 4, v19
	s_or_b32 s0, s31, s0
	v_add3_u32 v170, v23, v18, s1
	v_or_b32_e32 v18, s0, v22
	v_or_b32_e32 v18, s11, v18
	s_movk_i32 s26, 0x600
	v_add_u32_e32 v18, v161, v18
	v_mul_u32_u24_e32 v18, s26, v18
	v_and_b32_e32 v20, 0xffff, v24
	v_lshl_or_b32 v18, s4, 8, v18
	v_lshlrev_b32_e32 v160, 9, v158
	v_bitop3_b32 v20, s5, v20, v1 bitop3:0x36
	v_lshl_or_b32 v18, v1, 4, v18
	v_add_u32_e32 v164, -1, v162
	v_add_u32_e32 v165, 4, v162
	v_or3_b32 v166, v161, v25, 8
	v_or_b32_e32 v167, 0x1000, v23
	v_lshl_or_b32 v169, v20, 4, v160
	s_and_b32 s17, s17, 0xffff
	s_mov_b32 s19, 0x20000
	s_mov_b32 s18, 0x1800000
	v_add_u32_e32 v171, 0xfffe7c00, v18
	s_mov_b32 s33, s11
	s_mov_b32 s93, 0
	s_branch .LBB3_7

.LBB3_82:
	s_setprio 0
	s_mul_i32 s0, s9, s3
	s_lshl_b32 s1, s30, 6
	s_add_i32 s0, s0, s8
	s_or_b32 s1, s1, s31
	s_or_b32 s7, s1, s11
	s_mul_i32 s4, s0, 0x60000
	s_mul_hi_i32 s1, s0, 0x60000
	s_waitcnt lgkmcnt(0)
	s_add_u32 s6, s12, s4
	s_mulk_i32 s0, 0x300
	s_addc_u32 s8, s13, s1
	s_ashr_i32 s1, s0, 31
	s_lshl_b64 s[0:1], s[0:1], 2
	s_add_u32 s4, s14, s0
	s_addc_u32 s5, s15, s1
	s_mul_i32 s0, s2, 0x1800000
	s_mul_hi_u32 s1, s3, 0x1800000
	s_add_i32 s1, s1, s0
	s_mul_i32 s0, s3, 0x1800000
	s_add_u32 s0, s20, s0
	v_readfirstlane_b32 s2, v0
	s_addc_u32 s1, s21, s1
	s_lshr_b32 s9, s2, 6
	s_and_b32 s1, s1, 0xffff
	s_mul_i32 s2, s9, 0x6000
	v_and_b32_e32 v2, 63, v0
	s_mul_hi_u32 s3, s9, 0x6000
	s_add_u32 s2, s6, s2
	s_addc_u32 s3, s8, s3
	v_lshlrev_b32_e32 v82, 4, v2
	v_mov_b32_e32 v83, 0
	v_lshl_add_u64 v[118:119], s[2:3], 0, v[82:83]
	s_movk_i32 s6, 0x1000
	v_add_co_u32_e32 v50, vcc, s6, v118
	s_movk_i32 s6, 0x2000
	s_nop 0
	v_addc_co_u32_e32 v51, vcc, 0, v119, vcc
	v_add_co_u32_e32 v52, vcc, s6, v118
	global_load_dwordx4 v[2:5], v82, s[2:3] offset:1024
	global_load_dwordx4 v[6:9], v82, s[2:3] offset:2048
	v_addc_co_u32_e32 v53, vcc, 0, v119, vcc
	global_load_dwordx4 v[10:13], v82, s[2:3] offset:3072
	global_load_dwordx4 v[14:17], v[52:53], off offset:-4096
	global_load_dwordx4 v[18:21], v[50:51], off offset:1024
	global_load_dwordx4 v[22:25], v[50:51], off offset:2048
	global_load_dwordx4 v[26:29], v82, s[2:3]
	global_load_dwordx4 v[30:33], v[50:51], off offset:3072
	global_load_dwordx4 v[34:37], v[52:53], off
	global_load_dwordx4 v[38:41], v[52:53], off offset:1024
	global_load_dwordx4 v[42:45], v[52:53], off offset:2048
	global_load_dwordx4 v[46:49], v[52:53], off offset:3072
	s_movk_i32 s2, 0x3000
	v_add_co_u32_e32 v116, vcc, s2, v118
	s_movk_i32 s2, 0x4000
	s_nop 0
	v_addc_co_u32_e32 v117, vcc, 0, v119, vcc
	v_add_co_u32_e32 v156, vcc, s2, v118
	s_nop 1
	v_addc_co_u32_e32 v157, vcc, 0, v119, vcc
	s_barrier
	global_load_dwordx4 v[50:53], v[156:157], off offset:-4096
	global_load_dwordx4 v[54:57], v[116:117], off offset:1024
	global_load_dwordx4 v[58:61], v[116:117], off offset:2048
	v_mul_u32_u24_e32 v62, 0x556, v0
	v_lshlrev_b32_e32 v132, 9, v1
	v_lshrrev_b32_e32 v142, 16, v62
	v_xor_b32_e32 v62, v158, v1
	v_lshl_or_b32 v135, v62, 4, v132
	ds_read_b128 v[62:65], v135
	ds_read_b128 v[66:69], v135 offset:8192
	ds_read_b128 v[70:73], v135 offset:16384
	ds_read_b128 v[74:77], v135 offset:24576
	ds_read_b128 v[78:81], v135 offset:32768
	ds_read_b128 v[84:87], v135 offset:40960
	ds_read_b128 v[88:91], v135 offset:49152
	ds_read_b128 v[92:95], v135 offset:57344
	s_mul_i32 s6, s9, 48
	v_lshl_or_b32 v82, v158, 2, s6
	s_mul_i32 s6, s9, 0x60
	s_add_i32 s6, s6, 0x10000
	v_lshlrev_b32_e32 v96, 3, v142
	s_movk_i32 s9, 0x47
	v_lshl_or_b32 v248, v158, 3, s6
	s_or_b32 s6, s7, 8
	v_bitop3_b32 v143, v96, s9, v142 bitop3:0xc8
	s_mov_b32 s2, 0x1800000
	s_mov_b32 s3, 0x20000
	s_mov_b32 s8, 0x10000
	v_or_b32_e32 v140, s6, v143
	s_waitcnt vmcnt(8) lgkmcnt(7)
	v_mfma_f32_16x16x32_f16 v[96:99], v[26:29], v[62:65], 0
	s_waitcnt lgkmcnt(6)
	v_mfma_f32_16x16x32_f16 v[100:103], v[26:29], v[66:69], 0
	s_waitcnt lgkmcnt(5)
	v_mfma_f32_16x16x32_f16 v[104:107], v[26:29], v[70:73], 0
	s_waitcnt lgkmcnt(4)
	v_mfma_f32_16x16x32_f16 v[108:111], v[26:29], v[74:77], 0
	s_waitcnt lgkmcnt(3)
	v_mfma_f32_16x16x32_f16 v[112:115], v[26:29], v[78:81], 0
	s_waitcnt lgkmcnt(2)
	v_mfma_f32_16x16x32_f16 v[120:123], v[26:29], v[84:87], 0
	s_waitcnt lgkmcnt(1)
	v_mfma_f32_16x16x32_f16 v[124:127], v[26:29], v[88:91], 0
	s_waitcnt lgkmcnt(0)
	v_mfma_f32_16x16x32_f16 v[26:29], v[26:29], v[92:95], 0
	v_mfma_f32_16x16x32_f16 v[128:131], v[2:5], v[62:65], 0
	v_mfma_f32_16x16x32_f16 v[136:139], v[2:5], v[66:69], 0
	v_mfma_f32_16x16x32_f16 v[144:147], v[2:5], v[70:73], 0
	v_mfma_f32_16x16x32_f16 v[148:151], v[2:5], v[74:77], 0
	v_mfma_f32_16x16x32_f16 v[152:155], v[2:5], v[78:81], 0
	v_mfma_f32_16x16x32_f16 v[160:163], v[2:5], v[84:87], 0
	v_mfma_f32_16x16x32_f16 v[164:167], v[2:5], v[88:91], 0
	v_mfma_f32_16x16x32_f16 v[2:5], v[2:5], v[92:95], 0
	v_mfma_f32_16x16x32_f16 v[62:65], v[6:9], v[62:65], 0
	v_mfma_f32_16x16x32_f16 v[66:69], v[6:9], v[66:69], 0
	v_mfma_f32_16x16x32_f16 v[70:73], v[6:9], v[70:73], 0
	v_mfma_f32_16x16x32_f16 v[74:77], v[6:9], v[74:77], 0
	v_mfma_f32_16x16x32_f16 v[78:81], v[6:9], v[78:81], 0
	v_mfma_f32_16x16x32_f16 v[84:87], v[6:9], v[84:87], 0
	v_mfma_f32_16x16x32_f16 v[88:91], v[6:9], v[88:91], 0
	v_mfma_f32_16x16x32_f16 v[6:9], v[6:9], v[92:95], 0
	global_load_dwordx4 v[92:95], v[116:117], off offset:3072
	global_load_dwordx4 v[168:171], v[156:157], off
	global_load_dwordx4 v[172:175], v[156:157], off offset:1024
	v_bitop3_b32 v116, v158, v1, 4 bitop3:0x36
	v_lshl_or_b32 v133, v116, 4, v132
	ds_read_b128 v[176:179], v133
	ds_read_b128 v[180:183], v133 offset:8192
	ds_read_b128 v[184:187], v133 offset:16384
	ds_read_b128 v[188:191], v133 offset:24576
	ds_read_b128 v[192:195], v133 offset:32768
	ds_read_b128 v[196:199], v133 offset:40960
	ds_read_b128 v[200:203], v133 offset:49152
	ds_read_b128 v[204:207], v133 offset:57344
	s_waitcnt lgkmcnt(7)
	v_mfma_f32_16x16x32_f16 v[96:99], v[10:13], v[176:179], v[96:99]
	s_waitcnt lgkmcnt(6)
	v_mfma_f32_16x16x32_f16 v[100:103], v[10:13], v[180:183], v[100:103]
	s_waitcnt lgkmcnt(5)
	v_mfma_f32_16x16x32_f16 v[104:107], v[10:13], v[184:187], v[104:107]
	s_waitcnt lgkmcnt(4)
	v_mfma_f32_16x16x32_f16 v[108:111], v[10:13], v[188:191], v[108:111]
	s_waitcnt lgkmcnt(3)
	v_mfma_f32_16x16x32_f16 v[112:115], v[10:13], v[192:195], v[112:115]
	s_waitcnt lgkmcnt(2)
	v_mfma_f32_16x16x32_f16 v[120:123], v[10:13], v[196:199], v[120:123]
	s_waitcnt lgkmcnt(1)
	v_mfma_f32_16x16x32_f16 v[124:127], v[10:13], v[200:203], v[124:127]
	s_waitcnt lgkmcnt(0)
	v_mfma_f32_16x16x32_f16 v[10:13], v[10:13], v[204:207], v[26:29]
	v_mfma_f32_16x16x32_f16 v[26:29], v[14:17], v[176:179], v[128:131]
	v_mfma_f32_16x16x32_f16 v[128:131], v[14:17], v[180:183], v[136:139]
	v_mfma_f32_16x16x32_f16 v[136:139], v[14:17], v[184:187], v[144:147]
	v_mfma_f32_16x16x32_f16 v[144:147], v[14:17], v[188:191], v[148:151]
	v_mfma_f32_16x16x32_f16 v[148:151], v[14:17], v[192:195], v[152:155]
	v_mfma_f32_16x16x32_f16 v[152:155], v[14:17], v[196:199], v[160:163]
	v_mfma_f32_16x16x32_f16 v[160:163], v[14:17], v[200:203], v[164:167]
	v_mfma_f32_16x16x32_f16 v[2:5], v[14:17], v[204:207], v[2:5]
	v_mfma_f32_16x16x32_f16 v[14:17], v[18:21], v[176:179], v[62:65]
	v_mfma_f32_16x16x32_f16 v[62:65], v[18:21], v[180:183], v[66:69]
	v_mfma_f32_16x16x32_f16 v[66:69], v[18:21], v[184:187], v[70:73]
	v_mfma_f32_16x16x32_f16 v[70:73], v[18:21], v[188:191], v[74:77]
	v_mfma_f32_16x16x32_f16 v[74:77], v[18:21], v[192:195], v[78:81]
	v_mfma_f32_16x16x32_f16 v[78:81], v[18:21], v[196:199], v[84:87]
	v_mfma_f32_16x16x32_f16 v[84:87], v[18:21], v[200:203], v[88:91]
	v_mfma_f32_16x16x32_f16 v[6:9], v[18:21], v[204:207], v[6:9]
	s_movk_i32 s9, 0x5000
	v_add_co_u32_e32 v116, vcc, s9, v118
	global_load_dwordx4 v[88:91], v[156:157], off offset:2048
	global_load_dwordx4 v[164:167], v[156:157], off offset:3072
	v_addc_co_u32_e32 v117, vcc, 0, v119, vcc
	global_load_dwordx4 v[176:179], v[116:117], off
	v_bitop3_b32 v18, v158, v1, 8 bitop3:0x36
	v_lshl_or_b32 v134, v18, 4, v132
	ds_read_b128 v[18:21], v134
	ds_read_b128 v[180:183], v134 offset:8192
	ds_read_b128 v[184:187], v134 offset:16384
	ds_read_b128 v[188:191], v134 offset:24576
	ds_read_b128 v[192:195], v134 offset:32768
	ds_read_b128 v[196:199], v134 offset:40960
	ds_read_b128 v[200:203], v134 offset:49152
	ds_read_b128 v[204:207], v134 offset:57344
	s_waitcnt lgkmcnt(7)
	v_mfma_f32_16x16x32_f16 v[96:99], v[22:25], v[18:21], v[96:99]
	s_waitcnt lgkmcnt(6)
	v_mfma_f32_16x16x32_f16 v[100:103], v[22:25], v[180:183], v[100:103]
	s_waitcnt lgkmcnt(5)
	v_mfma_f32_16x16x32_f16 v[104:107], v[22:25], v[184:187], v[104:107]
	s_waitcnt lgkmcnt(4)
	v_mfma_f32_16x16x32_f16 v[108:111], v[22:25], v[188:191], v[108:111]
	s_waitcnt lgkmcnt(3)
	v_mfma_f32_16x16x32_f16 v[112:115], v[22:25], v[192:195], v[112:115]
	s_waitcnt lgkmcnt(2)
	v_mfma_f32_16x16x32_f16 v[120:123], v[22:25], v[196:199], v[120:123]
	s_waitcnt lgkmcnt(1)
	v_mfma_f32_16x16x32_f16 v[124:127], v[22:25], v[200:203], v[124:127]
	s_waitcnt lgkmcnt(0)
	v_mfma_f32_16x16x32_f16 v[10:13], v[22:25], v[204:207], v[10:13]
	s_waitcnt vmcnt(13)
	v_mfma_f32_16x16x32_f16 v[22:25], v[30:33], v[18:21], v[26:29]
	v_mfma_f32_16x16x32_f16 v[26:29], v[30:33], v[180:183], v[128:131]
	v_mfma_f32_16x16x32_f16 v[128:131], v[30:33], v[184:187], v[136:139]
	v_mfma_f32_16x16x32_f16 v[144:147], v[30:33], v[188:191], v[144:147]
	v_mfma_f32_16x16x32_f16 v[148:151], v[30:33], v[192:195], v[148:151]
	v_mfma_f32_16x16x32_f16 v[152:155], v[30:33], v[196:199], v[152:155]
	v_mfma_f32_16x16x32_f16 v[160:163], v[30:33], v[200:203], v[160:163]
	v_mfma_f32_16x16x32_f16 v[2:5], v[30:33], v[204:207], v[2:5]
	s_waitcnt vmcnt(12)
	v_mfma_f32_16x16x32_f16 v[14:17], v[34:37], v[18:21], v[14:17]
	v_mfma_f32_16x16x32_f16 v[18:21], v[34:37], v[180:183], v[62:65]
	v_mfma_f32_16x16x32_f16 v[30:33], v[34:37], v[184:187], v[66:69]
	v_mfma_f32_16x16x32_f16 v[62:65], v[34:37], v[188:191], v[70:73]
	v_mfma_f32_16x16x32_f16 v[66:69], v[34:37], v[192:195], v[74:77]
	v_mfma_f32_16x16x32_f16 v[70:73], v[34:37], v[196:199], v[78:81]
	v_mfma_f32_16x16x32_f16 v[74:77], v[34:37], v[200:203], v[84:87]
	v_mfma_f32_16x16x32_f16 v[6:9], v[34:37], v[204:207], v[6:9]
	s_nop 0
	global_load_dwordx4 v[78:81], v[116:117], off offset:1024
	global_load_dwordx4 v[180:183], v[116:117], off offset:2048
	global_load_dwordx4 v[184:187], v[116:117], off offset:3072
	v_bitop3_b32 v34, v158, v1, 12 bitop3:0x36
	v_lshl_or_b32 v136, v34, 4, v132
	ds_read_b128 v[34:37], v136
	ds_read_b128 v[84:87], v136 offset:8192
	ds_read_b128 v[188:191], v136 offset:16384
	ds_read_b128 v[192:195], v136 offset:24576
	ds_read_b128 v[196:199], v136 offset:32768
	ds_read_b128 v[200:203], v136 offset:40960
	ds_read_b128 v[204:207], v136 offset:49152
	ds_read_b128 v[208:211], v136 offset:57344
	s_waitcnt vmcnt(14) lgkmcnt(7)
	v_mfma_f32_16x16x32_f16 v[96:99], v[38:41], v[34:37], v[96:99]
	s_waitcnt lgkmcnt(6)
	v_mfma_f32_16x16x32_f16 v[100:103], v[38:41], v[84:87], v[100:103]
	s_waitcnt lgkmcnt(5)
	v_mfma_f32_16x16x32_f16 v[104:107], v[38:41], v[188:191], v[104:107]
	s_waitcnt lgkmcnt(4)
	v_mfma_f32_16x16x32_f16 v[108:111], v[38:41], v[192:195], v[108:111]
	s_waitcnt lgkmcnt(3)
	v_mfma_f32_16x16x32_f16 v[112:115], v[38:41], v[196:199], v[112:115]
	s_waitcnt lgkmcnt(2)
	v_mfma_f32_16x16x32_f16 v[120:123], v[38:41], v[200:203], v[120:123]
	s_waitcnt lgkmcnt(1)
	v_mfma_f32_16x16x32_f16 v[124:127], v[38:41], v[204:207], v[124:127]
	s_waitcnt lgkmcnt(0)
	v_mfma_f32_16x16x32_f16 v[212:215], v[38:41], v[208:211], v[10:13]
	s_waitcnt vmcnt(13)
	v_mfma_f32_16x16x32_f16 v[22:25], v[42:45], v[34:37], v[22:25]
	v_mfma_f32_16x16x32_f16 v[216:219], v[42:45], v[84:87], v[26:29]
	v_mfma_f32_16x16x32_f16 v[128:131], v[42:45], v[188:191], v[128:131]
	v_mfma_f32_16x16x32_f16 v[144:147], v[42:45], v[192:195], v[144:147]
	v_mfma_f32_16x16x32_f16 v[148:151], v[42:45], v[196:199], v[148:151]
	v_mfma_f32_16x16x32_f16 v[152:155], v[42:45], v[200:203], v[152:155]
	v_mfma_f32_16x16x32_f16 v[160:163], v[42:45], v[204:207], v[160:163]
	v_mfma_f32_16x16x32_f16 v[2:5], v[42:45], v[208:211], v[2:5]
	s_waitcnt vmcnt(12)
	v_mfma_f32_16x16x32_f16 v[14:17], v[46:49], v[34:37], v[14:17]
	v_mfma_f32_16x16x32_f16 v[18:21], v[46:49], v[84:87], v[18:21]
	v_mfma_f32_16x16x32_f16 v[30:33], v[46:49], v[188:191], v[30:33]
	v_mfma_f32_16x16x32_f16 v[34:37], v[46:49], v[192:195], v[62:65]
	v_mfma_f32_16x16x32_f16 v[42:45], v[46:49], v[196:199], v[66:69]
	v_mfma_f32_16x16x32_f16 v[62:65], v[46:49], v[200:203], v[70:73]
	v_mfma_f32_16x16x32_f16 v[66:69], v[46:49], v[204:207], v[74:77]
	v_mfma_f32_16x16x32_f16 v[6:9], v[46:49], v[208:211], v[6:9]
	s_mov_b32 s9, 0x30000
	v_add_co_u32_e32 v116, vcc, s9, v118
	s_mov_b32 s9, 0x31000
	s_nop 0
	v_addc_co_u32_e32 v117, vcc, 0, v119, vcc
	v_add_co_u32_e32 v156, vcc, s9, v118
	v_bitop3_b32 v46, v158, v1, 16 bitop3:0x36
	s_nop 0
	v_addc_co_u32_e32 v157, vcc, 0, v119, vcc
	global_load_dwordx4 v[38:41], v[156:157], off offset:-4096
	global_load_dwordx4 v[26:29], v[116:117], off offset:1024
	global_load_dwordx4 v[10:13], v[116:117], off offset:2048
	v_lshl_or_b32 v137, v46, 4, v132
	ds_read_b128 v[46:49], v137
	ds_read_b128 v[70:73], v137 offset:8192
	ds_read_b128 v[74:77], v137 offset:16384
	ds_read_b128 v[84:87], v137 offset:24576
	ds_read_b128 v[188:191], v137 offset:32768
	ds_read_b128 v[192:195], v137 offset:40960
	ds_read_b128 v[196:199], v137 offset:49152
	ds_read_b128 v[200:203], v137 offset:57344
	s_waitcnt vmcnt(14) lgkmcnt(7)
	v_mfma_f32_16x16x32_f16 v[96:99], v[50:53], v[46:49], v[96:99]
	s_waitcnt lgkmcnt(6)
	v_mfma_f32_16x16x32_f16 v[100:103], v[50:53], v[70:73], v[100:103]
	s_waitcnt lgkmcnt(5)
	v_mfma_f32_16x16x32_f16 v[104:107], v[50:53], v[74:77], v[104:107]
	s_waitcnt lgkmcnt(4)
	v_mfma_f32_16x16x32_f16 v[108:111], v[50:53], v[84:87], v[108:111]
	s_waitcnt lgkmcnt(3)
	v_mfma_f32_16x16x32_f16 v[112:115], v[50:53], v[188:191], v[112:115]
	s_waitcnt lgkmcnt(2)
	v_mfma_f32_16x16x32_f16 v[120:123], v[50:53], v[192:195], v[120:123]
	s_waitcnt lgkmcnt(1)
	v_mfma_f32_16x16x32_f16 v[124:127], v[50:53], v[196:199], v[124:127]
	s_waitcnt lgkmcnt(0)
	v_mfma_f32_16x16x32_f16 v[50:53], v[50:53], v[200:203], v[212:215]
	s_waitcnt vmcnt(13)
	v_mfma_f32_16x16x32_f16 v[204:207], v[54:57], v[46:49], v[22:25]
	v_mfma_f32_16x16x32_f16 v[208:211], v[54:57], v[70:73], v[216:219]
	v_mfma_f32_16x16x32_f16 v[128:131], v[54:57], v[74:77], v[128:131]
	v_mfma_f32_16x16x32_f16 v[144:147], v[54:57], v[84:87], v[144:147]
	v_mfma_f32_16x16x32_f16 v[148:151], v[54:57], v[188:191], v[148:151]
	v_mfma_f32_16x16x32_f16 v[152:155], v[54:57], v[192:195], v[152:155]
	v_mfma_f32_16x16x32_f16 v[160:163], v[54:57], v[196:199], v[160:163]
	v_mfma_f32_16x16x32_f16 v[54:57], v[54:57], v[200:203], v[2:5]
	s_waitcnt vmcnt(12)
	v_mfma_f32_16x16x32_f16 v[14:17], v[58:61], v[46:49], v[14:17]
	v_mfma_f32_16x16x32_f16 v[18:21], v[58:61], v[70:73], v[18:21]
	v_mfma_f32_16x16x32_f16 v[30:33], v[58:61], v[74:77], v[30:33]
	v_mfma_f32_16x16x32_f16 v[34:37], v[58:61], v[84:87], v[34:37]
	v_mfma_f32_16x16x32_f16 v[42:45], v[58:61], v[188:191], v[42:45]
	v_mfma_f32_16x16x32_f16 v[46:49], v[58:61], v[192:195], v[62:65]
	v_mfma_f32_16x16x32_f16 v[62:65], v[58:61], v[196:199], v[66:69]
	v_mfma_f32_16x16x32_f16 v[58:61], v[58:61], v[200:203], v[6:9]
	global_load_dwordx4 v[22:25], v[116:117], off offset:3072
	s_nop 1
	global_load_dwordx4 v[6:9], v[156:157], off
	global_load_dwordx4 v[2:5], v[156:157], off offset:1024
	v_bitop3_b32 v66, v158, v1, 20 bitop3:0x36
	v_lshl_or_b32 v138, v66, 4, v132
	ds_read_b128 v[66:69], v138
	ds_read_b128 v[70:73], v138 offset:8192
	ds_read_b128 v[74:77], v138 offset:16384
	ds_read_b128 v[84:87], v138 offset:24576
	ds_read_b128 v[188:191], v138 offset:32768
	ds_read_b128 v[192:195], v138 offset:40960
	ds_read_b128 v[196:199], v138 offset:49152
	ds_read_b128 v[200:203], v138 offset:57344
	s_waitcnt vmcnt(14) lgkmcnt(7)
	v_mfma_f32_16x16x32_f16 v[96:99], v[92:95], v[66:69], v[96:99]
	s_waitcnt lgkmcnt(6)
	v_mfma_f32_16x16x32_f16 v[100:103], v[92:95], v[70:73], v[100:103]
	s_waitcnt lgkmcnt(5)
	v_mfma_f32_16x16x32_f16 v[104:107], v[92:95], v[74:77], v[104:107]
	s_waitcnt lgkmcnt(4)
	v_mfma_f32_16x16x32_f16 v[108:111], v[92:95], v[84:87], v[108:111]
	s_waitcnt lgkmcnt(3)
	v_mfma_f32_16x16x32_f16 v[112:115], v[92:95], v[188:191], v[112:115]
	s_waitcnt lgkmcnt(2)
	v_mfma_f32_16x16x32_f16 v[212:215], v[92:95], v[192:195], v[120:123]
	s_waitcnt lgkmcnt(1)
	v_mfma_f32_16x16x32_f16 v[124:127], v[92:95], v[196:199], v[124:127]
	s_waitcnt lgkmcnt(0)
	v_mfma_f32_16x16x32_f16 v[50:53], v[92:95], v[200:203], v[50:53]
	s_waitcnt vmcnt(13)
	v_mfma_f32_16x16x32_f16 v[92:95], v[168:171], v[66:69], v[204:207]
	v_mfma_f32_16x16x32_f16 v[204:207], v[168:171], v[70:73], v[208:211]
	v_mfma_f32_16x16x32_f16 v[128:131], v[168:171], v[74:77], v[128:131]
	v_mfma_f32_16x16x32_f16 v[144:147], v[168:171], v[84:87], v[144:147]
	v_mfma_f32_16x16x32_f16 v[148:151], v[168:171], v[188:191], v[148:151]
	v_mfma_f32_16x16x32_f16 v[152:155], v[168:171], v[192:195], v[152:155]
	v_mfma_f32_16x16x32_f16 v[160:163], v[168:171], v[196:199], v[160:163]
	v_mfma_f32_16x16x32_f16 v[54:57], v[168:171], v[200:203], v[54:57]
	s_waitcnt vmcnt(12)
	v_mfma_f32_16x16x32_f16 v[66:69], v[172:175], v[66:69], v[14:17]
	v_mfma_f32_16x16x32_f16 v[70:73], v[172:175], v[70:73], v[18:21]
	v_mfma_f32_16x16x32_f16 v[74:77], v[172:175], v[74:77], v[30:33]
	v_mfma_f32_16x16x32_f16 v[34:37], v[172:175], v[84:87], v[34:37]
	v_mfma_f32_16x16x32_f16 v[42:45], v[172:175], v[188:191], v[42:45]
	v_mfma_f32_16x16x32_f16 v[46:49], v[172:175], v[192:195], v[46:49]
	v_mfma_f32_16x16x32_f16 v[62:65], v[172:175], v[196:199], v[62:65]
	v_mfma_f32_16x16x32_f16 v[58:61], v[172:175], v[200:203], v[58:61]
	s_mov_b32 s9, 0x33000
	v_add_co_u32_e32 v122, vcc, s9, v118
	global_load_dwordx4 v[30:33], v[156:157], off offset:2048
	global_load_dwordx4 v[14:17], v[156:157], off offset:3072
	v_addc_co_u32_e32 v123, vcc, 0, v119, vcc
	global_load_dwordx4 v[18:21], v[122:123], off offset:-4096
	v_bitop3_b32 v84, v158, v1, 24 bitop3:0x36
	v_lshl_or_b32 v139, v84, 4, v132
	ds_read_b128 v[84:87], v139
	ds_read_b128 v[168:171], v139 offset:8192
	ds_read_b128 v[172:175], v139 offset:16384
	ds_read_b128 v[188:191], v139 offset:24576
	ds_read_b128 v[192:195], v139 offset:32768
	ds_read_b128 v[196:199], v139 offset:40960
	ds_read_b128 v[200:203], v139 offset:49152
	ds_read_b128 v[208:211], v139 offset:57344
	s_mov_b32 s9, 0x32000
	v_add_co_u32_e32 v116, vcc, s9, v118
	s_nop 1
	v_addc_co_u32_e32 v117, vcc, 0, v119, vcc
	s_waitcnt vmcnt(14) lgkmcnt(7)
	v_mfma_f32_16x16x32_f16 v[96:99], v[88:91], v[84:87], v[96:99]
	s_waitcnt lgkmcnt(6)
	v_mfma_f32_16x16x32_f16 v[100:103], v[88:91], v[168:171], v[100:103]
	s_waitcnt lgkmcnt(5)
	v_mfma_f32_16x16x32_f16 v[104:107], v[88:91], v[172:175], v[104:107]
	s_waitcnt lgkmcnt(4)
	v_mfma_f32_16x16x32_f16 v[108:111], v[88:91], v[188:191], v[108:111]
	s_waitcnt lgkmcnt(3)
	v_mfma_f32_16x16x32_f16 v[112:115], v[88:91], v[192:195], v[112:115]
	s_waitcnt lgkmcnt(2)
	v_mfma_f32_16x16x32_f16 v[212:215], v[88:91], v[196:199], v[212:215]
	s_waitcnt lgkmcnt(1)
	v_mfma_f32_16x16x32_f16 v[124:127], v[88:91], v[200:203], v[124:127]
	s_waitcnt lgkmcnt(0)
	v_mfma_f32_16x16x32_f16 v[50:53], v[88:91], v[208:211], v[50:53]
	s_waitcnt vmcnt(13)
	v_mfma_f32_16x16x32_f16 v[90:93], v[164:167], v[84:87], v[92:95]
	v_mfma_f32_16x16x32_f16 v[204:207], v[164:167], v[168:171], v[204:207]
	v_mfma_f32_16x16x32_f16 v[128:131], v[164:167], v[172:175], v[128:131]
	v_mfma_f32_16x16x32_f16 v[144:147], v[164:167], v[188:191], v[144:147]
	v_mfma_f32_16x16x32_f16 v[148:151], v[164:167], v[192:195], v[148:151]
	v_mfma_f32_16x16x32_f16 v[152:155], v[164:167], v[196:199], v[152:155]
	v_mfma_f32_16x16x32_f16 v[160:163], v[164:167], v[200:203], v[160:163]
	v_mfma_f32_16x16x32_f16 v[54:57], v[164:167], v[208:211], v[54:57]
	s_waitcnt vmcnt(12)
	v_mfma_f32_16x16x32_f16 v[164:167], v[176:179], v[84:87], v[66:69]
	v_mfma_f32_16x16x32_f16 v[168:171], v[176:179], v[168:171], v[70:73]
	v_mfma_f32_16x16x32_f16 v[172:175], v[176:179], v[172:175], v[74:77]
	v_mfma_f32_16x16x32_f16 v[188:191], v[176:179], v[188:191], v[34:37]
	v_mfma_f32_16x16x32_f16 v[192:195], v[176:179], v[192:195], v[42:45]
	v_mfma_f32_16x16x32_f16 v[196:199], v[176:179], v[196:199], v[46:49]
	v_mfma_f32_16x16x32_f16 v[200:203], v[176:179], v[200:203], v[62:65]
	v_mfma_f32_16x16x32_f16 v[176:179], v[176:179], v[208:211], v[58:61]
	s_nop 0
	global_load_dwordx4 v[46:49], v[116:117], off offset:1024
	global_load_dwordx4 v[42:45], v[116:117], off offset:2048
	global_load_dwordx4 v[34:37], v[116:117], off offset:3072
	v_bitop3_b32 v58, v158, v1, 28 bitop3:0x36
	v_lshl_or_b32 v141, v58, 4, v132
	ds_read_b128 v[58:61], v141
	ds_read_b128 v[62:65], v141 offset:8192
	ds_read_b128 v[156:159], v141 offset:16384
	ds_read_b128 v[208:211], v141 offset:24576
	ds_read_b128 v[216:219], v141 offset:32768
	ds_read_b128 v[220:223], v141 offset:40960
	ds_read_b128 v[224:227], v141 offset:49152
	ds_read_b128 v[228:231], v141 offset:57344
	s_waitcnt vmcnt(14) lgkmcnt(7)
	v_mfma_f32_16x16x32_f16 v[232:235], v[78:81], v[58:61], v[96:99]
	s_waitcnt lgkmcnt(6)
	v_mfma_f32_16x16x32_f16 v[236:239], v[78:81], v[62:65], v[100:103]
	s_waitcnt lgkmcnt(5)
	v_mfma_f32_16x16x32_f16 v[240:243], v[78:81], v[156:159], v[104:107]
	s_waitcnt lgkmcnt(4)
	v_mfma_f32_16x16x32_f16 v[244:247], v[78:81], v[208:211], v[108:111]
	s_waitcnt lgkmcnt(3)
	v_mfma_f32_16x16x32_f16 v[106:109], v[78:81], v[216:219], v[112:115]
	s_waitcnt lgkmcnt(2)
	v_mfma_f32_16x16x32_f16 v[102:105], v[78:81], v[220:223], v[212:215]
	s_waitcnt lgkmcnt(1)
	v_mfma_f32_16x16x32_f16 v[94:97], v[78:81], v[224:227], v[124:127]
	s_waitcnt lgkmcnt(0)
	v_mfma_f32_16x16x32_f16 v[86:89], v[78:81], v[228:231], v[50:53]
	s_waitcnt vmcnt(13)
	v_mfma_f32_16x16x32_f16 v[124:127], v[180:183], v[58:61], v[90:93]
	v_mfma_f32_16x16x32_f16 v[204:207], v[180:183], v[62:65], v[204:207]
	v_mfma_f32_16x16x32_f16 v[212:215], v[180:183], v[156:159], v[128:131]
	v_mfma_f32_16x16x32_f16 v[144:147], v[180:183], v[208:211], v[144:147]
	v_mfma_f32_16x16x32_f16 v[78:81], v[180:183], v[216:219], v[148:151]
	v_mfma_f32_16x16x32_f16 v[74:77], v[180:183], v[220:223], v[152:155]
	v_mfma_f32_16x16x32_f16 v[70:73], v[180:183], v[224:227], v[160:163]
	v_mfma_f32_16x16x32_f16 v[66:69], v[180:183], v[228:231], v[54:57]
	s_waitcnt vmcnt(12)
	v_mfma_f32_16x16x32_f16 v[148:151], v[184:187], v[58:61], v[164:167]
	v_mfma_f32_16x16x32_f16 v[152:155], v[184:187], v[62:65], v[168:171]
	v_mfma_f32_16x16x32_f16 v[114:117], v[184:187], v[156:159], v[172:175]
	v_mfma_f32_16x16x32_f16 v[110:113], v[184:187], v[208:211], v[188:191]
	v_mfma_f32_16x16x32_f16 v[62:65], v[184:187], v[216:219], v[192:195]
	v_mfma_f32_16x16x32_f16 v[58:61], v[184:187], v[220:223], v[196:199]
	v_mfma_f32_16x16x32_f16 v[54:57], v[184:187], v[224:227], v[200:203]
	v_mfma_f32_16x16x32_f16 v[50:53], v[184:187], v[228:231], v[176:179]
	v_lshl_add_u64 v[120:121], v[82:83], 2, s[4:5]
	global_load_dwordx4 v[98:101], v[120:121], off
	global_load_dwordx4 v[90:93], v[120:121], off offset:64
	global_load_dwordx4 v[82:85], v[120:121], off offset:128
	s_movk_i32 s4, 0x310
	v_mad_u32_u24 v130, v1, s4, v248
	v_mov_b32_e32 v156, v237
	v_mov_b32_e32 v157, v238
	v_mov_b32_e32 v158, v241
	v_mov_b32_e32 v159, v242
	v_mov_b32_e32 v160, v245
	v_mov_b32_e32 v161, v246
	v_mov_b32_e32 v162, v205
	v_mov_b32_e32 v163, v206
	v_mov_b32_e32 v167, v146
	v_mov_b32_e32 v164, v213
	v_mov_b32_e32 v165, v214
	v_mov_b32_e32 v166, v145
	s_barrier
	v_add_u32_e32 v132, 0x3000, v130
	v_add_u32_e32 v131, 0x6000, v130
	s_mov_b32 s5, 0xfffffd0
	v_mul_i32_i24_e32 v174, s5, v142
	s_movk_i32 s4, 0x600
	s_movk_i32 s9, 0xc7
	s_waitcnt vmcnt(2)
	v_pk_add_f32 v[168:169], v[232:233], v[98:99]
	v_pk_add_f32 v[170:171], v[234:235], v[100:101]
	v_add_f32_e32 v1, v236, v98
	v_pk_mov_b32 v[128:129], v[98:99], v[100:101] op_sel:[1,0]
	v_add_f32_e32 v99, v239, v101
	s_waitcnt vmcnt(1)
	v_pk_add_f32 v[124:125], v[124:125], v[90:91]
	v_pk_add_f32 v[172:173], v[126:127], v[92:93]
	v_add_f32_e32 v178, v204, v90
	v_pk_mov_b32 v[126:127], v[90:91], v[92:93] op_sel:[1,0]
	v_add_f32_e32 v91, v207, v93
	v_add_f32_e32 v100, v240, v98
	v_add_f32_e32 v175, v243, v101
	v_add_f32_e32 v92, v212, v90
	v_add_f32_e32 v179, v215, v93
	v_add_f32_e32 v181, v147, v93
	v_cvt_pk_f16_f32 v147, v170, v171
	v_cvt_f16_f32_e32 v1, v1
	v_cvt_f16_f32_e32 v99, v99
	v_cvt_f16_f32_e32 v171, v178
	v_cvt_f16_f32_e32 v91, v91
	v_cvt_pk_f16_f32 v146, v168, v169
	v_cvt_f16_f32_e32 v100, v100
	v_cvt_f16_f32_e32 v168, v175
	v_cvt_pk_f16_f32 v124, v124, v125
	v_cvt_pk_f16_f32 v125, v172, v173
	v_cvt_f16_f32_e32 v92, v92
	v_cvt_f16_f32_e32 v172, v179
	v_add_f32_e32 v180, v144, v90
	s_waitcnt vmcnt(0)
	v_pk_add_f32 v[144:145], v[148:149], v[82:83]
	v_pk_add_f32 v[148:149], v[156:157], v[128:129]
	v_pk_add_f32 v[156:157], v[158:159], v[128:129]
	v_pk_add_f32 v[158:159], v[160:161], v[128:129]
	v_pk_add_f32 v[160:161], v[162:163], v[126:127]
	v_pk_add_f32 v[162:163], v[164:165], v[126:127]
	v_cvt_pk_f16_f32 v144, v144, v145
	v_cvt_pk_f16_f32 v145, v148, v149
	v_cvt_pk_f16_f32 v148, v156, v157
	v_cvt_pk_f16_f32 v157, v160, v161
	v_cvt_pk_f16_f32 v149, v158, v159
	v_cvt_pk_f16_f32 v159, v162, v163
	ds_write2_b64 v130, v[146:147], v[124:125] offset1:4
	v_pack_b32_f16 v124, v1, v145
	v_alignbit_b32 v125, v99, v145, 16
	v_pack_b32_f16 v156, v171, v157
	v_alignbit_b32 v157, v91, v157, 16
	v_pack_b32_f16 v146, v100, v148
	v_alignbit_b32 v147, v168, v148, 16
	v_pack_b32_f16 v158, v92, v159
	v_alignbit_b32 v159, v172, v159, 16
	ds_write2_b64 v132, v[124:125], v[156:157] offset0:32 offset1:36
	ds_write2_b64 v131, v[146:147], v[158:159] offset0:64 offset1:68
	v_pk_add_f32 v[124:125], v[150:151], v[84:85]
	v_add_f32_e32 v1, v152, v82
	v_cvt_pk_f16_f32 v145, v124, v125
	v_pk_mov_b32 v[124:125], v[82:83], v[84:85] op_sel:[1,0]
	v_add_f32_e32 v83, v155, v85
	v_cvt_f16_f32_e32 v1, v1
	v_cvt_f16_f32_e32 v83, v83
	ds_write_b64 v130, v[144:145] offset:64
	v_mov_b32_e32 v144, v153
	v_mov_b32_e32 v145, v154
	v_pk_add_f32 v[144:145], v[144:145], v[124:125]
	v_add_f32_e32 v176, v244, v98
	v_cvt_pk_f16_f32 v84, v144, v145
	v_pack_b32_f16 v144, v1, v84
	v_alignbit_b32 v145, v83, v84, 16
	v_add_f32_e32 v1, v114, v82
	v_add_f32_e32 v83, v117, v85
	v_cvt_f16_f32_e32 v1, v1
	v_cvt_f16_f32_e32 v83, v83
	v_mov_b32_e32 v114, v115
	v_mov_b32_e32 v115, v116
	v_pk_add_f32 v[114:115], v[114:115], v[124:125]
	v_add_f32_e32 v177, v247, v101
	v_cvt_pk_f16_f32 v84, v114, v115
	v_pack_b32_f16 v114, v1, v84
	v_alignbit_b32 v115, v83, v84, 16
	v_add_f32_e32 v1, v110, v82
	v_add_f32_e32 v83, v113, v85
	v_cvt_f16_f32_e32 v1, v1
	v_cvt_f16_f32_e32 v83, v83
	v_mov_b32_e32 v110, v111
	v_mov_b32_e32 v111, v112
	v_cvt_f16_f32_e32 v169, v176
	v_cvt_f16_f32_e32 v170, v177
	v_cvt_f16_f32_e32 v173, v180
	v_pk_add_f32 v[164:165], v[166:167], v[126:127]
	v_cvt_f16_f32_e32 v166, v181
	v_pk_add_f32 v[110:111], v[110:111], v[124:125]
	v_cvt_pk_f16_f32 v161, v164, v165
	v_cvt_pk_f16_f32 v84, v110, v111
	v_pack_b32_f16 v110, v1, v84
	v_alignbit_b32 v111, v83, v84, 16
	ds_write_b64 v130, v[110:111] offset:37696
	v_add_lshl_u32 v111, v174, v0, 4
	v_mul_u32_u24_e32 v83, 0x310, v142
	v_pack_b32_f16 v148, v169, v149
	v_alignbit_b32 v149, v170, v149, 16
	v_pack_b32_f16 v160, v173, v161
	v_alignbit_b32 v161, v166, v161, 16
	v_add_u32_e32 v91, 0x9000, v130
	v_add3_u32 v83, v111, v83, s8
	v_or_b32_e32 v84, 0x200, v0
	ds_write2_b64 v91, v[148:149], v[160:161] offset0:96 offset1:100
	ds_write_b64 v130, v[144:145] offset:12608
	ds_write_b64 v130, v[114:115] offset:25152
	s_waitcnt lgkmcnt(0)
	s_barrier
	ds_read_b128 v[114:117], v83
	v_mul_u32_u24_e32 v92, 0x556, v84
	v_lshrrev_b32_e32 v92, 16, v92
	v_or_b32_e32 v1, s7, v143
	v_mul_i32_i24_e32 v99, s5, v92
	v_mul_u32_u24_e32 v112, s4, v1
	v_add_lshl_u32 v113, v99, v84, 4
	v_mul_u32_u24_e32 v84, 0x310, v92
	v_add_u32_e32 v1, v112, v111
	v_add3_u32 v84, v113, v84, s8
	ds_read_b128 v[142:145], v84
	s_waitcnt lgkmcnt(1)
	buffer_store_dwordx4 v[114:117], v1, s[0:3], 0 offen sc1
	v_lshlrev_b32_e32 v1, 3, v92
	v_bitop3_b32 v154, v1, s9, v92 bitop3:0xc8
	v_or_b32_e32 v1, s7, v154
	v_mul_u32_u24_e32 v114, s4, v1
	v_add_u32_e32 v1, v114, v113
	s_waitcnt lgkmcnt(0)
	buffer_store_dwordx4 v[142:145], v1, s[0:3], 0 offen sc1
	v_or_b32_e32 v1, 0x400, v0
	v_mul_u32_u24_e32 v92, 0x556, v1
	v_lshrrev_b32_e32 v92, 16, v92
	v_mul_i32_i24_e32 v99, s5, v92
	v_lshlrev_b32_e32 v100, 3, v92
	s_movk_i32 s9, 0x1c7
	v_bitop3_b32 v155, v100, s9, v92 bitop3:0xc8
	v_add_lshl_u32 v115, v99, v1, 4
	v_mul_u32_u24_e32 v92, 0x310, v92
	v_or_b32_e32 v100, s7, v155
	v_add3_u32 v92, v115, v92, s8
	v_or_b32_e32 v99, 0x600, v0
	v_mul_u32_u24_e32 v116, s4, v100
	ds_read_b128 v[142:145], v92
	v_mul_u32_u24_e32 v100, 0x556, v99
	v_lshrrev_b32_e32 v100, 16, v100
	v_mul_i32_i24_e32 v110, s5, v100
	v_add_lshl_u32 v117, v110, v99, 4
	v_mul_u32_u24_e32 v99, 0x310, v100
	v_add_u32_e32 v1, v116, v115
	v_add3_u32 v99, v117, v99, s8
	ds_read_b128 v[146:149], v99
	s_waitcnt lgkmcnt(1)
	buffer_store_dwordx4 v[142:145], v1, s[0:3], 0 offen sc1
	v_lshlrev_b32_e32 v1, 3, v100
	v_bitop3_b32 v156, v1, s9, v100 bitop3:0xc8
	v_add_u32_e32 v1, s7, v156
	v_mul_u32_u24_e32 v142, s4, v1
	v_add_u32_e32 v1, v142, v117
	s_waitcnt lgkmcnt(0)
	buffer_store_dwordx4 v[146:149], v1, s[0:3], 0 offen sc1
	v_or_b32_e32 v1, 0x800, v0
	v_mul_u32_u24_e32 v100, 0xaab, v1
	v_lshrrev_b32_e32 v100, 17, v100
	v_mul_i32_i24_e32 v110, s5, v100
	v_lshlrev_b32_e32 v143, 3, v100
	v_bitop3_b32 v157, v143, s9, v100 bitop3:0xc8
	v_add_lshl_u32 v144, v110, v1, 4
	v_mul_u32_u24_e32 v100, 0x310, v100
	v_or_b32_e32 v0, 0xa00, v0
	v_add3_u32 v100, v100, v144, s8
	v_mul_u32_u24_e32 v110, 0xaab, v0
	ds_read_b128 v[146:149], v100
	v_lshrrev_b32_e32 v158, 17, v110
	v_mul_i32_i24_e32 v110, s5, v158
	v_or_b32_e32 v143, s7, v157
	v_add_lshl_u32 v145, v110, v0, 4
	v_mul_u32_u24_e32 v0, 0x310, v158
	v_mul_u32_u24_e32 v143, s4, v143
	v_add3_u32 v110, v0, v145, s8
	v_add_u32_e32 v1, v143, v144
	ds_read_b128 v[150:153], v110
	v_lshlrev_b32_e32 v0, 3, v158
	s_movk_i32 s5, 0x3c7
	s_waitcnt lgkmcnt(1)
	buffer_store_dwordx4 v[146:149], v1, s[0:3], 0 offen sc1
	v_mov_b32_e32 v1, v108
	v_add_f32_e32 v102, v102, v98
	v_bitop3_b32 v147, v0, s5, v158 bitop3:0xc8
	v_add_u32_e32 v0, s7, v147
	v_mul_u32_u24_e32 v146, s4, v0
	v_add_u32_e32 v0, v146, v145
	s_waitcnt lgkmcnt(0)
	buffer_store_dwordx4 v[150:153], v0, s[0:3], 0 offen sc1
	v_add_f32_e32 v0, v106, v98
	v_cvt_f16_f32_e32 v106, v0
	v_mov_b32_e32 v0, v107
	v_pk_add_f32 v[0:1], v[0:1], v[128:129]
	v_add_f32_e32 v94, v94, v98
	v_cvt_pk_f16_f32 v1, v0, v1
	v_pack_b32_f16 v0, v106, v1
	v_cvt_f16_f32_e32 v106, v102
	v_mov_b32_e32 v102, v103
	v_mov_b32_e32 v103, v104
	v_add_f32_e32 v104, v105, v101
	v_cvt_f16_f32_e32 v104, v104
	v_pk_add_f32 v[102:103], v[102:103], v[128:129]
	v_add_f32_e32 v86, v86, v98
	v_cvt_pk_f16_f32 v103, v102, v103
	v_pack_b32_f16 v102, v106, v103
	v_alignbit_b32 v103, v104, v103, 16
	v_cvt_f16_f32_e32 v104, v94
	v_mov_b32_e32 v94, v95
	v_mov_b32_e32 v95, v96
	v_add_f32_e32 v96, v97, v101
	v_cvt_f16_f32_e32 v96, v96
	v_pk_add_f32 v[94:95], v[94:95], v[128:129]
	v_add_f32_e32 v78, v78, v90
	v_cvt_pk_f16_f32 v95, v94, v95
	v_pack_b32_f16 v94, v104, v95
	v_alignbit_b32 v95, v96, v95, 16
	v_cvt_f16_f32_e32 v96, v86
	v_mov_b32_e32 v86, v87
	v_mov_b32_e32 v87, v88
	v_add_f32_e32 v88, v89, v101
	v_cvt_f16_f32_e32 v88, v88
	v_pk_add_f32 v[86:87], v[86:87], v[128:129]
	v_add_f32_e32 v107, v109, v101
	v_cvt_pk_f16_f32 v87, v86, v87
	v_pack_b32_f16 v86, v96, v87
	v_alignbit_b32 v87, v88, v87, 16
	v_cvt_f16_f32_e32 v88, v78
	v_mov_b32_e32 v78, v79
	v_mov_b32_e32 v79, v80
	v_add_f32_e32 v80, v81, v93
	v_cvt_f16_f32_e32 v107, v107
	v_cvt_f16_f32_e32 v80, v80
	v_pk_add_f32 v[78:79], v[78:79], v[126:127]
	s_nop 0
	v_cvt_pk_f16_f32 v79, v78, v79
	v_alignbit_b32 v1, v107, v1, 16
	v_pack_b32_f16 v78, v88, v79
	v_alignbit_b32 v79, v80, v79, 16
	s_barrier
	ds_write2_b64 v130, v[0:1], v[78:79] offset1:4
	v_add_f32_e32 v0, v74, v90
	v_cvt_f16_f32_e32 v74, v0
	v_mov_b32_e32 v0, v75
	v_add_f32_e32 v75, v77, v93
	v_cvt_f16_f32_e32 v75, v75
	v_mov_b32_e32 v1, v76
	v_pk_add_f32 v[0:1], v[0:1], v[126:127]
	s_nop 0
	v_cvt_pk_f16_f32 v1, v0, v1
	v_pack_b32_f16 v0, v74, v1
	v_alignbit_b32 v1, v75, v1, 16
	ds_write2_b64 v132, v[102:103], v[0:1] offset0:32 offset1:36
	v_add_f32_e32 v0, v70, v90
	v_cvt_f16_f32_e32 v70, v0
	v_mov_b32_e32 v0, v71
	v_add_f32_e32 v71, v73, v93
	v_cvt_f16_f32_e32 v71, v71
	v_mov_b32_e32 v1, v72
	v_pk_add_f32 v[0:1], v[0:1], v[126:127]
	s_nop 0
	v_cvt_pk_f16_f32 v1, v0, v1
	v_pack_b32_f16 v0, v70, v1
	v_alignbit_b32 v1, v71, v1, 16
	ds_write2_b64 v131, v[94:95], v[0:1] offset0:64 offset1:68
	v_add_f32_e32 v0, v66, v90
	v_cvt_f16_f32_e32 v66, v0
	v_mov_b32_e32 v0, v67
	v_add_f32_e32 v67, v69, v93
	v_cvt_f16_f32_e32 v67, v67
	v_mov_b32_e32 v1, v68
	v_pk_add_f32 v[0:1], v[0:1], v[126:127]
	v_mul_u32_u24_e32 v68, s4, v140
	v_cvt_pk_f16_f32 v1, v0, v1
	v_pack_b32_f16 v0, v66, v1
	v_alignbit_b32 v1, v67, v1, 16
	ds_write2_b64 v91, v[86:87], v[0:1] offset0:96 offset1:100
	v_add_f32_e32 v0, v62, v82
	v_cvt_f16_f32_e32 v62, v0
	v_mov_b32_e32 v0, v63
	v_add_f32_e32 v63, v65, v85
	v_cvt_f16_f32_e32 v63, v63
	v_mov_b32_e32 v1, v64
	v_pk_add_f32 v[0:1], v[0:1], v[124:125]
	s_nop 0
	v_cvt_pk_f16_f32 v1, v0, v1
	v_pack_b32_f16 v0, v62, v1
	v_alignbit_b32 v1, v63, v1, 16
	ds_write_b64 v130, v[0:1] offset:64
	v_add_f32_e32 v0, v58, v82
	v_cvt_f16_f32_e32 v58, v0
	v_mov_b32_e32 v0, v59
	v_add_f32_e32 v59, v61, v85
	v_cvt_f16_f32_e32 v59, v59
	v_mov_b32_e32 v1, v60
	v_pk_add_f32 v[0:1], v[0:1], v[124:125]
	s_nop 0
	v_cvt_pk_f16_f32 v1, v0, v1
	v_pack_b32_f16 v0, v58, v1
	v_alignbit_b32 v1, v59, v1, 16
	ds_write_b64 v130, v[0:1] offset:12608
	v_add_f32_e32 v0, v54, v82
	v_cvt_f16_f32_e32 v54, v0
	v_mov_b32_e32 v0, v55
	v_add_f32_e32 v55, v57, v85
	v_cvt_f16_f32_e32 v55, v55
	v_mov_b32_e32 v1, v56
	v_pk_add_f32 v[0:1], v[0:1], v[124:125]
	s_nop 0
	v_cvt_pk_f16_f32 v1, v0, v1
	v_pack_b32_f16 v0, v54, v1
	v_alignbit_b32 v1, v55, v1, 16
	ds_write_b64 v130, v[0:1] offset:25152
	v_add_f32_e32 v0, v50, v82
	v_cvt_f16_f32_e32 v50, v0
	v_mov_b32_e32 v0, v51
	v_add_f32_e32 v51, v53, v85
	v_cvt_f16_f32_e32 v51, v51
	v_mov_b32_e32 v1, v52
	v_pk_add_f32 v[0:1], v[0:1], v[124:125]
	s_nop 0
	v_cvt_pk_f16_f32 v1, v0, v1
	v_pack_b32_f16 v0, v50, v1
	v_alignbit_b32 v1, v51, v1, 16
	ds_write_b64 v130, v[0:1] offset:37696
	s_waitcnt lgkmcnt(0)
	s_barrier
	global_load_dwordx4 v[50:53], v[122:123], off
	global_load_dwordx4 v[54:57], v[122:123], off offset:1024
	global_load_dwordx4 v[58:61], v[122:123], off offset:2048
	ds_read_b128 v[62:65], v83
	ds_read_b128 v[70:73], v84
	v_add_u32_e32 v0, v68, v111
	ds_read_b128 v[74:77], v99
	s_waitcnt lgkmcnt(2)
	buffer_store_dwordx4 v[62:65], v0, s[0:3], 0 offen sc1
	v_or_b32_e32 v0, s6, v154
	v_mul_u32_u24_e32 v69, s4, v0
	ds_read_b128 v[62:65], v92
	v_add_u32_e32 v0, v69, v113
	s_waitcnt lgkmcnt(2)
	buffer_store_dwordx4 v[70:73], v0, s[0:3], 0 offen sc1
	v_or_b32_e32 v0, s6, v155
	s_nop 0
	v_mul_u32_u24_e32 v72, s4, v0
	v_add_u32_e32 v0, v72, v115
	s_waitcnt lgkmcnt(0)
	buffer_store_dwordx4 v[62:65], v0, s[0:3], 0 offen sc1
	v_add_u32_e32 v0, s6, v156
	v_mul_u32_u24_e32 v70, s4, v0
	ds_read_b128 v[62:65], v100
	v_add_u32_e32 v0, v70, v117
	buffer_store_dwordx4 v[74:77], v0, s[0:3], 0 offen sc1
	v_or_b32_e32 v0, s6, v157
	v_mul_u32_u24_e32 v71, s4, v0
	v_add_u32_e32 v0, v71, v144
	ds_read_b128 v[74:77], v110
	s_waitcnt lgkmcnt(1)
	buffer_store_dwordx4 v[62:65], v0, s[0:3], 0 offen sc1
	ds_read_b128 v[62:65], v135
	ds_read_b128 v[78:81], v135 offset:8192
	ds_read_b128 v[86:89], v135 offset:16384
	ds_read_b128 v[94:97], v135 offset:24576
	ds_read_b128 v[102:105], v135 offset:32768
	ds_read_b128 v[106:109], v135 offset:40960
	ds_read_b128 v[124:127], v135 offset:49152
	ds_read_b128 v[148:151], v135 offset:57344
	v_add_u32_e32 v0, s6, v147
	v_mul_u32_u24_e32 v73, s4, v0
	v_add_u32_e32 v0, v73, v145
	s_waitcnt lgkmcnt(8)
	buffer_store_dwordx4 v[74:77], v0, s[0:3], 0 offen sc1
	s_waitcnt lgkmcnt(7)
	s_nop 0
	v_mfma_f32_16x16x32_f16 v[74:77], v[38:41], v[62:65], 0
	s_waitcnt lgkmcnt(6)
	v_mfma_f32_16x16x32_f16 v[152:155], v[38:41], v[78:81], 0
	s_waitcnt lgkmcnt(5)
	v_mfma_f32_16x16x32_f16 v[156:159], v[38:41], v[86:89], 0
	s_waitcnt lgkmcnt(4)
	v_mfma_f32_16x16x32_f16 v[160:163], v[38:41], v[94:97], 0
	s_waitcnt lgkmcnt(3)
	v_mfma_f32_16x16x32_f16 v[164:167], v[38:41], v[102:105], 0
	s_waitcnt lgkmcnt(2)
	v_mfma_f32_16x16x32_f16 v[168:171], v[38:41], v[106:109], 0
	s_waitcnt lgkmcnt(1)
	v_mfma_f32_16x16x32_f16 v[172:175], v[38:41], v[124:127], 0
	s_waitcnt lgkmcnt(0)
	v_mfma_f32_16x16x32_f16 v[38:41], v[38:41], v[148:151], 0
	v_mfma_f32_16x16x32_f16 v[176:179], v[26:29], v[62:65], 0
	v_mfma_f32_16x16x32_f16 v[180:183], v[26:29], v[78:81], 0
	v_mfma_f32_16x16x32_f16 v[184:187], v[26:29], v[86:89], 0
	v_mfma_f32_16x16x32_f16 v[188:191], v[26:29], v[94:97], 0
	v_mfma_f32_16x16x32_f16 v[192:195], v[26:29], v[102:105], 0
	v_mfma_f32_16x16x32_f16 v[196:199], v[26:29], v[106:109], 0
	v_mfma_f32_16x16x32_f16 v[200:203], v[26:29], v[124:127], 0
	v_mfma_f32_16x16x32_f16 v[26:29], v[26:29], v[148:151], 0
	v_mfma_f32_16x16x32_f16 v[62:65], v[10:13], v[62:65], 0
	v_mfma_f32_16x16x32_f16 v[78:81], v[10:13], v[78:81], 0
	v_mfma_f32_16x16x32_f16 v[86:89], v[10:13], v[86:89], 0
	v_mfma_f32_16x16x32_f16 v[94:97], v[10:13], v[94:97], 0
	v_mfma_f32_16x16x32_f16 v[102:105], v[10:13], v[102:105], 0
	v_mfma_f32_16x16x32_f16 v[106:109], v[10:13], v[106:109], 0
	v_mfma_f32_16x16x32_f16 v[124:127], v[10:13], v[124:127], 0
	v_mfma_f32_16x16x32_f16 v[10:13], v[10:13], v[148:151], 0
	s_mov_b32 s4, 0x34000
	v_add_co_u32_e32 v66, vcc, s4, v118
	s_mov_b32 s4, 0x35000
	s_nop 0
	v_addc_co_u32_e32 v67, vcc, 0, v119, vcc
	v_add_co_u32_e32 v118, vcc, s4, v118
	s_nop 1
	v_addc_co_u32_e32 v119, vcc, 0, v119, vcc
	global_load_dwordx4 v[148:151], v[118:119], off offset:-4096
	global_load_dwordx4 v[204:207], v[122:123], off offset:3072
	global_load_dwordx4 v[208:211], v[66:67], off offset:1024
	ds_read_b128 v[212:215], v133
	ds_read_b128 v[216:219], v133 offset:8192
	ds_read_b128 v[220:223], v133 offset:16384
	ds_read_b128 v[224:227], v133 offset:24576
	ds_read_b128 v[228:231], v133 offset:32768
	ds_read_b128 v[232:235], v133 offset:40960
	ds_read_b128 v[236:239], v133 offset:49152
	ds_read_b128 v[240:243], v133 offset:57344
	s_waitcnt lgkmcnt(7)
	v_mfma_f32_16x16x32_f16 v[74:77], v[22:25], v[212:215], v[74:77]
	s_waitcnt lgkmcnt(6)
	v_mfma_f32_16x16x32_f16 v[152:155], v[22:25], v[216:219], v[152:155]
	s_waitcnt lgkmcnt(5)
	v_mfma_f32_16x16x32_f16 v[156:159], v[22:25], v[220:223], v[156:159]
	s_waitcnt lgkmcnt(4)
	v_mfma_f32_16x16x32_f16 v[160:163], v[22:25], v[224:227], v[160:163]
	s_waitcnt lgkmcnt(3)
	v_mfma_f32_16x16x32_f16 v[164:167], v[22:25], v[228:231], v[164:167]
	s_waitcnt lgkmcnt(2)
	v_mfma_f32_16x16x32_f16 v[168:171], v[22:25], v[232:235], v[168:171]
	s_waitcnt lgkmcnt(1)
	v_mfma_f32_16x16x32_f16 v[172:175], v[22:25], v[236:239], v[172:175]
	s_waitcnt lgkmcnt(0)
	v_mfma_f32_16x16x32_f16 v[22:25], v[22:25], v[240:243], v[38:41]
	v_mfma_f32_16x16x32_f16 v[38:41], v[6:9], v[212:215], v[176:179]
	v_mfma_f32_16x16x32_f16 v[176:179], v[6:9], v[216:219], v[180:183]
	v_mfma_f32_16x16x32_f16 v[180:183], v[6:9], v[220:223], v[184:187]
	v_mfma_f32_16x16x32_f16 v[184:187], v[6:9], v[224:227], v[188:191]
	v_mfma_f32_16x16x32_f16 v[188:191], v[6:9], v[228:231], v[192:195]
	v_mfma_f32_16x16x32_f16 v[192:195], v[6:9], v[232:235], v[196:199]
	v_mfma_f32_16x16x32_f16 v[196:199], v[6:9], v[236:239], v[200:203]
	v_mfma_f32_16x16x32_f16 v[6:9], v[6:9], v[240:243], v[26:29]
	v_mfma_f32_16x16x32_f16 v[26:29], v[2:5], v[212:215], v[62:65]
	v_mfma_f32_16x16x32_f16 v[62:65], v[2:5], v[216:219], v[78:81]
	v_mfma_f32_16x16x32_f16 v[78:81], v[2:5], v[220:223], v[86:89]
	v_mfma_f32_16x16x32_f16 v[86:89], v[2:5], v[224:227], v[94:97]
	v_mfma_f32_16x16x32_f16 v[94:97], v[2:5], v[228:231], v[102:105]
	v_mfma_f32_16x16x32_f16 v[102:105], v[2:5], v[232:235], v[106:109]
	v_mfma_f32_16x16x32_f16 v[106:109], v[2:5], v[236:239], v[124:127]
	v_mfma_f32_16x16x32_f16 v[0:3], v[2:5], v[240:243], v[10:13]
	s_nop 2
	global_load_dwordx4 v[10:13], v[66:67], off offset:2048
	global_load_dwordx4 v[122:125], v[66:67], off offset:3072
	global_load_dwordx4 v[126:129], v[118:119], off
	ds_read_b128 v[200:203], v134
	ds_read_b128 v[212:215], v134 offset:8192
	ds_read_b128 v[216:219], v134 offset:16384
	ds_read_b128 v[220:223], v134 offset:24576
	ds_read_b128 v[224:227], v134 offset:32768
	ds_read_b128 v[228:231], v134 offset:40960
	ds_read_b128 v[232:235], v134 offset:49152
	ds_read_b128 v[236:239], v134 offset:57344
	s_waitcnt lgkmcnt(7)
	v_mfma_f32_16x16x32_f16 v[74:77], v[30:33], v[200:203], v[74:77]
	s_waitcnt lgkmcnt(6)
	v_mfma_f32_16x16x32_f16 v[152:155], v[30:33], v[212:215], v[152:155]
	s_waitcnt lgkmcnt(5)
	v_mfma_f32_16x16x32_f16 v[156:159], v[30:33], v[216:219], v[156:159]
	s_waitcnt lgkmcnt(4)
	v_mfma_f32_16x16x32_f16 v[160:163], v[30:33], v[220:223], v[160:163]
	s_waitcnt lgkmcnt(3)
	v_mfma_f32_16x16x32_f16 v[164:167], v[30:33], v[224:227], v[164:167]
	s_waitcnt lgkmcnt(2)
	v_mfma_f32_16x16x32_f16 v[168:171], v[30:33], v[228:231], v[168:171]
	s_waitcnt lgkmcnt(1)
	v_mfma_f32_16x16x32_f16 v[172:175], v[30:33], v[232:235], v[172:175]
	s_waitcnt lgkmcnt(0)
	v_mfma_f32_16x16x32_f16 v[22:25], v[30:33], v[236:239], v[22:25]
	v_mfma_f32_16x16x32_f16 v[30:33], v[14:17], v[200:203], v[38:41]
	v_mfma_f32_16x16x32_f16 v[38:41], v[14:17], v[212:215], v[176:179]
	v_mfma_f32_16x16x32_f16 v[176:179], v[14:17], v[216:219], v[180:183]
	v_mfma_f32_16x16x32_f16 v[180:183], v[14:17], v[220:223], v[184:187]
	v_mfma_f32_16x16x32_f16 v[184:187], v[14:17], v[224:227], v[188:191]
	v_mfma_f32_16x16x32_f16 v[188:191], v[14:17], v[228:231], v[192:195]
	v_mfma_f32_16x16x32_f16 v[192:195], v[14:17], v[232:235], v[196:199]
	v_mfma_f32_16x16x32_f16 v[4:7], v[14:17], v[236:239], v[6:9]
	v_mfma_f32_16x16x32_f16 v[14:17], v[18:21], v[200:203], v[26:29]
	v_mfma_f32_16x16x32_f16 v[26:29], v[18:21], v[212:215], v[62:65]
	v_mfma_f32_16x16x32_f16 v[62:65], v[18:21], v[216:219], v[78:81]
	v_mfma_f32_16x16x32_f16 v[78:81], v[18:21], v[220:223], v[86:89]
	v_mfma_f32_16x16x32_f16 v[86:89], v[18:21], v[224:227], v[94:97]
	v_mfma_f32_16x16x32_f16 v[94:97], v[18:21], v[228:231], v[102:105]
	v_mfma_f32_16x16x32_f16 v[102:105], v[18:21], v[232:235], v[106:109]
	v_mfma_f32_16x16x32_f16 v[0:3], v[18:21], v[236:239], v[0:3]
	global_load_dwordx4 v[18:21], v[118:119], off offset:1024
	s_nop 0
	global_load_dwordx4 v[106:109], v[118:119], off offset:2048
	global_load_dwordx4 v[196:199], v[118:119], off offset:3072
	ds_read_b128 v[200:203], v136
	ds_read_b128 v[212:215], v136 offset:8192
	ds_read_b128 v[216:219], v136 offset:16384
	ds_read_b128 v[220:223], v136 offset:24576
	ds_read_b128 v[224:227], v136 offset:32768
	ds_read_b128 v[228:231], v136 offset:40960
	ds_read_b128 v[232:235], v136 offset:49152
	ds_read_b128 v[236:239], v136 offset:57344
	s_waitcnt lgkmcnt(7)
	v_mfma_f32_16x16x32_f16 v[74:77], v[46:49], v[200:203], v[74:77]
	s_waitcnt lgkmcnt(6)
	v_mfma_f32_16x16x32_f16 v[152:155], v[46:49], v[212:215], v[152:155]
	s_waitcnt lgkmcnt(5)
	v_mfma_f32_16x16x32_f16 v[156:159], v[46:49], v[216:219], v[156:159]
	s_waitcnt lgkmcnt(4)
	v_mfma_f32_16x16x32_f16 v[160:163], v[46:49], v[220:223], v[160:163]
	s_waitcnt lgkmcnt(3)
	v_mfma_f32_16x16x32_f16 v[164:167], v[46:49], v[224:227], v[164:167]
	s_waitcnt lgkmcnt(2)
	v_mfma_f32_16x16x32_f16 v[168:171], v[46:49], v[228:231], v[168:171]
	s_waitcnt lgkmcnt(1)
	v_mfma_f32_16x16x32_f16 v[172:175], v[46:49], v[232:235], v[172:175]
	s_waitcnt lgkmcnt(0)
	v_mfma_f32_16x16x32_f16 v[22:25], v[46:49], v[236:239], v[22:25]
	v_mfma_f32_16x16x32_f16 v[30:33], v[42:45], v[200:203], v[30:33]
	v_mfma_f32_16x16x32_f16 v[38:41], v[42:45], v[212:215], v[38:41]
	v_mfma_f32_16x16x32_f16 v[46:49], v[42:45], v[216:219], v[176:179]
	v_mfma_f32_16x16x32_f16 v[176:179], v[42:45], v[220:223], v[180:183]
	v_mfma_f32_16x16x32_f16 v[180:183], v[42:45], v[224:227], v[184:187]
	v_mfma_f32_16x16x32_f16 v[184:187], v[42:45], v[228:231], v[188:191]
	v_mfma_f32_16x16x32_f16 v[188:191], v[42:45], v[232:235], v[192:195]
	v_mfma_f32_16x16x32_f16 v[4:7], v[42:45], v[236:239], v[4:7]
	v_mfma_f32_16x16x32_f16 v[14:17], v[34:37], v[200:203], v[14:17]
	v_mfma_f32_16x16x32_f16 v[26:29], v[34:37], v[212:215], v[26:29]
	v_mfma_f32_16x16x32_f16 v[42:45], v[34:37], v[216:219], v[62:65]
	v_mfma_f32_16x16x32_f16 v[62:65], v[34:37], v[220:223], v[78:81]
	v_mfma_f32_16x16x32_f16 v[78:81], v[34:37], v[224:227], v[86:89]
	v_mfma_f32_16x16x32_f16 v[86:89], v[34:37], v[228:231], v[94:97]
	v_mfma_f32_16x16x32_f16 v[94:97], v[34:37], v[232:235], v[102:105]
	v_mfma_f32_16x16x32_f16 v[0:3], v[34:37], v[236:239], v[0:3]
	ds_read_b128 v[34:37], v137
	s_nop 0
	ds_read_b128 v[102:105], v137 offset:8192
	ds_read_b128 v[192:195], v137 offset:16384
	ds_read_b128 v[200:203], v137 offset:24576
	ds_read_b128 v[212:215], v137 offset:32768
	ds_read_b128 v[216:219], v137 offset:40960
	ds_read_b128 v[220:223], v137 offset:49152
	ds_read_b128 v[134:137], v137 offset:57344
	s_waitcnt vmcnt(17) lgkmcnt(7)
	v_mfma_f32_16x16x32_f16 v[74:77], v[50:53], v[34:37], v[74:77]
	s_waitcnt lgkmcnt(6)
	v_mfma_f32_16x16x32_f16 v[152:155], v[50:53], v[102:105], v[152:155]
	s_waitcnt lgkmcnt(5)
	v_mfma_f32_16x16x32_f16 v[156:159], v[50:53], v[192:195], v[156:159]
	s_waitcnt lgkmcnt(4)
	v_mfma_f32_16x16x32_f16 v[160:163], v[50:53], v[200:203], v[160:163]
	s_waitcnt lgkmcnt(3)
	v_mfma_f32_16x16x32_f16 v[164:167], v[50:53], v[212:215], v[164:167]
	s_waitcnt lgkmcnt(2)
	v_mfma_f32_16x16x32_f16 v[168:171], v[50:53], v[216:219], v[168:171]
	s_waitcnt lgkmcnt(1)
	v_mfma_f32_16x16x32_f16 v[172:175], v[50:53], v[220:223], v[172:175]
	s_waitcnt lgkmcnt(0)
	v_mfma_f32_16x16x32_f16 v[22:25], v[50:53], v[134:137], v[22:25]
	s_waitcnt vmcnt(16)
	v_mfma_f32_16x16x32_f16 v[30:33], v[54:57], v[34:37], v[30:33]
	v_mfma_f32_16x16x32_f16 v[38:41], v[54:57], v[102:105], v[38:41]
	v_mfma_f32_16x16x32_f16 v[46:49], v[54:57], v[192:195], v[46:49]
	v_mfma_f32_16x16x32_f16 v[50:53], v[54:57], v[200:203], v[176:179]
	v_mfma_f32_16x16x32_f16 v[176:179], v[54:57], v[212:215], v[180:183]
	v_mfma_f32_16x16x32_f16 v[180:183], v[54:57], v[216:219], v[184:187]
	v_mfma_f32_16x16x32_f16 v[184:187], v[54:57], v[220:223], v[188:191]
	v_mfma_f32_16x16x32_f16 v[4:7], v[54:57], v[134:137], v[4:7]
	s_waitcnt vmcnt(15)
	v_mfma_f32_16x16x32_f16 v[14:17], v[58:61], v[34:37], v[14:17]
	v_mfma_f32_16x16x32_f16 v[26:29], v[58:61], v[102:105], v[26:29]
	v_mfma_f32_16x16x32_f16 v[34:37], v[58:61], v[192:195], v[42:45]
	v_mfma_f32_16x16x32_f16 v[42:45], v[58:61], v[200:203], v[62:65]
	v_mfma_f32_16x16x32_f16 v[54:57], v[58:61], v[212:215], v[78:81]
	v_mfma_f32_16x16x32_f16 v[62:65], v[58:61], v[216:219], v[86:89]
	v_mfma_f32_16x16x32_f16 v[78:81], v[58:61], v[220:223], v[94:97]
	v_mfma_f32_16x16x32_f16 v[0:3], v[58:61], v[134:137], v[0:3]
	ds_read_b128 v[58:61], v138
	ds_read_b128 v[86:89], v138 offset:8192
	ds_read_b128 v[94:97], v138 offset:16384
	ds_read_b128 v[102:105], v138 offset:24576
	ds_read_b128 v[134:137], v138 offset:32768
	ds_read_b128 v[188:191], v138 offset:40960
	ds_read_b128 v[192:195], v138 offset:49152
	ds_read_b128 v[200:203], v138 offset:57344
	s_waitcnt vmcnt(7) lgkmcnt(7)
	v_mfma_f32_16x16x32_f16 v[74:77], v[204:207], v[58:61], v[74:77]
	s_waitcnt lgkmcnt(6)
	v_mfma_f32_16x16x32_f16 v[152:155], v[204:207], v[86:89], v[152:155]
	s_waitcnt lgkmcnt(5)
	v_mfma_f32_16x16x32_f16 v[156:159], v[204:207], v[94:97], v[156:159]
	s_waitcnt lgkmcnt(4)
	v_mfma_f32_16x16x32_f16 v[160:163], v[204:207], v[102:105], v[160:163]
	s_waitcnt lgkmcnt(3)
	v_mfma_f32_16x16x32_f16 v[164:167], v[204:207], v[134:137], v[164:167]
	s_waitcnt lgkmcnt(2)
	v_mfma_f32_16x16x32_f16 v[168:171], v[204:207], v[188:191], v[168:171]
	s_waitcnt lgkmcnt(1)
	v_mfma_f32_16x16x32_f16 v[172:175], v[204:207], v[192:195], v[172:175]
	s_waitcnt lgkmcnt(0)
	v_mfma_f32_16x16x32_f16 v[22:25], v[204:207], v[200:203], v[22:25]
	v_mfma_f32_16x16x32_f16 v[30:33], v[148:151], v[58:61], v[30:33]
	v_mfma_f32_16x16x32_f16 v[38:41], v[148:151], v[86:89], v[38:41]
	v_mfma_f32_16x16x32_f16 v[46:49], v[148:151], v[94:97], v[46:49]
	v_mfma_f32_16x16x32_f16 v[50:53], v[148:151], v[102:105], v[50:53]
	v_mfma_f32_16x16x32_f16 v[176:179], v[148:151], v[134:137], v[176:179]
	v_mfma_f32_16x16x32_f16 v[180:183], v[148:151], v[188:191], v[180:183]
	v_mfma_f32_16x16x32_f16 v[184:187], v[148:151], v[192:195], v[184:187]
	v_mfma_f32_16x16x32_f16 v[4:7], v[148:151], v[200:203], v[4:7]
	s_waitcnt vmcnt(6)
	v_mfma_f32_16x16x32_f16 v[14:17], v[208:211], v[58:61], v[14:17]
	v_mfma_f32_16x16x32_f16 v[26:29], v[208:211], v[86:89], v[26:29]
	v_mfma_f32_16x16x32_f16 v[34:37], v[208:211], v[94:97], v[34:37]
	v_mfma_f32_16x16x32_f16 v[42:45], v[208:211], v[102:105], v[42:45]
	v_mfma_f32_16x16x32_f16 v[54:57], v[208:211], v[134:137], v[54:57]
	v_mfma_f32_16x16x32_f16 v[58:61], v[208:211], v[188:191], v[62:65]
	v_mfma_f32_16x16x32_f16 v[62:65], v[208:211], v[192:195], v[78:81]
	v_mfma_f32_16x16x32_f16 v[0:3], v[208:211], v[200:203], v[0:3]
	s_nop 1
	ds_read_b128 v[78:81], v139
	ds_read_b128 v[86:89], v139 offset:8192
	ds_read_b128 v[94:97], v139 offset:16384
	ds_read_b128 v[102:105], v139 offset:24576
	ds_read_b128 v[134:137], v139 offset:32768
	ds_read_b128 v[148:151], v139 offset:40960
	ds_read_b128 v[188:191], v139 offset:49152
	ds_read_b128 v[192:195], v139 offset:57344
	s_waitcnt vmcnt(5) lgkmcnt(7)
	v_mfma_f32_16x16x32_f16 v[74:77], v[10:13], v[78:81], v[74:77]
	s_waitcnt lgkmcnt(6)
	v_mfma_f32_16x16x32_f16 v[152:155], v[10:13], v[86:89], v[152:155]
	s_waitcnt lgkmcnt(5)
	v_mfma_f32_16x16x32_f16 v[156:159], v[10:13], v[94:97], v[156:159]
	s_waitcnt lgkmcnt(4)
	v_mfma_f32_16x16x32_f16 v[160:163], v[10:13], v[102:105], v[160:163]
	s_waitcnt lgkmcnt(3)
	v_mfma_f32_16x16x32_f16 v[164:167], v[10:13], v[134:137], v[164:167]
	s_waitcnt lgkmcnt(2)
	v_mfma_f32_16x16x32_f16 v[168:171], v[10:13], v[148:151], v[168:171]
	s_waitcnt lgkmcnt(1)
	v_mfma_f32_16x16x32_f16 v[172:175], v[10:13], v[188:191], v[172:175]
	s_waitcnt lgkmcnt(0)
	v_mfma_f32_16x16x32_f16 v[8:11], v[10:13], v[192:195], v[22:25]
	s_waitcnt vmcnt(4)
	v_mfma_f32_16x16x32_f16 v[22:25], v[122:125], v[78:81], v[30:33]
	v_mfma_f32_16x16x32_f16 v[30:33], v[122:125], v[86:89], v[38:41]
	v_mfma_f32_16x16x32_f16 v[200:203], v[122:125], v[94:97], v[46:49]
	v_mfma_f32_16x16x32_f16 v[48:51], v[122:125], v[102:105], v[50:53]
	v_mfma_f32_16x16x32_f16 v[176:179], v[122:125], v[134:137], v[176:179]
	v_mfma_f32_16x16x32_f16 v[180:183], v[122:125], v[148:151], v[180:183]
	v_mfma_f32_16x16x32_f16 v[184:187], v[122:125], v[188:191], v[184:187]
	v_mfma_f32_16x16x32_f16 v[4:7], v[122:125], v[192:195], v[4:7]
	s_waitcnt vmcnt(3)
	v_mfma_f32_16x16x32_f16 v[12:15], v[126:129], v[78:81], v[14:17]
	v_mfma_f32_16x16x32_f16 v[78:81], v[126:129], v[86:89], v[26:29]
	v_mfma_f32_16x16x32_f16 v[86:89], v[126:129], v[94:97], v[34:37]
	v_mfma_f32_16x16x32_f16 v[40:43], v[126:129], v[102:105], v[42:45]
	v_mfma_f32_16x16x32_f16 v[94:97], v[126:129], v[134:137], v[54:57]
	v_mfma_f32_16x16x32_f16 v[102:105], v[126:129], v[148:151], v[58:61]
	v_mfma_f32_16x16x32_f16 v[64:67], v[126:129], v[188:191], v[62:65]
	v_mfma_f32_16x16x32_f16 v[0:3], v[126:129], v[192:195], v[0:3]
	s_nop 1
	ds_read_b128 v[60:63], v141
	ds_read_b128 v[122:125], v141 offset:8192
	ds_read_b128 v[126:129], v141 offset:16384
	ds_read_b128 v[134:137], v141 offset:24576
	ds_read_b128 v[148:151], v141 offset:32768
	ds_read_b128 v[188:191], v141 offset:40960
	ds_read_b128 v[192:195], v141 offset:49152
	ds_read_b128 v[138:141], v141 offset:57344
	s_waitcnt vmcnt(2) lgkmcnt(7)
	v_mfma_f32_16x16x32_f16 v[74:77], v[18:21], v[60:63], v[74:77]
	s_waitcnt lgkmcnt(6)
	v_mfma_f32_16x16x32_f16 v[152:155], v[18:21], v[122:125], v[152:155]
	s_waitcnt lgkmcnt(5)
	v_mfma_f32_16x16x32_f16 v[156:159], v[18:21], v[126:129], v[156:159]
	s_waitcnt lgkmcnt(4)
	v_mfma_f32_16x16x32_f16 v[160:163], v[18:21], v[134:137], v[160:163]
	s_waitcnt lgkmcnt(3)
	v_mfma_f32_16x16x32_f16 v[56:59], v[18:21], v[148:151], v[164:167]
	s_waitcnt lgkmcnt(2)
	v_mfma_f32_16x16x32_f16 v[52:55], v[18:21], v[188:191], v[168:171]
	s_waitcnt lgkmcnt(1)
	v_mfma_f32_16x16x32_f16 v[44:47], v[18:21], v[192:195], v[172:175]
	s_waitcnt lgkmcnt(0)
	v_mfma_f32_16x16x32_f16 v[36:39], v[18:21], v[138:141], v[8:11]
	s_waitcnt vmcnt(1)
	v_mfma_f32_16x16x32_f16 v[164:167], v[106:109], v[60:63], v[22:25]
	v_mfma_f32_16x16x32_f16 v[168:171], v[106:109], v[122:125], v[30:33]
	v_mfma_f32_16x16x32_f16 v[172:175], v[106:109], v[126:129], v[200:203]
	v_mfma_f32_16x16x32_f16 v[200:203], v[106:109], v[134:137], v[48:51]
	v_mfma_f32_16x16x32_f16 v[32:35], v[106:109], v[148:151], v[176:179]
	v_mfma_f32_16x16x32_f16 v[24:27], v[106:109], v[188:191], v[180:183]
	v_mfma_f32_16x16x32_f16 v[20:23], v[106:109], v[192:195], v[184:187]
	v_mfma_f32_16x16x32_f16 v[16:19], v[106:109], v[138:141], v[4:7]
	s_waitcnt vmcnt(0)
	v_mfma_f32_16x16x32_f16 v[106:109], v[196:199], v[60:63], v[12:15]
	v_mfma_f32_16x16x32_f16 v[78:81], v[196:199], v[122:125], v[78:81]
	v_mfma_f32_16x16x32_f16 v[86:89], v[196:199], v[126:129], v[86:89]
	v_mfma_f32_16x16x32_f16 v[60:63], v[196:199], v[134:137], v[40:43]
	v_mfma_f32_16x16x32_f16 v[12:15], v[196:199], v[148:151], v[94:97]
	v_mfma_f32_16x16x32_f16 v[8:11], v[196:199], v[188:191], v[102:105]
	v_mfma_f32_16x16x32_f16 v[4:7], v[196:199], v[192:195], v[64:67]
	v_mfma_f32_16x16x32_f16 v[0:3], v[196:199], v[138:141], v[0:3]
	global_load_dwordx4 v[48:51], v[120:121], off offset:1536
	global_load_dwordx4 v[40:43], v[120:121], off offset:1600
	global_load_dwordx4 v[28:31], v[120:121], off offset:1664
	v_mov_b32_e32 v94, v157
	v_mov_b32_e32 v95, v158
	v_mov_b32_e32 v96, v161
	v_mov_b32_e32 v97, v162
	v_mov_b32_e32 v64, v153
	v_mov_b32_e32 v65, v154
	v_mov_b32_e32 v102, v169
	v_mov_b32_e32 v103, v170
	v_mov_b32_e32 v104, v173
	v_mov_b32_e32 v105, v174
	v_mov_b32_e32 v118, v201
	v_mov_b32_e32 v119, v202
	s_barrier
	s_waitcnt vmcnt(2)
	v_pk_add_f32 v[74:75], v[74:75], v[48:49]
	v_add_f32_e32 v82, v152, v48
	v_pk_mov_b32 v[120:121], v[48:49], v[50:51] op_sel:[1,0]
	v_add_f32_e32 v49, v155, v51
	s_waitcnt vmcnt(1)
	v_pk_add_f32 v[122:123], v[164:165], v[40:41]
	v_add_f32_e32 v98, v168, v40
	v_pk_mov_b32 v[66:67], v[40:41], v[42:43] op_sel:[1,0]
	v_add_f32_e32 v41, v171, v43
	v_pk_add_f32 v[76:77], v[76:77], v[50:51]
	v_add_f32_e32 v50, v156, v48
	v_add_f32_e32 v85, v159, v51
	v_add_f32_e32 v90, v160, v48
	v_add_f32_e32 v93, v163, v51
	v_pk_add_f32 v[124:125], v[166:167], v[42:43]
	v_add_f32_e32 v42, v172, v40
	v_add_f32_e32 v101, v175, v43
	v_add_f32_e32 v126, v200, v40
	v_add_f32_e32 v127, v203, v43
	v_cvt_f16_f32_e32 v82, v82
	v_cvt_f16_f32_e32 v49, v49
	v_cvt_f16_f32_e32 v98, v98
	v_cvt_f16_f32_e32 v41, v41
	v_cvt_pk_f16_f32 v74, v74, v75
	v_cvt_pk_f16_f32 v75, v76, v77
	v_cvt_f16_f32_e32 v50, v50
	v_pk_add_f32 v[76:77], v[94:95], v[120:121]
	v_cvt_f16_f32_e32 v85, v85
	v_cvt_f16_f32_e32 v90, v90
	v_pk_add_f32 v[94:95], v[96:97], v[120:121]
	v_cvt_f16_f32_e32 v93, v93
	v_cvt_pk_f16_f32 v96, v122, v123
	v_cvt_f16_f32_e32 v42, v42
	v_cvt_f16_f32_e32 v101, v101
	v_cvt_f16_f32_e32 v122, v126
	v_cvt_f16_f32_e32 v123, v127
	v_pk_add_f32 v[64:65], v[64:65], v[120:121]
	v_pk_add_f32 v[102:103], v[102:103], v[66:67]
	v_pk_add_f32 v[104:105], v[104:105], v[66:67]
	v_pk_add_f32 v[118:119], v[118:119], v[66:67]
	v_cvt_pk_f16_f32 v65, v64, v65
	v_cvt_pk_f16_f32 v76, v76, v77
	v_cvt_pk_f16_f32 v77, v94, v95
	v_cvt_pk_f16_f32 v95, v102, v103
	s_waitcnt vmcnt(0)
	v_pk_add_f32 v[106:107], v[106:107], v[28:29]
	v_pk_add_f32 v[108:109], v[108:109], v[30:31]
	v_cvt_pk_f16_f32 v97, v124, v125
	v_cvt_pk_f16_f32 v102, v104, v105
	v_cvt_pk_f16_f32 v103, v118, v119
	v_pack_b32_f16 v64, v82, v65
	v_alignbit_b32 v65, v49, v65, 16
	v_pack_b32_f16 v94, v98, v95
	v_alignbit_b32 v95, v41, v95, 16
	v_add_f32_e32 v78, v78, v28
	v_cvt_pk_f16_f32 v106, v106, v107
	v_cvt_pk_f16_f32 v107, v108, v109
	ds_write2_b64 v130, v[74:75], v[96:97] offset1:4
	ds_write_b64 v130, v[106:107] offset:64
	v_pack_b32_f16 v74, v50, v76
	v_alignbit_b32 v75, v85, v76, 16
	v_pack_b32_f16 v76, v90, v77
	v_alignbit_b32 v77, v93, v77, 16
	v_pack_b32_f16 v96, v42, v102
	v_alignbit_b32 v97, v101, v102, 16
	v_pack_b32_f16 v102, v122, v103
	v_alignbit_b32 v103, v123, v103, 16
	ds_write2_b64 v132, v[64:65], v[94:95] offset0:32 offset1:36
	ds_write2_b64 v131, v[74:75], v[96:97] offset0:64 offset1:68
	ds_write2_b64 v91, v[76:77], v[102:103] offset0:96 offset1:100
	v_pk_mov_b32 v[64:65], v[28:29], v[30:31] op_sel:[1,0]
	v_add_f32_e32 v29, v81, v31
	v_cvt_f16_f32_e32 v78, v78
	v_cvt_f16_f32_e32 v29, v29
	v_mov_b32_e32 v74, v79
	v_mov_b32_e32 v75, v80
	v_pk_add_f32 v[74:75], v[74:75], v[64:65]
	v_add_f32_e32 v56, v56, v48
	v_cvt_pk_f16_f32 v30, v74, v75
	v_pack_b32_f16 v74, v78, v30
	v_alignbit_b32 v75, v29, v30, 16
	v_add_f32_e32 v29, v86, v28
	v_add_f32_e32 v30, v89, v31
	v_cvt_f16_f32_e32 v29, v29
	v_cvt_f16_f32_e32 v30, v30
	ds_write_b64 v130, v[74:75] offset:12608
	v_mov_b32_e32 v74, v87
	v_mov_b32_e32 v75, v88
	v_pk_add_f32 v[74:75], v[74:75], v[64:65]
	v_add_f32_e32 v52, v52, v48
	v_cvt_pk_f16_f32 v41, v74, v75
	v_pack_b32_f16 v74, v29, v41
	v_alignbit_b32 v75, v30, v41, 16
	v_add_f32_e32 v29, v60, v28
	v_add_f32_e32 v30, v63, v31
	v_cvt_f16_f32_e32 v29, v29
	v_cvt_f16_f32_e32 v30, v30
	v_mov_b32_e32 v60, v61
	v_mov_b32_e32 v61, v62
	v_pk_add_f32 v[60:61], v[60:61], v[64:65]
	ds_write_b64 v130, v[74:75] offset:25152
	v_cvt_pk_f16_f32 v41, v60, v61
	v_pack_b32_f16 v60, v29, v41
	v_alignbit_b32 v61, v30, v41, 16
	ds_write_b64 v130, v[60:61] offset:37696
	s_waitcnt lgkmcnt(0)
	s_barrier
	ds_read_b128 v[60:63], v83
	ds_read_b128 v[74:77], v84
	v_add_u32_e32 v29, 0x300, v111
	v_add_u32_e32 v30, v29, v112
	v_add_f32_e32 v44, v44, v48
	s_waitcnt lgkmcnt(1)
	buffer_store_dwordx4 v[60:63], v30, s[0:3], 0 offen sc1
	v_add_u32_e32 v30, 0x300, v113
	ds_read_b128 v[60:63], v92
	v_add_u32_e32 v41, v30, v114
	s_waitcnt lgkmcnt(1)
	buffer_store_dwordx4 v[74:77], v41, s[0:3], 0 offen sc1
	ds_read_b128 v[74:77], v99
	v_add_u32_e32 v41, 0x300, v115
	v_add_u32_e32 v42, v41, v116
	s_waitcnt lgkmcnt(1)
	buffer_store_dwordx4 v[60:63], v42, s[0:3], 0 offen sc1
	v_add_u32_e32 v42, 0x300, v117
	ds_read_b128 v[60:63], v100
	v_add_u32_e32 v49, v42, v142
	s_waitcnt lgkmcnt(1)
	buffer_store_dwordx4 v[74:77], v49, s[0:3], 0 offen sc1
	ds_read_b128 v[74:77], v110
	v_add_u32_e32 v49, 0x300, v144
	v_add_u32_e32 v50, v49, v143
	s_waitcnt lgkmcnt(1)
	buffer_store_dwordx4 v[60:63], v50, s[0:3], 0 offen sc1
	v_add_u32_e32 v50, 0x300, v145
	v_add_f32_e32 v36, v36, v48
	v_add_u32_e32 v60, v50, v146
	s_waitcnt lgkmcnt(0)
	buffer_store_dwordx4 v[74:77], v60, s[0:3], 0 offen sc1
	v_cvt_f16_f32_e32 v60, v56
	v_mov_b32_e32 v56, v57
	v_mov_b32_e32 v57, v58
	v_add_f32_e32 v58, v59, v51
	v_cvt_f16_f32_e32 v58, v58
	v_pk_add_f32 v[56:57], v[56:57], v[120:121]
	v_add_f32_e32 v32, v32, v40
	v_cvt_pk_f16_f32 v57, v56, v57
	v_pack_b32_f16 v56, v60, v57
	v_alignbit_b32 v57, v58, v57, 16
	v_cvt_f16_f32_e32 v58, v52
	v_mov_b32_e32 v52, v53
	v_mov_b32_e32 v53, v54
	v_add_f32_e32 v54, v55, v51
	v_cvt_f16_f32_e32 v54, v54
	v_pk_add_f32 v[52:53], v[52:53], v[120:121]
	v_add_f32_e32 v24, v24, v40
	v_cvt_pk_f16_f32 v53, v52, v53
	v_pack_b32_f16 v52, v58, v53
	v_alignbit_b32 v53, v54, v53, 16
	v_cvt_f16_f32_e32 v54, v44
	v_mov_b32_e32 v44, v45
	v_mov_b32_e32 v45, v46
	v_add_f32_e32 v46, v47, v51
	v_cvt_f16_f32_e32 v46, v46
	v_pk_add_f32 v[44:45], v[44:45], v[120:121]
	s_nop 0
	v_cvt_pk_f16_f32 v45, v44, v45
	v_pack_b32_f16 v44, v54, v45
	v_alignbit_b32 v45, v46, v45, 16
	v_cvt_f16_f32_e32 v46, v36
	v_mov_b32_e32 v36, v37
	v_mov_b32_e32 v37, v38
	v_add_f32_e32 v38, v39, v51
	v_cvt_f16_f32_e32 v38, v38
	v_pk_add_f32 v[36:37], v[36:37], v[120:121]
	s_barrier
	v_cvt_pk_f16_f32 v37, v36, v37
	v_pack_b32_f16 v36, v46, v37
	v_alignbit_b32 v37, v38, v37, 16
	v_cvt_f16_f32_e32 v38, v32
	v_mov_b32_e32 v32, v33
	v_mov_b32_e32 v33, v34
	v_add_f32_e32 v34, v35, v43
	v_cvt_f16_f32_e32 v34, v34
	v_pk_add_f32 v[32:33], v[32:33], v[66:67]
	s_nop 0
	v_cvt_pk_f16_f32 v33, v32, v33
	v_pack_b32_f16 v32, v38, v33
	v_alignbit_b32 v33, v34, v33, 16
	ds_write2_b64 v130, v[56:57], v[32:33] offset1:4
	v_cvt_f16_f32_e32 v32, v24
	v_mov_b32_e32 v24, v25
	v_mov_b32_e32 v25, v26
	v_add_f32_e32 v26, v27, v43
	v_cvt_f16_f32_e32 v26, v26
	v_pk_add_f32 v[24:25], v[24:25], v[66:67]
	v_add_f32_e32 v20, v20, v40
	v_cvt_pk_f16_f32 v25, v24, v25
	v_pack_b32_f16 v24, v32, v25
	v_alignbit_b32 v25, v26, v25, 16
	ds_write2_b64 v132, v[52:53], v[24:25] offset0:32 offset1:36
	v_cvt_f16_f32_e32 v24, v20
	v_mov_b32_e32 v20, v21
	v_mov_b32_e32 v21, v22
	v_add_f32_e32 v22, v23, v43
	v_cvt_f16_f32_e32 v22, v22
	v_pk_add_f32 v[20:21], v[20:21], v[66:67]
	v_add_f32_e32 v16, v16, v40
	v_cvt_pk_f16_f32 v21, v20, v21
	v_pack_b32_f16 v20, v24, v21
	v_alignbit_b32 v21, v22, v21, 16
	ds_write2_b64 v131, v[44:45], v[20:21] offset0:64 offset1:68
	v_cvt_f16_f32_e32 v20, v16
	v_mov_b32_e32 v16, v17
	v_mov_b32_e32 v17, v18
	v_add_f32_e32 v18, v19, v43
	v_cvt_f16_f32_e32 v18, v18
	v_pk_add_f32 v[16:17], v[16:17], v[66:67]
	v_add_f32_e32 v12, v12, v28
	v_cvt_pk_f16_f32 v17, v16, v17
	v_pack_b32_f16 v16, v20, v17
	v_alignbit_b32 v17, v18, v17, 16
	ds_write2_b64 v91, v[36:37], v[16:17] offset0:96 offset1:100
	v_cvt_f16_f32_e32 v16, v12
	v_mov_b32_e32 v12, v13
	v_mov_b32_e32 v13, v14
	v_add_f32_e32 v14, v15, v31
	v_cvt_f16_f32_e32 v14, v14
	v_pk_add_f32 v[12:13], v[12:13], v[64:65]
	v_add_f32_e32 v8, v8, v28
	v_cvt_pk_f16_f32 v13, v12, v13
	v_pack_b32_f16 v12, v16, v13
	v_alignbit_b32 v13, v14, v13, 16
	ds_write_b64 v130, v[12:13] offset:64
	v_cvt_f16_f32_e32 v12, v8
	v_mov_b32_e32 v8, v9
	v_mov_b32_e32 v9, v10
	v_add_f32_e32 v10, v11, v31
	v_cvt_f16_f32_e32 v10, v10
	v_pk_add_f32 v[8:9], v[8:9], v[64:65]
	v_add_f32_e32 v4, v4, v28
	v_cvt_pk_f16_f32 v9, v8, v9
	v_pack_b32_f16 v8, v12, v9
	v_alignbit_b32 v9, v10, v9, 16
	ds_write_b64 v130, v[8:9] offset:12608
	v_cvt_f16_f32_e32 v8, v4
	v_mov_b32_e32 v4, v5
	v_mov_b32_e32 v5, v6
	v_add_f32_e32 v6, v7, v31
	v_cvt_f16_f32_e32 v6, v6
	v_pk_add_f32 v[4:5], v[4:5], v[64:65]
	v_add_f32_e32 v0, v0, v28
	v_cvt_pk_f16_f32 v5, v4, v5
	v_pack_b32_f16 v4, v8, v5
	v_alignbit_b32 v5, v6, v5, 16
	ds_write_b64 v130, v[4:5] offset:25152
	v_cvt_f16_f32_e32 v4, v0
	v_mov_b32_e32 v0, v1
	v_mov_b32_e32 v1, v2
	v_add_f32_e32 v2, v3, v31
	v_cvt_f16_f32_e32 v2, v2
	v_pk_add_f32 v[0:1], v[0:1], v[64:65]
	v_add_u32_e32 v8, v29, v68
	v_cvt_pk_f16_f32 v1, v0, v1
	v_pack_b32_f16 v0, v4, v1
	v_alignbit_b32 v1, v2, v1, 16
	ds_write_b64 v130, v[0:1] offset:37696
	s_waitcnt lgkmcnt(0)
	s_barrier
	ds_read_b128 v[0:3], v83
	ds_read_b128 v[4:7], v84
	v_add_u32_e32 v12, v42, v70
	s_waitcnt lgkmcnt(1)
	buffer_store_dwordx4 v[0:3], v8, s[0:3], 0 offen sc1
	ds_read_b128 v[0:3], v92
	v_add_u32_e32 v8, v30, v69
	s_waitcnt lgkmcnt(1)
	buffer_store_dwordx4 v[4:7], v8, s[0:3], 0 offen sc1
	v_add_u32_e32 v8, v41, v72
	ds_read_b128 v[4:7], v99
	s_waitcnt lgkmcnt(1)
	buffer_store_dwordx4 v[0:3], v8, s[0:3], 0 offen sc1
	ds_read_b128 v[0:3], v100
	ds_read_b128 v[8:11], v110
	s_waitcnt lgkmcnt(2)
	buffer_store_dwordx4 v[4:7], v12, s[0:3], 0 offen sc1
	s_nop 1
	v_add_u32_e32 v4, v49, v71
	s_waitcnt lgkmcnt(1)
	buffer_store_dwordx4 v[0:3], v4, s[0:3], 0 offen sc1
	s_nop 1
	v_add_u32_e32 v0, v50, v73
	s_waitcnt lgkmcnt(0)
	buffer_store_dwordx4 v[8:11], v0, s[0:3], 0 offen sc1
	s_endpgm
	.p2alignl 8, 3212836864

.LBB4_4:
	global_load_dwordx4 v[2:5], v[170:171], off
	global_load_dwordx4 v[8:11], v[172:173], off
	global_load_dwordx4 v[210:213], v[170:171], off offset:16
	global_load_dwordx4 v[214:217], v[172:173], off offset:16
	s_lshl_b32 s48, s46, 3
	s_add_i32 s48, s48, s44
	v_or_b32_e32 v199, s48, v178
	v_add_u32_e32 v168, v199, v181
	v_add_u32_e32 v201, -1, v199
	v_mul_u32_u24_e32 v6, s47, v168
	v_or_b32_e32 v7, v201, v182
	v_or_b32_e32 v6, v6, v166
	s_mov_b64 s[4:5], -1
	s_and_b64 vcc, exec, s[26:27]
	v_cmp_gt_u32_e64 s[2:3], 64, v7
	v_lshlrev_b32_e32 v200, 1, v6
	s_cbranch_vccz .LBB4_42
	global_load_dwordx3 v[154:156], v169, s[10:11]
	v_cmp_lt_u32_e64 s[64:65], 0, v199
	v_cmp_gt_u32_e64 s[66:67], 63, v199
	v_cmp_lt_u32_e64 s[68:69], 0, v180
	v_cmp_gt_u32_e64 s[70:71], 60, v180
	buffer_load_dwordx4 v[206:209], v200, s[36:39], 0 offen
	s_and_b64 s[72:73], s[68:69], s[64:65]
	s_and_b64 s[74:75], s[68:69], s[66:67]
	s_and_b64 s[76:77], s[70:71], s[64:65]
	s_and_b64 s[78:79], s[70:71], s[66:67]
	v_add_u32_e32 v245, 0xfffe7c00, v200
	v_add_u32_e32 v246, 0xfffe8000, v200
	s_mov_b64 exec, s[72:73]
	buffer_load_dwordx4 v[122:125], v245, s[36:39], 0 offen
	buffer_load_dwordx4 v[82:85], v245, s[36:39], 0 offen offset:512
	s_mov_b64 exec, -1
	s_mov_b64 exec, s[68:69]
	buffer_load_dwordx4 v[138:141], v246, s[36:39], 0 offen offset:512
	buffer_load_dwordx4 v[106:109], v246, s[36:39], 0 offen offset:1024
	s_mov_b64 exec, -1
	s_mov_b64 exec, s[74:75]
	buffer_load_dwordx4 v[146:149], v246, s[36:39], 0 offen offset:2048
	buffer_load_dwordx4 v[126:129], v246, s[36:39], 0 offen offset:2560
	s_mov_b64 exec, -1
	v_add_u32_e32 v245, 0xfffffc00, v200
	s_mov_b64 exec, s[64:65]
	buffer_load_dwordx4 v[94:97], v245, s[36:39], 0 offen
	buffer_load_dwordx4 v[54:57], v245, s[36:39], 0 offen offset:512
	s_mov_b64 exec, -1
	buffer_load_dwordx4 v[118:121], v200, s[36:39], 0 offen offset:512
	buffer_load_dwordx4 v[74:77], v200, s[36:39], 0 offen offset:1024
	s_mov_b64 exec, s[66:67]
	buffer_load_dwordx4 v[134:137], v200, s[36:39], 0 offen offset:2048
	buffer_load_dwordx4 v[98:101], v200, s[36:39], 0 offen offset:2560
	s_mov_b64 exec, -1
	v_add_u32_e32 v245, 0x17c00, v200
	v_add_u32_e32 v246, 0x18000, v200
	s_mov_b64 exec, s[64:65]
	buffer_load_dwordx4 v[62:65], v245, s[36:39], 0 offen
	buffer_load_dwordx4 v[30:33], v245, s[36:39], 0 offen offset:512
	s_mov_b64 exec, -1
	buffer_load_dwordx4 v[78:81], v246, s[36:39], 0 offen offset:512
	buffer_load_dwordx4 v[42:45], v246, s[36:39], 0 offen offset:1024
	s_mov_b64 exec, s[66:67]
	buffer_load_dwordx4 v[102:105], v246, s[36:39], 0 offen offset:2048
	buffer_load_dwordx4 v[58:61], v246, s[36:39], 0 offen offset:2560
	s_mov_b64 exec, -1
	v_add_u32_e32 v245, 0x18000, v200
	buffer_load_dwordx4 v[162:165], v245, s[36:39], 0 offen
	v_add_u32_e32 v246, 0x30000, v200
	buffer_load_dwordx4 v[158:161], v246, s[36:39], 0 offen
	v_add_u32_e32 v245, 0x2fc00, v200
	v_add_u32_e32 v246, 0x30000, v200
	v_add_u32_e32 v247, 0x47c00, v200
	v_add_u32_e32 v248, 0x48000, v200
	v_add_u32_e32 v249, 0x5fc00, v200
	v_add_u32_e32 v250, 0x60000, v200
	s_waitcnt vmcnt(22)
	v_cvt_pk_f16_f32 v6, v2, v3
	v_cvt_pk_f16_f32 v2, v8, v9
	v_cvt_pk_f16_f32 v7, v4, v5
	v_cvt_pk_f16_f32 v3, v10, v11
	v_cvt_pk_f16_f32 v8, v210, v211
	v_cvt_pk_f16_f32 v4, v214, v215
	v_cvt_pk_f16_f32 v9, v212, v213
	v_cvt_pk_f16_f32 v5, v216, v217
	s_not_b64 exec, s[72:73]
	s_cbranch_execz .Lmyf_C1_0
	v_mov_b32_e32 v122, v6
	v_mov_b32_e32 v123, v7
	v_mov_b32_e32 v124, v8
	v_mov_b32_e32 v125, v9
	v_mov_b32_e32 v82, v2
	v_mov_b32_e32 v83, v3
	v_mov_b32_e32 v84, v4
	v_mov_b32_e32 v85, v5

.LBB4_155:
	s_setprio 0
	s_load_dword s0, s[0:1], 0x88
	s_lshl_b32 s1, s45, 6
	s_and_b32 s1, s1, 0xfffffe00
	s_or_b32 s2, s1, s44
	v_readfirstlane_b32 s4, v0
	s_waitcnt lgkmcnt(0)
	s_mul_i32 s3, s0, 0x60000
	s_mul_hi_i32 s1, s0, 0x60000
	s_add_u32 s3, s28, s3
	s_mulk_i32 s0, 0x300
	s_addc_u32 s5, s29, s1
	s_ashr_i32 s1, s0, 31
	s_lshl_b64 s[0:1], s[0:1], 2
	s_add_u32 s0, s30, s0
	s_addc_u32 s1, s31, s1
	s_lshr_b32 s6, s4, 6
	s_and_b32 s25, s25, 0xffff
	s_mul_i32 s4, s6, 0x6000
	v_and_b32_e32 v2, 63, v0
	s_mul_hi_u32 s7, s6, 0x6000
	s_add_u32 s4, s3, s4
	s_addc_u32 s5, s5, s7
	v_lshlrev_b32_e32 v56, 4, v2
	v_mov_b32_e32 v57, 0
	v_lshl_add_u64 v[54:55], s[4:5], 0, v[56:57]
	s_movk_i32 s3, 0x1000
	v_add_co_u32_e32 v50, vcc, s3, v54
	s_movk_i32 s3, 0x2000
	s_nop 0
	v_addc_co_u32_e32 v51, vcc, 0, v55, vcc
	v_add_co_u32_e32 v52, vcc, s3, v54
	global_load_dwordx4 v[2:5], v56, s[4:5] offset:1024
	global_load_dwordx4 v[6:9], v56, s[4:5] offset:2048
	v_addc_co_u32_e32 v53, vcc, 0, v55, vcc
	global_load_dwordx4 v[10:13], v56, s[4:5] offset:3072
	global_load_dwordx4 v[14:17], v[52:53], off offset:-4096
	global_load_dwordx4 v[18:21], v[50:51], off offset:1024
	global_load_dwordx4 v[22:25], v[50:51], off offset:2048
	global_load_dwordx4 v[26:29], v56, s[4:5]
	global_load_dwordx4 v[30:33], v[50:51], off offset:3072
	global_load_dwordx4 v[34:37], v[52:53], off
	global_load_dwordx4 v[38:41], v[52:53], off offset:1024
	global_load_dwordx4 v[42:45], v[52:53], off offset:2048
	global_load_dwordx4 v[46:49], v[52:53], off offset:3072
	s_movk_i32 s3, 0x3000
	v_add_co_u32_e32 v58, vcc, s3, v54
	s_movk_i32 s3, 0x4000
	s_nop 0
	v_addc_co_u32_e32 v59, vcc, 0, v55, vcc
	v_add_co_u32_e32 v140, vcc, s3, v54
	s_nop 1
	v_addc_co_u32_e32 v141, vcc, 0, v55, vcc
	s_barrier
	global_load_dwordx4 v[50:53], v[140:141], off offset:-4096
	global_load_dwordx4 v[62:65], v[58:59], off offset:1024
	global_load_dwordx4 v[68:71], v[58:59], off offset:2048
	v_lshlrev_b32_e32 v67, 9, v1
	v_xor_b32_e32 v61, v167, v1
	v_lshl_or_b32 v66, v61, 4, v67
	ds_read_b128 v[72:75], v66
	ds_read_b128 v[76:79], v66 offset:8192
	ds_read_b128 v[80:83], v66 offset:16384
	ds_read_b128 v[84:87], v66 offset:24576
	v_mul_u32_u24_e32 v60, 0x556, v0
	v_lshrrev_b32_e32 v60, 16, v60
	s_mul_i32 s3, s6, 48
	v_lshlrev_b32_e32 v61, 3, v60
	s_movk_i32 s5, 0x47
	v_lshl_or_b32 v56, v167, 2, s3
	s_mov_b32 s3, 0xfffffd0
	v_bitop3_b32 v61, v61, s5, v60 bitop3:0xc8
	s_mov_b32 s27, 0x20000
	s_mov_b32 s26, 0x1800000
	s_mul_i32 s4, s6, 0x60
	v_mul_i32_i24_e32 v150, s3, v60
	v_or_b32_e32 v61, s2, v61
	s_waitcnt vmcnt(8) lgkmcnt(3)
	v_mfma_f32_16x16x32_f16 v[88:91], v[26:29], v[72:75], 0
	s_waitcnt lgkmcnt(2)
	v_mfma_f32_16x16x32_f16 v[92:95], v[26:29], v[76:79], 0
	s_waitcnt lgkmcnt(1)
	v_mfma_f32_16x16x32_f16 v[96:99], v[26:29], v[80:83], 0
	s_waitcnt lgkmcnt(0)
	v_mfma_f32_16x16x32_f16 v[26:29], v[26:29], v[84:87], 0
	v_mfma_f32_16x16x32_f16 v[100:103], v[2:5], v[72:75], 0
	v_mfma_f32_16x16x32_f16 v[104:107], v[2:5], v[76:79], 0
	v_mfma_f32_16x16x32_f16 v[108:111], v[2:5], v[80:83], 0
	v_mfma_f32_16x16x32_f16 v[2:5], v[2:5], v[84:87], 0
	v_mfma_f32_16x16x32_f16 v[112:115], v[6:9], v[72:75], 0
	v_mfma_f32_16x16x32_f16 v[74:77], v[6:9], v[76:79], 0
	v_mfma_f32_16x16x32_f16 v[78:81], v[6:9], v[80:83], 0
	v_mfma_f32_16x16x32_f16 v[6:9], v[6:9], v[84:87], 0
	global_load_dwordx4 v[82:85], v[58:59], off offset:3072
	global_load_dwordx4 v[116:119], v[140:141], off
	global_load_dwordx4 v[120:123], v[140:141], off offset:1024
	v_bitop3_b32 v58, v167, v1, 4 bitop3:0x36
	v_lshl_or_b32 v72, v58, 4, v67
	ds_read_b128 v[124:127], v72
	ds_read_b128 v[128:131], v72 offset:8192
	ds_read_b128 v[132:135], v72 offset:16384
	ds_read_b128 v[136:139], v72 offset:24576
	s_waitcnt lgkmcnt(3)
	v_mfma_f32_16x16x32_f16 v[86:89], v[10:13], v[124:127], v[88:91]
	s_waitcnt lgkmcnt(2)
	v_mfma_f32_16x16x32_f16 v[90:93], v[10:13], v[128:131], v[92:95]
	s_waitcnt lgkmcnt(1)
	v_mfma_f32_16x16x32_f16 v[94:97], v[10:13], v[132:135], v[96:99]
	s_waitcnt lgkmcnt(0)
	v_mfma_f32_16x16x32_f16 v[10:13], v[10:13], v[136:139], v[26:29]
	v_mfma_f32_16x16x32_f16 v[26:29], v[14:17], v[124:127], v[100:103]
	v_mfma_f32_16x16x32_f16 v[98:101], v[14:17], v[128:131], v[104:107]
	v_mfma_f32_16x16x32_f16 v[102:105], v[14:17], v[132:135], v[108:111]
	v_mfma_f32_16x16x32_f16 v[2:5], v[14:17], v[136:139], v[2:5]
	v_mfma_f32_16x16x32_f16 v[14:17], v[18:21], v[124:127], v[112:115]
	v_mfma_f32_16x16x32_f16 v[106:109], v[18:21], v[128:131], v[74:77]
	v_mfma_f32_16x16x32_f16 v[76:79], v[18:21], v[132:135], v[78:81]
	v_mfma_f32_16x16x32_f16 v[6:9], v[18:21], v[136:139], v[6:9]
	s_movk_i32 s5, 0x5000
	v_add_co_u32_e32 v58, vcc, s5, v54
	global_load_dwordx4 v[110:113], v[140:141], off offset:2048
	global_load_dwordx4 v[124:127], v[140:141], off offset:3072
	v_addc_co_u32_e32 v59, vcc, 0, v55, vcc
	global_load_dwordx4 v[128:131], v[58:59], off
	v_bitop3_b32 v18, v167, v1, 8 bitop3:0x36
	v_lshl_or_b32 v74, v18, 4, v67
	ds_read_b128 v[18:21], v74
	ds_read_b128 v[132:135], v74 offset:8192
	ds_read_b128 v[136:139], v74 offset:16384
	ds_read_b128 v[140:143], v74 offset:24576
	s_waitcnt lgkmcnt(3)
	v_mfma_f32_16x16x32_f16 v[86:89], v[22:25], v[18:21], v[86:89]
	s_waitcnt lgkmcnt(2)
	v_mfma_f32_16x16x32_f16 v[90:93], v[22:25], v[132:135], v[90:93]
	s_waitcnt lgkmcnt(1)
	v_mfma_f32_16x16x32_f16 v[94:97], v[22:25], v[136:139], v[94:97]
	s_waitcnt lgkmcnt(0)
	v_mfma_f32_16x16x32_f16 v[10:13], v[22:25], v[140:143], v[10:13]
	s_waitcnt vmcnt(13)
	v_mfma_f32_16x16x32_f16 v[22:25], v[30:33], v[18:21], v[26:29]
	v_mfma_f32_16x16x32_f16 v[26:29], v[30:33], v[132:135], v[98:101]
	v_mfma_f32_16x16x32_f16 v[98:101], v[30:33], v[136:139], v[102:105]
	v_mfma_f32_16x16x32_f16 v[2:5], v[30:33], v[140:143], v[2:5]
	s_waitcnt vmcnt(12)
	v_mfma_f32_16x16x32_f16 v[14:17], v[34:37], v[18:21], v[14:17]
	v_mfma_f32_16x16x32_f16 v[18:21], v[34:37], v[132:135], v[106:109]
	v_mfma_f32_16x16x32_f16 v[30:33], v[34:37], v[136:139], v[76:79]
	v_mfma_f32_16x16x32_f16 v[6:9], v[34:37], v[140:143], v[6:9]
	global_load_dwordx4 v[102:105], v[58:59], off offset:1024
	global_load_dwordx4 v[106:109], v[58:59], off offset:2048
	global_load_dwordx4 v[132:135], v[58:59], off offset:3072
	v_bitop3_b32 v34, v167, v1, 12 bitop3:0x36
	v_lshl_or_b32 v75, v34, 4, v67
	ds_read_b128 v[34:37], v75
	ds_read_b128 v[76:79], v75 offset:8192
	ds_read_b128 v[136:139], v75 offset:16384
	ds_read_b128 v[140:143], v75 offset:24576
	s_waitcnt vmcnt(14) lgkmcnt(3)
	v_mfma_f32_16x16x32_f16 v[86:89], v[38:41], v[34:37], v[86:89]
	s_waitcnt lgkmcnt(2)
	v_mfma_f32_16x16x32_f16 v[90:93], v[38:41], v[76:79], v[90:93]
	s_waitcnt lgkmcnt(1)
	v_mfma_f32_16x16x32_f16 v[94:97], v[38:41], v[136:139], v[94:97]
	s_waitcnt lgkmcnt(0)
	v_mfma_f32_16x16x32_f16 v[10:13], v[38:41], v[140:143], v[10:13]
	s_waitcnt vmcnt(13)
	v_mfma_f32_16x16x32_f16 v[38:41], v[42:45], v[34:37], v[22:25]
	v_mfma_f32_16x16x32_f16 v[144:147], v[42:45], v[76:79], v[26:29]
	v_mfma_f32_16x16x32_f16 v[98:101], v[42:45], v[136:139], v[98:101]
	v_mfma_f32_16x16x32_f16 v[2:5], v[42:45], v[140:143], v[2:5]
	s_waitcnt vmcnt(12)
	v_mfma_f32_16x16x32_f16 v[14:17], v[46:49], v[34:37], v[14:17]
	v_mfma_f32_16x16x32_f16 v[18:21], v[46:49], v[76:79], v[18:21]
	v_mfma_f32_16x16x32_f16 v[30:33], v[46:49], v[136:139], v[30:33]
	v_mfma_f32_16x16x32_f16 v[6:9], v[46:49], v[140:143], v[6:9]
	s_mov_b32 s5, 0x30000
	v_add_co_u32_e32 v58, vcc, s5, v54
	s_mov_b32 s5, 0x31000
	s_nop 0
	v_addc_co_u32_e32 v59, vcc, 0, v55, vcc
	v_add_co_u32_e32 v148, vcc, s5, v54
	v_bitop3_b32 v42, v167, v1, 16 bitop3:0x36
	s_nop 0
	v_addc_co_u32_e32 v149, vcc, 0, v55, vcc
	global_load_dwordx4 v[34:37], v[148:149], off offset:-4096
	global_load_dwordx4 v[26:29], v[58:59], off offset:1024
	global_load_dwordx4 v[22:25], v[58:59], off offset:2048
	v_lshl_or_b32 v76, v42, 4, v67
	ds_read_b128 v[42:45], v76
	ds_read_b128 v[46:49], v76 offset:8192
	ds_read_b128 v[78:81], v76 offset:16384
	ds_read_b128 v[136:139], v76 offset:24576
	s_waitcnt vmcnt(14) lgkmcnt(3)
	v_mfma_f32_16x16x32_f16 v[86:89], v[50:53], v[42:45], v[86:89]
	s_waitcnt lgkmcnt(2)
	v_mfma_f32_16x16x32_f16 v[90:93], v[50:53], v[46:49], v[90:93]
	s_waitcnt lgkmcnt(1)
	v_mfma_f32_16x16x32_f16 v[94:97], v[50:53], v[78:81], v[94:97]
	s_waitcnt lgkmcnt(0)
	v_mfma_f32_16x16x32_f16 v[10:13], v[50:53], v[136:139], v[10:13]
	s_waitcnt vmcnt(13)
	v_mfma_f32_16x16x32_f16 v[38:41], v[62:65], v[42:45], v[38:41]
	v_mfma_f32_16x16x32_f16 v[50:53], v[62:65], v[46:49], v[144:147]
	v_mfma_f32_16x16x32_f16 v[98:101], v[62:65], v[78:81], v[98:101]
	v_mfma_f32_16x16x32_f16 v[62:65], v[62:65], v[136:139], v[2:5]
	s_waitcnt vmcnt(12)
	v_mfma_f32_16x16x32_f16 v[42:45], v[68:71], v[42:45], v[14:17]
	v_mfma_f32_16x16x32_f16 v[18:21], v[68:71], v[46:49], v[18:21]
	v_mfma_f32_16x16x32_f16 v[30:33], v[68:71], v[78:81], v[30:33]
	v_mfma_f32_16x16x32_f16 v[46:49], v[68:71], v[136:139], v[6:9]
	global_load_dwordx4 v[14:17], v[58:59], off offset:3072
	s_nop 1
	global_load_dwordx4 v[6:9], v[148:149], off
	global_load_dwordx4 v[2:5], v[148:149], off offset:1024
	v_bitop3_b32 v58, v167, v1, 20 bitop3:0x36
	v_lshl_or_b32 v77, v58, 4, v67
	ds_read_b128 v[68:71], v77
	ds_read_b128 v[78:81], v77 offset:8192
	ds_read_b128 v[136:139], v77 offset:16384
	ds_read_b128 v[140:143], v77 offset:24576
	s_waitcnt vmcnt(14) lgkmcnt(3)
	v_mfma_f32_16x16x32_f16 v[86:89], v[82:85], v[68:71], v[86:89]
	s_waitcnt lgkmcnt(2)
	v_mfma_f32_16x16x32_f16 v[90:93], v[82:85], v[78:81], v[90:93]
	s_waitcnt lgkmcnt(1)
	v_mfma_f32_16x16x32_f16 v[94:97], v[82:85], v[136:139], v[94:97]
	s_waitcnt lgkmcnt(0)
	v_mfma_f32_16x16x32_f16 v[82:85], v[82:85], v[140:143], v[10:13]
	s_waitcnt vmcnt(13)
	v_mfma_f32_16x16x32_f16 v[38:41], v[116:119], v[68:71], v[38:41]
	v_mfma_f32_16x16x32_f16 v[50:53], v[116:119], v[78:81], v[50:53]
	v_mfma_f32_16x16x32_f16 v[98:101], v[116:119], v[136:139], v[98:101]
	v_mfma_f32_16x16x32_f16 v[62:65], v[116:119], v[140:143], v[62:65]
	s_waitcnt vmcnt(12)
	v_mfma_f32_16x16x32_f16 v[42:45], v[120:123], v[68:71], v[42:45]
	v_mfma_f32_16x16x32_f16 v[68:71], v[120:123], v[78:81], v[18:21]
	v_mfma_f32_16x16x32_f16 v[114:117], v[120:123], v[136:139], v[30:33]
	v_mfma_f32_16x16x32_f16 v[46:49], v[120:123], v[140:143], v[46:49]
	s_mov_b32 s5, 0x33000
	v_add_co_u32_e32 v58, vcc, s5, v54
	global_load_dwordx4 v[18:21], v[148:149], off offset:2048
	global_load_dwordx4 v[10:13], v[148:149], off offset:3072
	v_addc_co_u32_e32 v59, vcc, 0, v55, vcc
	global_load_dwordx4 v[30:33], v[58:59], off offset:-4096
	v_bitop3_b32 v73, v167, v1, 24 bitop3:0x36
	v_lshl_or_b32 v78, v73, 4, v67
	ds_read_b128 v[118:121], v78
	ds_read_b128 v[136:139], v78 offset:8192
	ds_read_b128 v[140:143], v78 offset:16384
	ds_read_b128 v[144:147], v78 offset:24576
	s_mov_b32 s5, 0x32000
	v_add_co_u32_e32 v148, vcc, s5, v54
	s_nop 1
	v_addc_co_u32_e32 v149, vcc, 0, v55, vcc
	s_waitcnt vmcnt(14) lgkmcnt(3)
	v_mfma_f32_16x16x32_f16 v[86:89], v[110:113], v[118:121], v[86:89]
	s_waitcnt lgkmcnt(2)
	v_mfma_f32_16x16x32_f16 v[90:93], v[110:113], v[136:139], v[90:93]
	s_waitcnt lgkmcnt(1)
	v_mfma_f32_16x16x32_f16 v[94:97], v[110:113], v[140:143], v[94:97]
	s_waitcnt lgkmcnt(0)
	v_mfma_f32_16x16x32_f16 v[80:83], v[110:113], v[144:147], v[82:85]
	s_waitcnt vmcnt(13)
	v_mfma_f32_16x16x32_f16 v[110:113], v[124:127], v[118:121], v[38:41]
	v_mfma_f32_16x16x32_f16 v[50:53], v[124:127], v[136:139], v[50:53]
	v_mfma_f32_16x16x32_f16 v[98:101], v[124:127], v[140:143], v[98:101]
	v_mfma_f32_16x16x32_f16 v[62:65], v[124:127], v[144:147], v[62:65]
	s_waitcnt vmcnt(12)
	v_mfma_f32_16x16x32_f16 v[118:121], v[128:131], v[118:121], v[42:45]
	v_mfma_f32_16x16x32_f16 v[68:71], v[128:131], v[136:139], v[68:71]
	v_mfma_f32_16x16x32_f16 v[114:117], v[128:131], v[140:143], v[114:117]
	v_mfma_f32_16x16x32_f16 v[122:125], v[128:131], v[144:147], v[46:49]
	s_nop 2
	global_load_dwordx4 v[46:49], v[148:149], off offset:1024
	global_load_dwordx4 v[42:45], v[148:149], off offset:2048
	global_load_dwordx4 v[38:41], v[148:149], off offset:3072
	v_bitop3_b32 v73, v167, v1, 28 bitop3:0x36
	v_lshl_or_b32 v79, v73, 4, v67
	ds_read_b128 v[126:129], v79
	ds_read_b128 v[136:139], v79 offset:8192
	ds_read_b128 v[140:143], v79 offset:16384
	ds_read_b128 v[144:147], v79 offset:24576
	s_waitcnt vmcnt(14) lgkmcnt(3)
	v_mfma_f32_16x16x32_f16 v[84:87], v[102:105], v[126:129], v[86:89]
	s_waitcnt lgkmcnt(2)
	v_mfma_f32_16x16x32_f16 v[88:91], v[102:105], v[136:139], v[90:93]
	s_waitcnt lgkmcnt(1)
	v_mfma_f32_16x16x32_f16 v[92:95], v[102:105], v[140:143], v[94:97]
	s_waitcnt lgkmcnt(0)
	v_mfma_f32_16x16x32_f16 v[80:83], v[102:105], v[144:147], v[80:83]
	s_waitcnt vmcnt(13)
	v_mfma_f32_16x16x32_f16 v[102:105], v[106:109], v[126:129], v[110:113]
	v_mfma_f32_16x16x32_f16 v[110:113], v[106:109], v[136:139], v[50:53]
	v_mfma_f32_16x16x32_f16 v[96:99], v[106:109], v[140:143], v[98:101]
	v_mfma_f32_16x16x32_f16 v[62:65], v[106:109], v[144:147], v[62:65]
	s_waitcnt vmcnt(12)
	v_mfma_f32_16x16x32_f16 v[106:109], v[132:135], v[126:129], v[118:121]
	v_mfma_f32_16x16x32_f16 v[118:121], v[132:135], v[136:139], v[68:71]
	v_mfma_f32_16x16x32_f16 v[114:117], v[132:135], v[140:143], v[114:117]
	v_mfma_f32_16x16x32_f16 v[50:53], v[132:135], v[144:147], v[122:125]
	v_lshl_add_u64 v[56:57], v[56:57], 2, s[0:1]
	s_nop 1
	global_load_dwordx4 v[122:125], v[56:57], off
	global_load_dwordx4 v[126:129], v[56:57], off offset:64
	global_load_dwordx4 v[130:133], v[56:57], off offset:128
	v_lshl_or_b32 v67, v167, 3, s4
	s_movk_i32 s0, 0x310
	v_mov_b32_e32 v100, v89
	v_mov_b32_e32 v101, v90
	v_mov_b32_e32 v134, v93
	v_mov_b32_e32 v135, v94
	v_mov_b32_e32 v140, v97
	v_mov_b32_e32 v141, v98
	v_mad_u32_u24 v69, v1, s0, v67
	v_mov_b32_e32 v143, v64
	v_mov_b32_e32 v136, v81
	v_mov_b32_e32 v137, v82
	v_mov_b32_e32 v138, v111
	v_mov_b32_e32 v139, v112
	v_mov_b32_e32 v142, v63
	v_add_u32_e32 v73, 0x8000, v69
	s_barrier
	v_add_u32_e32 v70, 0xb000, v69
	v_add_u32_e32 v71, 0xe000, v69
	v_add_u32_e32 v68, 0x9300, v69
	s_movk_i32 s1, 0x600
	s_movk_i32 s6, 0x1c7
	s_waitcnt vmcnt(2)
	v_pk_add_f32 v[84:85], v[84:85], v[122:123]
	v_add_f32_e32 v1, v88, v122
	v_pk_mov_b32 v[88:89], v[122:123], v[124:125] op_sel:[1,0]
	v_add_f32_e32 v67, v91, v125
	v_add_f32_e32 v92, v92, v122
	v_add_f32_e32 v93, v95, v125
	v_add_f32_e32 v94, v80, v122
	v_add_f32_e32 v95, v83, v125
	s_waitcnt vmcnt(1)
	v_add_f32_e32 v97, v110, v126
	v_add_f32_e32 v98, v113, v129
	v_add_f32_e32 v96, v96, v126
	v_add_f32_e32 v99, v99, v129
	v_cvt_pk_f16_f32 v64, v84, v85
	v_cvt_f16_f32_e32 v1, v1
	v_pk_add_f32 v[84:85], v[100:101], v[88:89]
	v_cvt_f16_f32_e32 v67, v67
	v_cvt_f16_f32_e32 v100, v92
	v_cvt_f16_f32_e32 v101, v93
	v_cvt_f16_f32_e32 v94, v94
	v_cvt_f16_f32_e32 v95, v95
	v_cvt_f16_f32_e32 v97, v97
	v_cvt_f16_f32_e32 v98, v98
	v_pk_add_f32 v[86:87], v[86:87], v[124:125]
	v_pk_add_f32 v[80:81], v[102:103], v[126:127]
	v_pk_add_f32 v[82:83], v[104:105], v[128:129]
	v_pk_mov_b32 v[90:91], v[126:127], v[128:129] op_sel:[1,0]
	v_cvt_f16_f32_e32 v96, v96
	v_cvt_f16_f32_e32 v99, v99
	v_add_f32_e32 v102, v62, v126
	v_add_f32_e32 v103, v65, v129
	s_waitcnt vmcnt(0)
	v_pk_add_f32 v[62:63], v[106:107], v[130:131]
	v_cvt_pk_f16_f32 v65, v86, v87
	v_pk_add_f32 v[86:87], v[134:135], v[88:89]
	v_pk_add_f32 v[88:89], v[136:137], v[88:89]
	v_cvt_pk_f16_f32 v80, v80, v81
	v_cvt_pk_f16_f32 v81, v82, v83
	v_pk_add_f32 v[82:83], v[138:139], v[90:91]
	v_pk_add_f32 v[92:93], v[140:141], v[90:91]
	v_cvt_pk_f16_f32 v62, v62, v63
	v_cvt_pk_f16_f32 v63, v84, v85
	v_cvt_pk_f16_f32 v84, v86, v87
	v_cvt_pk_f16_f32 v85, v88, v89
	v_cvt_pk_f16_f32 v86, v82, v83
	v_cvt_pk_f16_f32 v87, v92, v93
	ds_write2_b64 v73, v[64:65], v[80:81] offset1:4
	v_pack_b32_f16 v64, v1, v63
	v_alignbit_b32 v65, v67, v63, 16
	v_pack_b32_f16 v80, v100, v84
	v_alignbit_b32 v81, v101, v84, 16
	v_pack_b32_f16 v82, v94, v85
	v_alignbit_b32 v83, v95, v85, 16
	v_pack_b32_f16 v84, v97, v86
	v_alignbit_b32 v85, v98, v86, 16
	v_pack_b32_f16 v86, v96, v87
	v_alignbit_b32 v87, v99, v87, 16
	ds_write2_b64 v70, v[64:65], v[84:85] offset0:32 offset1:36
	ds_write2_b64 v71, v[80:81], v[86:87] offset0:64 offset1:68
	v_pk_add_f32 v[64:65], v[108:109], v[132:133]
	v_add_f32_e32 v1, v118, v130
	v_cvt_pk_f16_f32 v63, v64, v65
	v_cvt_f16_f32_e32 v1, v1
	v_add_f32_e32 v67, v121, v133
	ds_write_b64 v69, v[62:63] offset:32832
	v_mov_b32_e32 v62, v119
	v_mov_b32_e32 v63, v120
	v_pk_mov_b32 v[64:65], v[130:131], v[132:133] op_sel:[1,0]
	v_cvt_f16_f32_e32 v67, v67
	v_pk_add_f32 v[62:63], v[62:63], v[64:65]
	v_cvt_f16_f32_e32 v102, v102
	v_cvt_pk_f16_f32 v63, v62, v63
	v_pack_b32_f16 v62, v1, v63
	v_add_f32_e32 v1, v114, v130
	v_alignbit_b32 v63, v67, v63, 16
	v_cvt_f16_f32_e32 v1, v1
	ds_write_b64 v69, v[62:63] offset:45376
	v_mov_b32_e32 v62, v115
	v_mov_b32_e32 v63, v116
	v_pk_add_f32 v[62:63], v[62:63], v[64:65]
	v_add_f32_e32 v67, v117, v133
	v_cvt_pk_f16_f32 v63, v62, v63
	v_pack_b32_f16 v62, v1, v63
	v_add_f32_e32 v1, v50, v130
	v_mov_b32_e32 v50, v51
	v_mov_b32_e32 v51, v52
	v_add_f32_e32 v52, v53, v133
	v_cvt_f16_f32_e32 v103, v103
	v_cvt_f16_f32_e32 v67, v67
	v_cvt_f16_f32_e32 v1, v1
	v_cvt_f16_f32_e32 v52, v52
	v_pk_add_f32 v[90:91], v[142:143], v[90:91]
	v_pk_add_f32 v[50:51], v[50:51], v[64:65]
	v_cvt_pk_f16_f32 v89, v90, v91
	v_cvt_pk_f16_f32 v51, v50, v51
	v_pack_b32_f16 v88, v102, v89
	v_alignbit_b32 v89, v103, v89, 16
	v_add_u32_e32 v80, 0x8000, v68
	v_alignbit_b32 v63, v67, v63, 16
	v_pack_b32_f16 v50, v1, v51
	v_alignbit_b32 v51, v52, v51, 16
	ds_write2_b64 v80, v[82:83], v[88:89] offset1:4
	ds_write_b64 v69, v[62:63] offset:57920
	ds_write_b64 v68, v[50:51] offset:32832
	s_waitcnt lgkmcnt(0)
	s_barrier
	global_load_dwordx4 v[82:85], v[58:59], off
	global_load_dwordx4 v[86:89], v[58:59], off offset:1024
	global_load_dwordx4 v[90:93], v[58:59], off offset:2048
	v_add_lshl_u32 v52, v150, v0, 4
	v_mad_u64_u32 v[50:51], s[4:5], v61, s1, v[52:53]
	v_or_b32_e32 v1, 0x200, v0
	v_mad_u32_u24 v51, v60, s0, v52
	v_mul_u32_u24_e32 v52, 0x556, v1
	v_lshrrev_b32_e32 v53, 16, v52
	v_mul_i32_i24_e32 v52, s3, v53
	v_add_lshl_u32 v52, v52, v1, 4
	v_lshlrev_b32_e32 v1, 3, v53
	s_movk_i32 s4, 0xc7
	ds_read_b128 v[60:63], v51 offset:32768
	v_bitop3_b32 v1, v1, s4, v53 bitop3:0xc8
	v_or_b32_e32 v1, s2, v1
	v_mad_u32_u24 v81, v53, s0, v52
	v_mad_u64_u32 v[52:53], s[4:5], v1, s1, v[52:53]
	v_or_b32_e32 v1, 0x400, v0
	v_mul_u32_u24_e32 v53, 0x556, v1
	v_lshrrev_b32_e32 v53, 16, v53
	ds_read_b128 v[94:97], v81 offset:32768
	s_waitcnt lgkmcnt(1)
	buffer_store_dwordx4 v[60:63], v50, s[24:27], 0 offen sc1
	s_waitcnt lgkmcnt(0)
	buffer_store_dwordx4 v[94:97], v52, s[24:27], 0 offen sc1
	v_lshlrev_b32_e32 v61, 3, v53
	v_mul_i32_i24_e32 v60, s3, v53
	v_bitop3_b32 v61, v61, s6, v53 bitop3:0xc8
	v_or_b32_e32 v61, s2, v61
	v_add_lshl_u32 v62, v60, v1, 4
	v_mad_u64_u32 v[60:61], s[4:5], v61, s1, v[62:63]
	v_or_b32_e32 v1, 0x600, v0
	v_mad_u32_u24 v53, v53, s0, v62
	v_mul_u32_u24_e32 v61, 0x556, v1
	ds_read_b128 v[62:65], v53 offset:32768
	v_lshrrev_b32_e32 v67, 16, v61
	v_mul_i32_i24_e32 v94, s3, v67
	v_add_lshl_u32 v98, v94, v1, 4
	v_lshrrev_b32_e32 v1, 13, v61
	v_mad_u32_u24 v160, v67, s0, v98
	v_and_b32_e32 v1, 0x1c0, v1
	v_bfe_u32 v61, v61, 16, 3
	ds_read_b128 v[94:97], v160 offset:32768
	v_or3_b32 v1, s2, v61, v1
	s_waitcnt lgkmcnt(1)
	buffer_store_dwordx4 v[62:65], v60, s[24:27], 0 offen sc1
	s_nop 1
	v_mad_u64_u32 v[62:63], s[4:5], v1, s1, v[98:99]
	v_or_b32_e32 v1, 0x800, v0
	v_mul_u32_u24_e32 v61, 0xaab, v1
	v_lshrrev_b32_e32 v61, 17, v61
	v_mul_i32_i24_e32 v63, s3, v61
	v_lshlrev_b32_e32 v64, 3, v61
	s_waitcnt lgkmcnt(0)
	buffer_store_dwordx4 v[94:97], v62, s[24:27], 0 offen sc1
	v_bitop3_b32 v64, v64, s6, v61 bitop3:0xc8
	v_or_b32_e32 v64, s2, v64
	v_add_lshl_u32 v94, v63, v1, 4
	v_mad_u32_u24 v61, v61, s0, v94
	v_or_b32_e32 v0, 0xa00, v0
	v_mad_u64_u32 v[64:65], s[4:5], v64, s1, v[94:95]
	ds_read_b128 v[94:97], v61 offset:32768
	v_mul_u32_u24_e32 v1, 0xaab, v0
	v_lshrrev_b32_e32 v63, 17, v1
	v_mul_i32_i24_e32 v65, s3, v63
	v_add_lshl_u32 v0, v65, v0, 4
	v_mad_u32_u24 v63, v63, s0, v0
	ds_read_b128 v[98:101], v63 offset:32768
	s_waitcnt lgkmcnt(1)
	buffer_store_dwordx4 v[94:97], v64, s[24:27], 0 offen sc1
	ds_read_b128 v[94:97], v66
	ds_read_b128 v[102:105], v66 offset:8192
	ds_read_b128 v[106:109], v66 offset:16384
	ds_read_b128 v[110:113], v66 offset:24576
	v_lshrrev_b32_e32 v65, 14, v1
	v_and_b32_e32 v65, 0x1c0, v65
	v_bfe_u32 v1, v1, 17, 3
	v_or3_b32 v1, s2, v1, v65
	v_mad_u64_u32 v[66:67], s[0:1], v1, s1, v[0:1]
	s_waitcnt lgkmcnt(4)
	buffer_store_dwordx4 v[98:101], v66, s[24:27], 0 offen sc1
	s_waitcnt lgkmcnt(3)
	s_nop 0
	v_mfma_f32_16x16x32_f16 v[98:101], v[34:37], v[94:97], 0
	s_waitcnt lgkmcnt(2)
	v_mfma_f32_16x16x32_f16 v[114:117], v[34:37], v[102:105], 0
	s_waitcnt lgkmcnt(1)
	v_mfma_f32_16x16x32_f16 v[118:121], v[34:37], v[106:109], 0
	s_waitcnt lgkmcnt(0)
	v_mfma_f32_16x16x32_f16 v[34:37], v[34:37], v[110:113], 0
	v_mfma_f32_16x16x32_f16 v[122:125], v[26:29], v[94:97], 0
	v_mfma_f32_16x16x32_f16 v[126:129], v[26:29], v[102:105], 0
	v_mfma_f32_16x16x32_f16 v[130:133], v[26:29], v[106:109], 0
	v_mfma_f32_16x16x32_f16 v[26:29], v[26:29], v[110:113], 0
	v_mfma_f32_16x16x32_f16 v[94:97], v[22:25], v[94:97], 0
	v_mfma_f32_16x16x32_f16 v[102:105], v[22:25], v[102:105], 0
	v_mfma_f32_16x16x32_f16 v[106:109], v[22:25], v[106:109], 0
	v_mfma_f32_16x16x32_f16 v[22:25], v[22:25], v[110:113], 0
	s_mov_b32 s0, 0x34000
	v_add_co_u32_e32 v158, vcc, s0, v54
	s_mov_b32 s0, 0x35000
	s_nop 0
	v_addc_co_u32_e32 v159, vcc, 0, v55, vcc
	v_add_co_u32_e32 v54, vcc, s0, v54
	s_nop 1
	v_addc_co_u32_e32 v55, vcc, 0, v55, vcc
	global_load_dwordx4 v[110:113], v[54:55], off offset:-4096
	global_load_dwordx4 v[134:137], v[58:59], off offset:3072
	global_load_dwordx4 v[138:141], v[158:159], off offset:1024
	ds_read_b128 v[142:145], v72
	ds_read_b128 v[146:149], v72 offset:8192
	ds_read_b128 v[150:153], v72 offset:16384
	ds_read_b128 v[154:157], v72 offset:24576
	s_waitcnt lgkmcnt(3)
	v_mfma_f32_16x16x32_f16 v[98:101], v[14:17], v[142:145], v[98:101]
	s_waitcnt lgkmcnt(2)
	v_mfma_f32_16x16x32_f16 v[114:117], v[14:17], v[146:149], v[114:117]
	s_waitcnt lgkmcnt(1)
	v_mfma_f32_16x16x32_f16 v[118:121], v[14:17], v[150:153], v[118:121]
	s_waitcnt lgkmcnt(0)
	v_mfma_f32_16x16x32_f16 v[14:17], v[14:17], v[154:157], v[34:37]
	v_mfma_f32_16x16x32_f16 v[34:37], v[6:9], v[142:145], v[122:125]
	v_mfma_f32_16x16x32_f16 v[122:125], v[6:9], v[146:149], v[126:129]
	v_mfma_f32_16x16x32_f16 v[126:129], v[6:9], v[150:153], v[130:133]
	v_mfma_f32_16x16x32_f16 v[6:9], v[6:9], v[154:157], v[26:29]
	v_mfma_f32_16x16x32_f16 v[26:29], v[2:5], v[142:145], v[94:97]
	v_mfma_f32_16x16x32_f16 v[94:97], v[2:5], v[146:149], v[102:105]
	v_mfma_f32_16x16x32_f16 v[102:105], v[2:5], v[150:153], v[106:109]
	v_mfma_f32_16x16x32_f16 v[0:3], v[2:5], v[154:157], v[22:25]
	s_nop 2
	global_load_dwordx4 v[22:25], v[158:159], off offset:2048
	global_load_dwordx4 v[106:109], v[158:159], off offset:3072
	global_load_dwordx4 v[130:133], v[54:55], off
	ds_read_b128 v[142:145], v74
	ds_read_b128 v[146:149], v74 offset:8192
	ds_read_b128 v[150:153], v74 offset:16384
	ds_read_b128 v[154:157], v74 offset:24576
	s_waitcnt lgkmcnt(3)
	v_mfma_f32_16x16x32_f16 v[98:101], v[18:21], v[142:145], v[98:101]
	s_waitcnt lgkmcnt(2)
	v_mfma_f32_16x16x32_f16 v[114:117], v[18:21], v[146:149], v[114:117]
	s_waitcnt lgkmcnt(1)
	v_mfma_f32_16x16x32_f16 v[118:121], v[18:21], v[150:153], v[118:121]
	s_waitcnt lgkmcnt(0)
	v_mfma_f32_16x16x32_f16 v[14:17], v[18:21], v[154:157], v[14:17]
	v_mfma_f32_16x16x32_f16 v[18:21], v[10:13], v[142:145], v[34:37]
	v_mfma_f32_16x16x32_f16 v[34:37], v[10:13], v[146:149], v[122:125]
	v_mfma_f32_16x16x32_f16 v[122:125], v[10:13], v[150:153], v[126:129]
	v_mfma_f32_16x16x32_f16 v[4:7], v[10:13], v[154:157], v[6:9]
	v_mfma_f32_16x16x32_f16 v[8:11], v[30:33], v[142:145], v[26:29]
	v_mfma_f32_16x16x32_f16 v[26:29], v[30:33], v[146:149], v[94:97]
	v_mfma_f32_16x16x32_f16 v[94:97], v[30:33], v[150:153], v[102:105]
	v_mfma_f32_16x16x32_f16 v[0:3], v[30:33], v[154:157], v[0:3]
	global_load_dwordx4 v[30:33], v[54:55], off offset:1024
	s_nop 0
	global_load_dwordx4 v[102:105], v[54:55], off offset:2048
	global_load_dwordx4 v[126:129], v[54:55], off offset:3072
	ds_read_b128 v[142:145], v75
	ds_read_b128 v[146:149], v75 offset:8192
	ds_read_b128 v[150:153], v75 offset:16384
	ds_read_b128 v[154:157], v75 offset:24576
	s_waitcnt lgkmcnt(3)
	v_mfma_f32_16x16x32_f16 v[98:101], v[46:49], v[142:145], v[98:101]
	s_waitcnt lgkmcnt(2)
	v_mfma_f32_16x16x32_f16 v[114:117], v[46:49], v[146:149], v[114:117]
	s_waitcnt lgkmcnt(1)
	v_mfma_f32_16x16x32_f16 v[118:121], v[46:49], v[150:153], v[118:121]
	s_waitcnt lgkmcnt(0)
	v_mfma_f32_16x16x32_f16 v[12:15], v[46:49], v[154:157], v[14:17]
	v_mfma_f32_16x16x32_f16 v[16:19], v[42:45], v[142:145], v[18:21]
	v_mfma_f32_16x16x32_f16 v[34:37], v[42:45], v[146:149], v[34:37]
	v_mfma_f32_16x16x32_f16 v[46:49], v[42:45], v[150:153], v[122:125]
	v_mfma_f32_16x16x32_f16 v[4:7], v[42:45], v[154:157], v[4:7]
	v_mfma_f32_16x16x32_f16 v[8:11], v[38:41], v[142:145], v[8:11]
	v_mfma_f32_16x16x32_f16 v[26:29], v[38:41], v[146:149], v[26:29]
	v_mfma_f32_16x16x32_f16 v[42:45], v[38:41], v[150:153], v[94:97]
	v_mfma_f32_16x16x32_f16 v[0:3], v[38:41], v[154:157], v[0:3]
	ds_read_b128 v[38:41], v76
	s_nop 0
	ds_read_b128 v[94:97], v76 offset:8192
	ds_read_b128 v[122:125], v76 offset:16384
	ds_read_b128 v[142:145], v76 offset:24576
	s_waitcnt vmcnt(17) lgkmcnt(3)
	v_mfma_f32_16x16x32_f16 v[98:101], v[82:85], v[38:41], v[98:101]
	s_waitcnt lgkmcnt(2)
	v_mfma_f32_16x16x32_f16 v[114:117], v[82:85], v[94:97], v[114:117]
	s_waitcnt lgkmcnt(1)
	v_mfma_f32_16x16x32_f16 v[118:121], v[82:85], v[122:125], v[118:121]
	s_waitcnt lgkmcnt(0)
	v_mfma_f32_16x16x32_f16 v[12:15], v[82:85], v[142:145], v[12:15]
	s_waitcnt vmcnt(16)
	v_mfma_f32_16x16x32_f16 v[16:19], v[86:89], v[38:41], v[16:19]
	v_mfma_f32_16x16x32_f16 v[34:37], v[86:89], v[94:97], v[34:37]
	v_mfma_f32_16x16x32_f16 v[46:49], v[86:89], v[122:125], v[46:49]
	v_mfma_f32_16x16x32_f16 v[4:7], v[86:89], v[142:145], v[4:7]
	s_waitcnt vmcnt(15)
	v_mfma_f32_16x16x32_f16 v[8:11], v[90:93], v[38:41], v[8:11]
	v_mfma_f32_16x16x32_f16 v[26:29], v[90:93], v[94:97], v[26:29]
	v_mfma_f32_16x16x32_f16 v[38:41], v[90:93], v[122:125], v[42:45]
	v_mfma_f32_16x16x32_f16 v[0:3], v[90:93], v[142:145], v[0:3]
	s_nop 1
	ds_read_b128 v[42:45], v77
	ds_read_b128 v[82:85], v77 offset:8192
	ds_read_b128 v[86:89], v77 offset:16384
	ds_read_b128 v[74:77], v77 offset:24576
	s_waitcnt vmcnt(7) lgkmcnt(3)
	v_mfma_f32_16x16x32_f16 v[90:93], v[134:137], v[42:45], v[98:101]
	s_waitcnt lgkmcnt(2)
	v_mfma_f32_16x16x32_f16 v[94:97], v[134:137], v[82:85], v[114:117]
	s_waitcnt lgkmcnt(1)
	v_mfma_f32_16x16x32_f16 v[98:101], v[134:137], v[86:89], v[118:121]
	s_waitcnt lgkmcnt(0)
	v_mfma_f32_16x16x32_f16 v[12:15], v[134:137], v[74:77], v[12:15]
	v_mfma_f32_16x16x32_f16 v[16:19], v[110:113], v[42:45], v[16:19]
	v_mfma_f32_16x16x32_f16 v[34:37], v[110:113], v[82:85], v[34:37]
	v_mfma_f32_16x16x32_f16 v[46:49], v[110:113], v[86:89], v[46:49]
	v_mfma_f32_16x16x32_f16 v[4:7], v[110:113], v[74:77], v[4:7]
	s_waitcnt vmcnt(6)
	v_mfma_f32_16x16x32_f16 v[8:11], v[138:141], v[42:45], v[8:11]
	v_mfma_f32_16x16x32_f16 v[26:29], v[138:141], v[82:85], v[26:29]
	v_mfma_f32_16x16x32_f16 v[38:41], v[138:141], v[86:89], v[38:41]
	v_mfma_f32_16x16x32_f16 v[0:3], v[138:141], v[74:77], v[0:3]
	ds_read_b128 v[42:45], v78
	ds_read_b128 v[74:77], v78 offset:8192
	ds_read_b128 v[82:85], v78 offset:16384
	ds_read_b128 v[86:89], v78 offset:24576
	s_waitcnt vmcnt(5) lgkmcnt(3)
	v_mfma_f32_16x16x32_f16 v[90:93], v[22:25], v[42:45], v[90:93]
	s_waitcnt lgkmcnt(2)
	v_mfma_f32_16x16x32_f16 v[94:97], v[22:25], v[74:77], v[94:97]
	s_waitcnt lgkmcnt(1)
	v_mfma_f32_16x16x32_f16 v[98:101], v[22:25], v[82:85], v[98:101]
	s_waitcnt lgkmcnt(0)
	v_mfma_f32_16x16x32_f16 v[12:15], v[22:25], v[86:89], v[12:15]
	s_waitcnt vmcnt(4)
	v_mfma_f32_16x16x32_f16 v[16:19], v[106:109], v[42:45], v[16:19]
	v_mfma_f32_16x16x32_f16 v[20:23], v[106:109], v[74:77], v[34:37]
	v_mfma_f32_16x16x32_f16 v[34:37], v[106:109], v[82:85], v[46:49]
	v_mfma_f32_16x16x32_f16 v[4:7], v[106:109], v[86:89], v[4:7]
	s_waitcnt vmcnt(3)
	v_mfma_f32_16x16x32_f16 v[8:11], v[130:133], v[42:45], v[8:11]
	v_mfma_f32_16x16x32_f16 v[24:27], v[130:133], v[74:77], v[26:29]
	v_mfma_f32_16x16x32_f16 v[38:41], v[130:133], v[82:85], v[38:41]
	v_mfma_f32_16x16x32_f16 v[0:3], v[130:133], v[86:89], v[0:3]
	ds_read_b128 v[42:45], v79
	ds_read_b128 v[46:49], v79 offset:8192
	ds_read_b128 v[74:77], v79 offset:16384
	ds_read_b128 v[82:85], v79 offset:24576
	s_waitcnt vmcnt(2) lgkmcnt(3)
	v_mfma_f32_16x16x32_f16 v[86:89], v[30:33], v[42:45], v[90:93]
	s_waitcnt lgkmcnt(2)
	v_mfma_f32_16x16x32_f16 v[90:93], v[30:33], v[46:49], v[94:97]
	s_waitcnt lgkmcnt(1)
	v_mfma_f32_16x16x32_f16 v[94:97], v[30:33], v[74:77], v[98:101]
	s_waitcnt lgkmcnt(0)
	v_mfma_f32_16x16x32_f16 v[12:15], v[30:33], v[82:85], v[12:15]
	s_waitcnt vmcnt(1)
	v_mfma_f32_16x16x32_f16 v[16:19], v[102:105], v[42:45], v[16:19]
	v_mfma_f32_16x16x32_f16 v[20:23], v[102:105], v[46:49], v[20:23]
	v_mfma_f32_16x16x32_f16 v[28:31], v[102:105], v[74:77], v[34:37]
	v_mfma_f32_16x16x32_f16 v[4:7], v[102:105], v[82:85], v[4:7]
	s_waitcnt vmcnt(0)
	v_mfma_f32_16x16x32_f16 v[8:11], v[126:129], v[42:45], v[8:11]
	v_mfma_f32_16x16x32_f16 v[24:27], v[126:129], v[46:49], v[24:27]
	v_mfma_f32_16x16x32_f16 v[32:35], v[126:129], v[74:77], v[38:41]
	v_mfma_f32_16x16x32_f16 v[0:3], v[126:129], v[82:85], v[0:3]
	s_nop 1
	global_load_dwordx4 v[36:39], v[56:57], off offset:1536
	global_load_dwordx4 v[40:43], v[56:57], off offset:1600
	global_load_dwordx4 v[44:47], v[56:57], off offset:1664
	v_mov_b32_e32 v58, v21
	v_mov_b32_e32 v59, v22
	v_mov_b32_e32 v74, v29
	v_mov_b32_e32 v56, v13
	v_mov_b32_e32 v57, v14
	v_mov_b32_e32 v75, v30
	v_mov_b32_e32 v48, v91
	v_mov_b32_e32 v49, v92
	v_mov_b32_e32 v54, v95
	v_mov_b32_e32 v55, v96
	v_mov_b32_e32 v76, v5
	v_mov_b32_e32 v77, v6
	s_barrier
	s_waitcnt vmcnt(2)
	v_pk_add_f32 v[78:79], v[86:87], v[36:37]
	v_pk_add_f32 v[82:83], v[88:89], v[38:39]
	v_add_f32_e32 v21, v90, v36
	v_pk_mov_b32 v[84:85], v[36:37], v[38:39] op_sel:[1,0]
	v_add_f32_e32 v22, v93, v39
	v_add_f32_e32 v29, v94, v36
	v_add_f32_e32 v36, v12, v36
	v_add_f32_e32 v37, v15, v39
	s_waitcnt vmcnt(1)
	v_add_f32_e32 v38, v20, v40
	v_add_f32_e32 v23, v23, v43
	v_add_f32_e32 v30, v97, v39
	v_pk_add_f32 v[12:13], v[16:17], v[40:41]
	v_pk_add_f32 v[14:15], v[18:19], v[42:43]
	v_pk_mov_b32 v[16:17], v[40:41], v[42:43] op_sel:[1,0]
	v_add_f32_e32 v28, v28, v40
	v_add_f32_e32 v31, v31, v43
	v_add_f32_e32 v39, v4, v40
	v_add_f32_e32 v40, v7, v43
	v_cvt_f16_f32_e32 v41, v21
	v_cvt_f16_f32_e32 v42, v22
	v_cvt_f16_f32_e32 v36, v36
	v_cvt_f16_f32_e32 v37, v37
	v_cvt_f16_f32_e32 v38, v38
	v_cvt_f16_f32_e32 v43, v23
	v_cvt_f16_f32_e32 v29, v29
	v_cvt_f16_f32_e32 v30, v30
	v_cvt_f16_f32_e32 v28, v28
	v_cvt_f16_f32_e32 v31, v31
	v_cvt_f16_f32_e32 v39, v39
	v_cvt_f16_f32_e32 v40, v40
	s_waitcnt vmcnt(0)
	v_pk_add_f32 v[4:5], v[8:9], v[44:45]
	v_pk_add_f32 v[6:7], v[10:11], v[46:47]
	v_pk_add_f32 v[10:11], v[48:49], v[84:85]
	v_pk_add_f32 v[20:21], v[56:57], v[84:85]
	v_cvt_pk_f16_f32 v12, v12, v13
	v_cvt_pk_f16_f32 v13, v14, v15
	v_pk_add_f32 v[14:15], v[58:59], v[16:17]
	v_cvt_pk_f16_f32 v8, v78, v79
	v_cvt_pk_f16_f32 v9, v82, v83
	v_pk_add_f32 v[18:19], v[54:55], v[84:85]
	v_pk_add_f32 v[22:23], v[74:75], v[16:17]
	v_pk_add_f32 v[16:17], v[76:77], v[16:17]
	v_cvt_pk_f16_f32 v4, v4, v5
	v_cvt_pk_f16_f32 v5, v6, v7
	v_cvt_pk_f16_f32 v6, v10, v11
	v_cvt_pk_f16_f32 v10, v20, v21
	v_cvt_pk_f16_f32 v11, v14, v15
	v_cvt_pk_f16_f32 v7, v18, v19
	v_cvt_pk_f16_f32 v14, v22, v23
	v_cvt_pk_f16_f32 v15, v16, v17
	ds_write2_b64 v73, v[8:9], v[12:13] offset1:4
	ds_write_b64 v69, v[4:5] offset:32832
	v_pack_b32_f16 v4, v41, v6
	v_alignbit_b32 v5, v42, v6, 16
	v_pack_b32_f16 v8, v36, v10
	v_alignbit_b32 v9, v37, v10, 16
	v_pack_b32_f16 v10, v38, v11
	v_alignbit_b32 v11, v43, v11, 16
	v_add_f32_e32 v24, v24, v44
	v_pack_b32_f16 v6, v29, v7
	v_alignbit_b32 v7, v30, v7, 16
	v_pack_b32_f16 v12, v28, v14
	v_alignbit_b32 v13, v31, v14, 16
	v_pack_b32_f16 v14, v39, v15
	v_alignbit_b32 v15, v40, v15, 16
	ds_write2_b64 v70, v[4:5], v[10:11] offset0:32 offset1:36
	ds_write2_b64 v71, v[6:7], v[12:13] offset0:64 offset1:68
	ds_write2_b64 v80, v[8:9], v[14:15] offset1:4
	v_add_f32_e32 v8, v27, v47
	v_cvt_f16_f32_e32 v24, v24
	v_cvt_f16_f32_e32 v8, v8
	v_mov_b32_e32 v4, v25
	v_mov_b32_e32 v5, v26
	v_pk_mov_b32 v[6:7], v[44:45], v[46:47] op_sel:[1,0]
	v_add_f32_e32 v9, v35, v47
	v_pk_add_f32 v[4:5], v[4:5], v[6:7]
	v_cvt_f16_f32_e32 v9, v9
	v_cvt_pk_f16_f32 v5, v4, v5
	v_pack_b32_f16 v4, v24, v5
	v_alignbit_b32 v5, v8, v5, 16
	ds_write_b64 v69, v[4:5] offset:45376
	v_add_f32_e32 v4, v32, v44
	v_cvt_f16_f32_e32 v8, v4
	v_mov_b32_e32 v4, v33
	v_mov_b32_e32 v5, v34
	v_pk_add_f32 v[4:5], v[4:5], v[6:7]
	v_add_f32_e32 v0, v0, v44
	v_cvt_pk_f16_f32 v5, v4, v5
	v_pack_b32_f16 v4, v8, v5
	v_alignbit_b32 v5, v9, v5, 16
	ds_write_b64 v69, v[4:5] offset:57920
	v_cvt_f16_f32_e32 v4, v0
	v_mov_b32_e32 v0, v1
	v_mov_b32_e32 v1, v2
	v_add_f32_e32 v2, v3, v47
	v_cvt_f16_f32_e32 v2, v2
	v_pk_add_f32 v[0:1], v[0:1], v[6:7]
	s_nop 0
	v_cvt_pk_f16_f32 v1, v0, v1
	v_pack_b32_f16 v0, v4, v1
	v_alignbit_b32 v1, v2, v1, 16
	ds_write_b64 v68, v[0:1] offset:32832
	s_waitcnt lgkmcnt(0)
	s_barrier
	ds_read_b128 v[0:3], v51 offset:32768
	ds_read_b128 v[4:7], v81 offset:32768
	s_waitcnt lgkmcnt(1)
	buffer_store_dwordx4 v[0:3], v50, s[24:27], 0 offen offset:768 sc1
	ds_read_b128 v[0:3], v53 offset:32768
	ds_read_b128 v[8:11], v160 offset:32768
	ds_read_b128 v[12:15], v61 offset:32768
	ds_read_b128 v[16:19], v63 offset:32768
	s_waitcnt lgkmcnt(4)
	buffer_store_dwordx4 v[4:7], v52, s[24:27], 0 offen offset:768 sc1
	s_waitcnt lgkmcnt(3)
	buffer_store_dwordx4 v[0:3], v60, s[24:27], 0 offen offset:768 sc1
	s_waitcnt lgkmcnt(2)
	buffer_store_dwordx4 v[8:11], v62, s[24:27], 0 offen offset:768 sc1
	s_waitcnt lgkmcnt(1)
	buffer_store_dwordx4 v[12:15], v64, s[24:27], 0 offen offset:768 sc1
	s_waitcnt lgkmcnt(0)
	buffer_store_dwordx4 v[16:19], v66, s[24:27], 0 offen offset:768 sc1
	s_endpgm
	.p2alignl 8, 3212836864

.LBB5_79:
	s_mul_i32 s0, s13, s3
	s_lshl_b32 s1, s15, 6
	s_add_i32 s0, s0, s12
	s_and_b32 s1, s1, 0xfffffe00
	s_or_b32 s6, s1, s2
	s_mul_i32 s2, s0, 0x60000
	s_mul_hi_i32 s1, s0, 0x60000
	s_add_u32 s2, s8, s2
	s_mulk_i32 s0, 0x300
	s_addc_u32 s7, s9, s1
	s_ashr_i32 s1, s0, 31
	s_lshl_b64 s[0:1], s[0:1], 2
	s_add_u32 s4, s10, s0
	s_addc_u32 s5, s11, s1
	s_mul_i32 s0, s3, 0x1800000
	s_mul_hi_i32 s1, s3, 0x1800000
	s_add_u32 s0, s20, s0
	v_readfirstlane_b32 s3, v0
	s_addc_u32 s1, s21, s1
	s_lshr_b32 s8, s3, 6
	s_and_b32 s1, s1, 0xffff
	s_mul_i32 s9, s8, 0x6000
	v_and_b32_e32 v2, 63, v0
	s_mul_hi_u32 s3, s8, 0x6000
	s_add_u32 s2, s2, s9
	s_addc_u32 s3, s7, s3
	v_lshlrev_b32_e32 v56, 4, v2
	v_mov_b32_e32 v57, 0
	v_lshl_add_u64 v[54:55], s[2:3], 0, v[56:57]
	s_movk_i32 s7, 0x1000
	v_add_co_u32_e32 v50, vcc, s7, v54
	s_movk_i32 s7, 0x2000
	s_nop 0
	v_addc_co_u32_e32 v51, vcc, 0, v55, vcc
	v_add_co_u32_e32 v52, vcc, s7, v54
	global_load_dwordx4 v[2:5], v56, s[2:3] offset:1024
	global_load_dwordx4 v[6:9], v56, s[2:3] offset:2048
	v_addc_co_u32_e32 v53, vcc, 0, v55, vcc
	global_load_dwordx4 v[10:13], v56, s[2:3] offset:3072
	global_load_dwordx4 v[14:17], v[52:53], off offset:-4096
	global_load_dwordx4 v[18:21], v[50:51], off offset:1024
	global_load_dwordx4 v[22:25], v[50:51], off offset:2048
	global_load_dwordx4 v[26:29], v56, s[2:3]
	global_load_dwordx4 v[30:33], v[50:51], off offset:3072
	global_load_dwordx4 v[34:37], v[52:53], off
	global_load_dwordx4 v[38:41], v[52:53], off offset:1024
	global_load_dwordx4 v[42:45], v[52:53], off offset:2048
	global_load_dwordx4 v[46:49], v[52:53], off offset:3072
	s_movk_i32 s2, 0x3000
	v_add_co_u32_e32 v58, vcc, s2, v54
	s_movk_i32 s2, 0x4000
	s_nop 0
	v_addc_co_u32_e32 v59, vcc, 0, v55, vcc
	v_add_co_u32_e32 v140, vcc, s2, v54
	s_waitcnt lgkmcnt(0)
	s_nop 0
	v_addc_co_u32_e32 v141, vcc, 0, v55, vcc
	s_barrier
	global_load_dwordx4 v[50:53], v[140:141], off offset:-4096
	global_load_dwordx4 v[62:65], v[58:59], off offset:1024
	global_load_dwordx4 v[68:71], v[58:59], off offset:2048
	v_lshlrev_b32_e32 v67, 9, v1
	v_xor_b32_e32 v61, v158, v1
	v_lshl_or_b32 v66, v61, 4, v67
	ds_read_b128 v[72:75], v66
	ds_read_b128 v[76:79], v66 offset:8192
	ds_read_b128 v[80:83], v66 offset:16384
	ds_read_b128 v[84:87], v66 offset:24576
	v_mul_u32_u24_e32 v60, 0x556, v0
	v_lshrrev_b32_e32 v60, 16, v60
	s_mul_i32 s7, s8, 48
	v_lshlrev_b32_e32 v61, 3, v60
	s_movk_i32 s9, 0x47
	v_lshl_or_b32 v56, v158, 2, s7
	s_mov_b32 s7, 0xfffffd0
	v_bitop3_b32 v61, v61, s9, v60 bitop3:0xc8
	s_mov_b32 s2, 0x1800000
	s_mov_b32 s3, 0x20000
	s_mulk_i32 s8, 0x60
	v_mul_i32_i24_e32 v150, s7, v60
	v_or_b32_e32 v61, s6, v61
	s_waitcnt vmcnt(8) lgkmcnt(3)
	v_mfma_f32_16x16x32_f16 v[88:91], v[26:29], v[72:75], 0
	s_waitcnt lgkmcnt(2)
	v_mfma_f32_16x16x32_f16 v[92:95], v[26:29], v[76:79], 0
	s_waitcnt lgkmcnt(1)
	v_mfma_f32_16x16x32_f16 v[96:99], v[26:29], v[80:83], 0
	s_waitcnt lgkmcnt(0)
	v_mfma_f32_16x16x32_f16 v[26:29], v[26:29], v[84:87], 0
	v_mfma_f32_16x16x32_f16 v[100:103], v[2:5], v[72:75], 0
	v_mfma_f32_16x16x32_f16 v[104:107], v[2:5], v[76:79], 0
	v_mfma_f32_16x16x32_f16 v[108:111], v[2:5], v[80:83], 0
	v_mfma_f32_16x16x32_f16 v[2:5], v[2:5], v[84:87], 0
	v_mfma_f32_16x16x32_f16 v[112:115], v[6:9], v[72:75], 0
	v_mfma_f32_16x16x32_f16 v[74:77], v[6:9], v[76:79], 0
	v_mfma_f32_16x16x32_f16 v[78:81], v[6:9], v[80:83], 0
	v_mfma_f32_16x16x32_f16 v[6:9], v[6:9], v[84:87], 0
	global_load_dwordx4 v[82:85], v[58:59], off offset:3072
	global_load_dwordx4 v[116:119], v[140:141], off
	global_load_dwordx4 v[120:123], v[140:141], off offset:1024
	v_bitop3_b32 v58, v158, v1, 4 bitop3:0x36
	v_lshl_or_b32 v72, v58, 4, v67
	ds_read_b128 v[124:127], v72
	ds_read_b128 v[128:131], v72 offset:8192
	ds_read_b128 v[132:135], v72 offset:16384
	ds_read_b128 v[136:139], v72 offset:24576
	s_waitcnt lgkmcnt(3)
	v_mfma_f32_16x16x32_f16 v[86:89], v[10:13], v[124:127], v[88:91]
	s_waitcnt lgkmcnt(2)
	v_mfma_f32_16x16x32_f16 v[90:93], v[10:13], v[128:131], v[92:95]
	s_waitcnt lgkmcnt(1)
	v_mfma_f32_16x16x32_f16 v[94:97], v[10:13], v[132:135], v[96:99]
	s_waitcnt lgkmcnt(0)
	v_mfma_f32_16x16x32_f16 v[10:13], v[10:13], v[136:139], v[26:29]
	v_mfma_f32_16x16x32_f16 v[26:29], v[14:17], v[124:127], v[100:103]
	v_mfma_f32_16x16x32_f16 v[98:101], v[14:17], v[128:131], v[104:107]
	v_mfma_f32_16x16x32_f16 v[102:105], v[14:17], v[132:135], v[108:111]
	v_mfma_f32_16x16x32_f16 v[2:5], v[14:17], v[136:139], v[2:5]
	v_mfma_f32_16x16x32_f16 v[14:17], v[18:21], v[124:127], v[112:115]
	v_mfma_f32_16x16x32_f16 v[106:109], v[18:21], v[128:131], v[74:77]
	v_mfma_f32_16x16x32_f16 v[76:79], v[18:21], v[132:135], v[78:81]
	v_mfma_f32_16x16x32_f16 v[6:9], v[18:21], v[136:139], v[6:9]
	s_movk_i32 s9, 0x5000
	v_add_co_u32_e32 v58, vcc, s9, v54
	global_load_dwordx4 v[110:113], v[140:141], off offset:2048
	global_load_dwordx4 v[124:127], v[140:141], off offset:3072
	v_addc_co_u32_e32 v59, vcc, 0, v55, vcc
	global_load_dwordx4 v[128:131], v[58:59], off
	v_bitop3_b32 v18, v158, v1, 8 bitop3:0x36
	v_lshl_or_b32 v74, v18, 4, v67
	ds_read_b128 v[18:21], v74
	ds_read_b128 v[132:135], v74 offset:8192
	ds_read_b128 v[136:139], v74 offset:16384
	ds_read_b128 v[140:143], v74 offset:24576
	s_waitcnt lgkmcnt(3)
	v_mfma_f32_16x16x32_f16 v[86:89], v[22:25], v[18:21], v[86:89]
	s_waitcnt lgkmcnt(2)
	v_mfma_f32_16x16x32_f16 v[90:93], v[22:25], v[132:135], v[90:93]
	s_waitcnt lgkmcnt(1)
	v_mfma_f32_16x16x32_f16 v[94:97], v[22:25], v[136:139], v[94:97]
	s_waitcnt lgkmcnt(0)
	v_mfma_f32_16x16x32_f16 v[10:13], v[22:25], v[140:143], v[10:13]
	s_waitcnt vmcnt(13)
	v_mfma_f32_16x16x32_f16 v[22:25], v[30:33], v[18:21], v[26:29]
	v_mfma_f32_16x16x32_f16 v[26:29], v[30:33], v[132:135], v[98:101]
	v_mfma_f32_16x16x32_f16 v[98:101], v[30:33], v[136:139], v[102:105]
	v_mfma_f32_16x16x32_f16 v[2:5], v[30:33], v[140:143], v[2:5]
	s_waitcnt vmcnt(12)
	v_mfma_f32_16x16x32_f16 v[14:17], v[34:37], v[18:21], v[14:17]
	v_mfma_f32_16x16x32_f16 v[18:21], v[34:37], v[132:135], v[106:109]
	v_mfma_f32_16x16x32_f16 v[30:33], v[34:37], v[136:139], v[76:79]
	v_mfma_f32_16x16x32_f16 v[6:9], v[34:37], v[140:143], v[6:9]
	global_load_dwordx4 v[102:105], v[58:59], off offset:1024
	global_load_dwordx4 v[106:109], v[58:59], off offset:2048
	global_load_dwordx4 v[132:135], v[58:59], off offset:3072
	v_bitop3_b32 v34, v158, v1, 12 bitop3:0x36
	v_lshl_or_b32 v75, v34, 4, v67
	ds_read_b128 v[34:37], v75
	ds_read_b128 v[76:79], v75 offset:8192
	ds_read_b128 v[136:139], v75 offset:16384
	ds_read_b128 v[140:143], v75 offset:24576
	s_waitcnt vmcnt(14) lgkmcnt(3)
	v_mfma_f32_16x16x32_f16 v[86:89], v[38:41], v[34:37], v[86:89]
	s_waitcnt lgkmcnt(2)
	v_mfma_f32_16x16x32_f16 v[90:93], v[38:41], v[76:79], v[90:93]
	s_waitcnt lgkmcnt(1)
	v_mfma_f32_16x16x32_f16 v[94:97], v[38:41], v[136:139], v[94:97]
	s_waitcnt lgkmcnt(0)
	v_mfma_f32_16x16x32_f16 v[10:13], v[38:41], v[140:143], v[10:13]
	s_waitcnt vmcnt(13)
	v_mfma_f32_16x16x32_f16 v[38:41], v[42:45], v[34:37], v[22:25]
	v_mfma_f32_16x16x32_f16 v[144:147], v[42:45], v[76:79], v[26:29]
	v_mfma_f32_16x16x32_f16 v[98:101], v[42:45], v[136:139], v[98:101]
	v_mfma_f32_16x16x32_f16 v[2:5], v[42:45], v[140:143], v[2:5]
	s_waitcnt vmcnt(12)
	v_mfma_f32_16x16x32_f16 v[14:17], v[46:49], v[34:37], v[14:17]
	v_mfma_f32_16x16x32_f16 v[18:21], v[46:49], v[76:79], v[18:21]
	v_mfma_f32_16x16x32_f16 v[30:33], v[46:49], v[136:139], v[30:33]
	v_mfma_f32_16x16x32_f16 v[6:9], v[46:49], v[140:143], v[6:9]
	s_mov_b32 s9, 0x30000
	v_add_co_u32_e32 v58, vcc, s9, v54
	s_mov_b32 s9, 0x31000
	s_nop 0
	v_addc_co_u32_e32 v59, vcc, 0, v55, vcc
	v_add_co_u32_e32 v148, vcc, s9, v54
	v_bitop3_b32 v42, v158, v1, 16 bitop3:0x36
	s_nop 0
	v_addc_co_u32_e32 v149, vcc, 0, v55, vcc
	global_load_dwordx4 v[34:37], v[148:149], off offset:-4096
	global_load_dwordx4 v[26:29], v[58:59], off offset:1024
	global_load_dwordx4 v[22:25], v[58:59], off offset:2048
	v_lshl_or_b32 v76, v42, 4, v67
	ds_read_b128 v[42:45], v76
	ds_read_b128 v[46:49], v76 offset:8192
	ds_read_b128 v[78:81], v76 offset:16384
	ds_read_b128 v[136:139], v76 offset:24576
	s_waitcnt vmcnt(14) lgkmcnt(3)
	v_mfma_f32_16x16x32_f16 v[86:89], v[50:53], v[42:45], v[86:89]
	s_waitcnt lgkmcnt(2)
	v_mfma_f32_16x16x32_f16 v[90:93], v[50:53], v[46:49], v[90:93]
	s_waitcnt lgkmcnt(1)
	v_mfma_f32_16x16x32_f16 v[94:97], v[50:53], v[78:81], v[94:97]
	s_waitcnt lgkmcnt(0)
	v_mfma_f32_16x16x32_f16 v[10:13], v[50:53], v[136:139], v[10:13]
	s_waitcnt vmcnt(13)
	v_mfma_f32_16x16x32_f16 v[38:41], v[62:65], v[42:45], v[38:41]
	v_mfma_f32_16x16x32_f16 v[50:53], v[62:65], v[46:49], v[144:147]
	v_mfma_f32_16x16x32_f16 v[98:101], v[62:65], v[78:81], v[98:101]
	v_mfma_f32_16x16x32_f16 v[62:65], v[62:65], v[136:139], v[2:5]
	s_waitcnt vmcnt(12)
	v_mfma_f32_16x16x32_f16 v[42:45], v[68:71], v[42:45], v[14:17]
	v_mfma_f32_16x16x32_f16 v[18:21], v[68:71], v[46:49], v[18:21]
	v_mfma_f32_16x16x32_f16 v[30:33], v[68:71], v[78:81], v[30:33]
	v_mfma_f32_16x16x32_f16 v[46:49], v[68:71], v[136:139], v[6:9]
	global_load_dwordx4 v[14:17], v[58:59], off offset:3072
	s_nop 1
	global_load_dwordx4 v[6:9], v[148:149], off
	global_load_dwordx4 v[2:5], v[148:149], off offset:1024
	v_bitop3_b32 v58, v158, v1, 20 bitop3:0x36
	v_lshl_or_b32 v77, v58, 4, v67
	ds_read_b128 v[68:71], v77
	ds_read_b128 v[78:81], v77 offset:8192
	ds_read_b128 v[136:139], v77 offset:16384
	ds_read_b128 v[140:143], v77 offset:24576
	s_waitcnt vmcnt(14) lgkmcnt(3)
	v_mfma_f32_16x16x32_f16 v[86:89], v[82:85], v[68:71], v[86:89]
	s_waitcnt lgkmcnt(2)
	v_mfma_f32_16x16x32_f16 v[90:93], v[82:85], v[78:81], v[90:93]
	s_waitcnt lgkmcnt(1)
	v_mfma_f32_16x16x32_f16 v[94:97], v[82:85], v[136:139], v[94:97]
	s_waitcnt lgkmcnt(0)
	v_mfma_f32_16x16x32_f16 v[82:85], v[82:85], v[140:143], v[10:13]
	s_waitcnt vmcnt(13)
	v_mfma_f32_16x16x32_f16 v[38:41], v[116:119], v[68:71], v[38:41]
	v_mfma_f32_16x16x32_f16 v[50:53], v[116:119], v[78:81], v[50:53]
	v_mfma_f32_16x16x32_f16 v[98:101], v[116:119], v[136:139], v[98:101]
	v_mfma_f32_16x16x32_f16 v[62:65], v[116:119], v[140:143], v[62:65]
	s_waitcnt vmcnt(12)
	v_mfma_f32_16x16x32_f16 v[42:45], v[120:123], v[68:71], v[42:45]
	v_mfma_f32_16x16x32_f16 v[68:71], v[120:123], v[78:81], v[18:21]
	v_mfma_f32_16x16x32_f16 v[114:117], v[120:123], v[136:139], v[30:33]
	v_mfma_f32_16x16x32_f16 v[46:49], v[120:123], v[140:143], v[46:49]
	s_mov_b32 s9, 0x33000
	v_add_co_u32_e32 v58, vcc, s9, v54
	global_load_dwordx4 v[18:21], v[148:149], off offset:2048
	global_load_dwordx4 v[10:13], v[148:149], off offset:3072
	v_addc_co_u32_e32 v59, vcc, 0, v55, vcc
	global_load_dwordx4 v[30:33], v[58:59], off offset:-4096
	v_bitop3_b32 v73, v158, v1, 24 bitop3:0x36
	v_lshl_or_b32 v78, v73, 4, v67
	ds_read_b128 v[118:121], v78
	ds_read_b128 v[136:139], v78 offset:8192
	ds_read_b128 v[140:143], v78 offset:16384
	ds_read_b128 v[144:147], v78 offset:24576
	s_mov_b32 s9, 0x32000
	v_add_co_u32_e32 v148, vcc, s9, v54
	s_nop 1
	v_addc_co_u32_e32 v149, vcc, 0, v55, vcc
	s_waitcnt vmcnt(14) lgkmcnt(3)
	v_mfma_f32_16x16x32_f16 v[86:89], v[110:113], v[118:121], v[86:89]
	s_waitcnt lgkmcnt(2)
	v_mfma_f32_16x16x32_f16 v[90:93], v[110:113], v[136:139], v[90:93]
	s_waitcnt lgkmcnt(1)
	v_mfma_f32_16x16x32_f16 v[94:97], v[110:113], v[140:143], v[94:97]
	s_waitcnt lgkmcnt(0)
	v_mfma_f32_16x16x32_f16 v[80:83], v[110:113], v[144:147], v[82:85]
	s_waitcnt vmcnt(13)
	v_mfma_f32_16x16x32_f16 v[110:113], v[124:127], v[118:121], v[38:41]
	v_mfma_f32_16x16x32_f16 v[50:53], v[124:127], v[136:139], v[50:53]
	v_mfma_f32_16x16x32_f16 v[98:101], v[124:127], v[140:143], v[98:101]
	v_mfma_f32_16x16x32_f16 v[62:65], v[124:127], v[144:147], v[62:65]
	s_waitcnt vmcnt(12)
	v_mfma_f32_16x16x32_f16 v[118:121], v[128:131], v[118:121], v[42:45]
	v_mfma_f32_16x16x32_f16 v[68:71], v[128:131], v[136:139], v[68:71]
	v_mfma_f32_16x16x32_f16 v[114:117], v[128:131], v[140:143], v[114:117]
	v_mfma_f32_16x16x32_f16 v[122:125], v[128:131], v[144:147], v[46:49]
	s_nop 2
	global_load_dwordx4 v[46:49], v[148:149], off offset:1024
	global_load_dwordx4 v[42:45], v[148:149], off offset:2048
	global_load_dwordx4 v[38:41], v[148:149], off offset:3072
	v_bitop3_b32 v73, v158, v1, 28 bitop3:0x36
	v_lshl_or_b32 v79, v73, 4, v67
	ds_read_b128 v[126:129], v79
	ds_read_b128 v[136:139], v79 offset:8192
	ds_read_b128 v[140:143], v79 offset:16384
	ds_read_b128 v[144:147], v79 offset:24576
	s_waitcnt vmcnt(14) lgkmcnt(3)
	v_mfma_f32_16x16x32_f16 v[84:87], v[102:105], v[126:129], v[86:89]
	s_waitcnt lgkmcnt(2)
	v_mfma_f32_16x16x32_f16 v[88:91], v[102:105], v[136:139], v[90:93]
	s_waitcnt lgkmcnt(1)
	v_mfma_f32_16x16x32_f16 v[92:95], v[102:105], v[140:143], v[94:97]
	s_waitcnt lgkmcnt(0)
	v_mfma_f32_16x16x32_f16 v[80:83], v[102:105], v[144:147], v[80:83]
	s_waitcnt vmcnt(13)
	v_mfma_f32_16x16x32_f16 v[102:105], v[106:109], v[126:129], v[110:113]
	v_mfma_f32_16x16x32_f16 v[110:113], v[106:109], v[136:139], v[50:53]
	v_mfma_f32_16x16x32_f16 v[96:99], v[106:109], v[140:143], v[98:101]
	v_mfma_f32_16x16x32_f16 v[62:65], v[106:109], v[144:147], v[62:65]
	s_waitcnt vmcnt(12)
	v_mfma_f32_16x16x32_f16 v[106:109], v[132:135], v[126:129], v[118:121]
	v_mfma_f32_16x16x32_f16 v[118:121], v[132:135], v[136:139], v[68:71]
	v_mfma_f32_16x16x32_f16 v[114:117], v[132:135], v[140:143], v[114:117]
	v_mfma_f32_16x16x32_f16 v[50:53], v[132:135], v[144:147], v[122:125]
	v_lshl_add_u64 v[56:57], v[56:57], 2, s[4:5]
	s_nop 1
	global_load_dwordx4 v[122:125], v[56:57], off
	global_load_dwordx4 v[126:129], v[56:57], off offset:64
	global_load_dwordx4 v[130:133], v[56:57], off offset:128
	v_lshl_or_b32 v67, v158, 3, s8
	s_movk_i32 s4, 0x310
	v_mov_b32_e32 v100, v89
	v_mov_b32_e32 v101, v90
	v_mov_b32_e32 v134, v93
	v_mov_b32_e32 v135, v94
	v_mov_b32_e32 v140, v97
	v_mov_b32_e32 v141, v98
	v_mad_u32_u24 v69, v1, s4, v67
	v_mov_b32_e32 v143, v64
	v_mov_b32_e32 v136, v81
	v_mov_b32_e32 v137, v82
	v_mov_b32_e32 v138, v111
	v_mov_b32_e32 v139, v112
	v_mov_b32_e32 v142, v63
	v_add_u32_e32 v73, 0x8000, v69
	s_barrier
	v_add_u32_e32 v70, 0xb000, v69
	v_add_u32_e32 v71, 0xe000, v69
	v_add_u32_e32 v68, 0x9300, v69
	s_movk_i32 s5, 0x600
	s_movk_i32 s10, 0x1c7
	s_waitcnt vmcnt(2)
	v_pk_add_f32 v[84:85], v[84:85], v[122:123]
	v_add_f32_e32 v1, v88, v122
	v_pk_mov_b32 v[88:89], v[122:123], v[124:125] op_sel:[1,0]
	v_add_f32_e32 v67, v91, v125
	v_add_f32_e32 v92, v92, v122
	v_add_f32_e32 v93, v95, v125
	v_add_f32_e32 v94, v80, v122
	v_add_f32_e32 v95, v83, v125
	s_waitcnt vmcnt(1)
	v_add_f32_e32 v97, v110, v126
	v_add_f32_e32 v98, v113, v129
	v_add_f32_e32 v96, v96, v126
	v_add_f32_e32 v99, v99, v129
	v_cvt_pk_f16_f32 v64, v84, v85
	v_cvt_f16_f32_e32 v1, v1
	v_pk_add_f32 v[84:85], v[100:101], v[88:89]
	v_cvt_f16_f32_e32 v67, v67
	v_cvt_f16_f32_e32 v100, v92
	v_cvt_f16_f32_e32 v101, v93
	v_cvt_f16_f32_e32 v94, v94
	v_cvt_f16_f32_e32 v95, v95
	v_cvt_f16_f32_e32 v97, v97
	v_cvt_f16_f32_e32 v98, v98
	v_pk_add_f32 v[86:87], v[86:87], v[124:125]
	v_pk_add_f32 v[80:81], v[102:103], v[126:127]
	v_pk_add_f32 v[82:83], v[104:105], v[128:129]
	v_pk_mov_b32 v[90:91], v[126:127], v[128:129] op_sel:[1,0]
	v_cvt_f16_f32_e32 v96, v96
	v_cvt_f16_f32_e32 v99, v99
	v_add_f32_e32 v102, v62, v126
	v_add_f32_e32 v103, v65, v129
	s_waitcnt vmcnt(0)
	v_pk_add_f32 v[62:63], v[106:107], v[130:131]
	v_cvt_pk_f16_f32 v65, v86, v87
	v_pk_add_f32 v[86:87], v[134:135], v[88:89]
	v_pk_add_f32 v[88:89], v[136:137], v[88:89]
	v_cvt_pk_f16_f32 v80, v80, v81
	v_cvt_pk_f16_f32 v81, v82, v83
	v_pk_add_f32 v[82:83], v[138:139], v[90:91]
	v_pk_add_f32 v[92:93], v[140:141], v[90:91]
	v_cvt_pk_f16_f32 v62, v62, v63
	v_cvt_pk_f16_f32 v63, v84, v85
	v_cvt_pk_f16_f32 v84, v86, v87
	v_cvt_pk_f16_f32 v85, v88, v89
	v_cvt_pk_f16_f32 v86, v82, v83
	v_cvt_pk_f16_f32 v87, v92, v93
	ds_write2_b64 v73, v[64:65], v[80:81] offset1:4
	v_pack_b32_f16 v64, v1, v63
	v_alignbit_b32 v65, v67, v63, 16
	v_pack_b32_f16 v80, v100, v84
	v_alignbit_b32 v81, v101, v84, 16
	v_pack_b32_f16 v82, v94, v85
	v_alignbit_b32 v83, v95, v85, 16
	v_pack_b32_f16 v84, v97, v86
	v_alignbit_b32 v85, v98, v86, 16
	v_pack_b32_f16 v86, v96, v87
	v_alignbit_b32 v87, v99, v87, 16
	ds_write2_b64 v70, v[64:65], v[84:85] offset0:32 offset1:36
	ds_write2_b64 v71, v[80:81], v[86:87] offset0:64 offset1:68
	v_pk_add_f32 v[64:65], v[108:109], v[132:133]
	v_add_f32_e32 v1, v118, v130
	v_cvt_pk_f16_f32 v63, v64, v65
	v_cvt_f16_f32_e32 v1, v1
	v_add_f32_e32 v67, v121, v133
	ds_write_b64 v69, v[62:63] offset:32832
	v_mov_b32_e32 v62, v119
	v_mov_b32_e32 v63, v120
	v_pk_mov_b32 v[64:65], v[130:131], v[132:133] op_sel:[1,0]
	v_cvt_f16_f32_e32 v67, v67
	v_pk_add_f32 v[62:63], v[62:63], v[64:65]
	v_cvt_f16_f32_e32 v102, v102
	v_cvt_pk_f16_f32 v63, v62, v63
	v_pack_b32_f16 v62, v1, v63
	v_add_f32_e32 v1, v114, v130
	v_alignbit_b32 v63, v67, v63, 16
	v_cvt_f16_f32_e32 v1, v1
	ds_write_b64 v69, v[62:63] offset:45376
	v_mov_b32_e32 v62, v115
	v_mov_b32_e32 v63, v116
	v_pk_add_f32 v[62:63], v[62:63], v[64:65]
	v_add_f32_e32 v67, v117, v133
	v_cvt_pk_f16_f32 v63, v62, v63
	v_pack_b32_f16 v62, v1, v63
	v_add_f32_e32 v1, v50, v130
	v_mov_b32_e32 v50, v51
	v_mov_b32_e32 v51, v52
	v_add_f32_e32 v52, v53, v133
	v_cvt_f16_f32_e32 v103, v103
	v_cvt_f16_f32_e32 v67, v67
	v_cvt_f16_f32_e32 v1, v1
	v_cvt_f16_f32_e32 v52, v52
	v_pk_add_f32 v[90:91], v[142:143], v[90:91]
	v_pk_add_f32 v[50:51], v[50:51], v[64:65]
	v_cvt_pk_f16_f32 v89, v90, v91
	v_cvt_pk_f16_f32 v51, v50, v51
	v_pack_b32_f16 v88, v102, v89
	v_alignbit_b32 v89, v103, v89, 16
	v_add_u32_e32 v80, 0x8000, v68
	v_alignbit_b32 v63, v67, v63, 16
	v_pack_b32_f16 v50, v1, v51
	v_alignbit_b32 v51, v52, v51, 16
	ds_write2_b64 v80, v[82:83], v[88:89] offset1:4
	ds_write_b64 v69, v[62:63] offset:57920
	ds_write_b64 v68, v[50:51] offset:32832
	s_waitcnt lgkmcnt(0)
	s_barrier
	global_load_dwordx4 v[82:85], v[58:59], off
	global_load_dwordx4 v[86:89], v[58:59], off offset:1024
	global_load_dwordx4 v[90:93], v[58:59], off offset:2048
	v_add_lshl_u32 v52, v150, v0, 4
	v_mad_u64_u32 v[50:51], s[8:9], v61, s5, v[52:53]
	v_or_b32_e32 v1, 0x200, v0
	v_mad_u32_u24 v51, v60, s4, v52
	v_mul_u32_u24_e32 v52, 0x556, v1
	v_lshrrev_b32_e32 v53, 16, v52
	v_mul_i32_i24_e32 v52, s7, v53
	v_add_lshl_u32 v52, v52, v1, 4
	v_lshlrev_b32_e32 v1, 3, v53
	s_movk_i32 s8, 0xc7
	ds_read_b128 v[60:63], v51 offset:32768
	v_bitop3_b32 v1, v1, s8, v53 bitop3:0xc8
	v_or_b32_e32 v1, s6, v1
	v_mad_u32_u24 v81, v53, s4, v52
	v_mad_u64_u32 v[52:53], s[8:9], v1, s5, v[52:53]
	v_or_b32_e32 v1, 0x400, v0
	v_mul_u32_u24_e32 v53, 0x556, v1
	v_lshrrev_b32_e32 v53, 16, v53
	ds_read_b128 v[94:97], v81 offset:32768
	s_waitcnt lgkmcnt(1)
	buffer_store_dwordx4 v[60:63], v50, s[0:3], 0 offen sc1
	s_waitcnt lgkmcnt(0)
	buffer_store_dwordx4 v[94:97], v52, s[0:3], 0 offen sc1
	v_lshlrev_b32_e32 v61, 3, v53
	v_mul_i32_i24_e32 v60, s7, v53
	v_bitop3_b32 v61, v61, s10, v53 bitop3:0xc8
	v_or_b32_e32 v61, s6, v61
	v_add_lshl_u32 v62, v60, v1, 4
	v_mad_u64_u32 v[60:61], s[8:9], v61, s5, v[62:63]
	v_or_b32_e32 v1, 0x600, v0
	v_mad_u32_u24 v53, v53, s4, v62
	v_mul_u32_u24_e32 v61, 0x556, v1
	ds_read_b128 v[62:65], v53 offset:32768
	v_lshrrev_b32_e32 v67, 16, v61
	v_mul_i32_i24_e32 v94, s7, v67
	v_add_lshl_u32 v98, v94, v1, 4
	v_lshrrev_b32_e32 v1, 13, v61
	v_mad_u32_u24 v160, v67, s4, v98
	v_and_b32_e32 v1, 0x1c0, v1
	v_bfe_u32 v61, v61, 16, 3
	ds_read_b128 v[94:97], v160 offset:32768
	v_or3_b32 v1, s6, v61, v1
	s_waitcnt lgkmcnt(1)
	buffer_store_dwordx4 v[62:65], v60, s[0:3], 0 offen sc1
	s_nop 1
	v_mad_u64_u32 v[62:63], s[8:9], v1, s5, v[98:99]
	v_or_b32_e32 v1, 0x800, v0
	v_mul_u32_u24_e32 v61, 0xaab, v1
	v_lshrrev_b32_e32 v61, 17, v61
	v_mul_i32_i24_e32 v63, s7, v61
	v_lshlrev_b32_e32 v64, 3, v61
	s_waitcnt lgkmcnt(0)
	buffer_store_dwordx4 v[94:97], v62, s[0:3], 0 offen sc1
	v_bitop3_b32 v64, v64, s10, v61 bitop3:0xc8
	v_or_b32_e32 v64, s6, v64
	v_add_lshl_u32 v94, v63, v1, 4
	v_mad_u32_u24 v61, v61, s4, v94
	v_or_b32_e32 v0, 0xa00, v0
	v_mad_u64_u32 v[64:65], s[8:9], v64, s5, v[94:95]
	ds_read_b128 v[94:97], v61 offset:32768
	v_mul_u32_u24_e32 v1, 0xaab, v0
	v_lshrrev_b32_e32 v63, 17, v1
	v_mul_i32_i24_e32 v65, s7, v63
	v_add_lshl_u32 v0, v65, v0, 4
	v_mad_u32_u24 v63, v63, s4, v0
	ds_read_b128 v[98:101], v63 offset:32768
	s_waitcnt lgkmcnt(1)
	buffer_store_dwordx4 v[94:97], v64, s[0:3], 0 offen sc1
	ds_read_b128 v[94:97], v66
	ds_read_b128 v[102:105], v66 offset:8192
	ds_read_b128 v[106:109], v66 offset:16384
	ds_read_b128 v[110:113], v66 offset:24576
	v_lshrrev_b32_e32 v65, 14, v1
	v_and_b32_e32 v65, 0x1c0, v65
	v_bfe_u32 v1, v1, 17, 3
	v_or3_b32 v1, s6, v1, v65
	v_mad_u64_u32 v[66:67], s[4:5], v1, s5, v[0:1]
	s_waitcnt lgkmcnt(4)
	buffer_store_dwordx4 v[98:101], v66, s[0:3], 0 offen sc1
	s_waitcnt lgkmcnt(3)
	s_nop 0
	v_mfma_f32_16x16x32_f16 v[98:101], v[34:37], v[94:97], 0
	s_waitcnt lgkmcnt(2)
	v_mfma_f32_16x16x32_f16 v[114:117], v[34:37], v[102:105], 0
	s_waitcnt lgkmcnt(1)
	v_mfma_f32_16x16x32_f16 v[118:121], v[34:37], v[106:109], 0
	s_waitcnt lgkmcnt(0)
	v_mfma_f32_16x16x32_f16 v[34:37], v[34:37], v[110:113], 0
	v_mfma_f32_16x16x32_f16 v[122:125], v[26:29], v[94:97], 0
	v_mfma_f32_16x16x32_f16 v[126:129], v[26:29], v[102:105], 0
	v_mfma_f32_16x16x32_f16 v[130:133], v[26:29], v[106:109], 0
	v_mfma_f32_16x16x32_f16 v[26:29], v[26:29], v[110:113], 0
	v_mfma_f32_16x16x32_f16 v[94:97], v[22:25], v[94:97], 0
	v_mfma_f32_16x16x32_f16 v[102:105], v[22:25], v[102:105], 0
	v_mfma_f32_16x16x32_f16 v[106:109], v[22:25], v[106:109], 0
	v_mfma_f32_16x16x32_f16 v[22:25], v[22:25], v[110:113], 0
	s_mov_b32 s4, 0x34000
	v_add_co_u32_e32 v158, vcc, s4, v54
	s_mov_b32 s4, 0x35000
	s_nop 0
	v_addc_co_u32_e32 v159, vcc, 0, v55, vcc
	v_add_co_u32_e32 v54, vcc, s4, v54
	s_nop 1
	v_addc_co_u32_e32 v55, vcc, 0, v55, vcc
	global_load_dwordx4 v[110:113], v[54:55], off offset:-4096
	global_load_dwordx4 v[134:137], v[58:59], off offset:3072
	global_load_dwordx4 v[138:141], v[158:159], off offset:1024
	ds_read_b128 v[142:145], v72
	ds_read_b128 v[146:149], v72 offset:8192
	ds_read_b128 v[150:153], v72 offset:16384
	ds_read_b128 v[154:157], v72 offset:24576
	s_waitcnt lgkmcnt(3)
	v_mfma_f32_16x16x32_f16 v[98:101], v[14:17], v[142:145], v[98:101]
	s_waitcnt lgkmcnt(2)
	v_mfma_f32_16x16x32_f16 v[114:117], v[14:17], v[146:149], v[114:117]
	s_waitcnt lgkmcnt(1)
	v_mfma_f32_16x16x32_f16 v[118:121], v[14:17], v[150:153], v[118:121]
	s_waitcnt lgkmcnt(0)
	v_mfma_f32_16x16x32_f16 v[14:17], v[14:17], v[154:157], v[34:37]
	v_mfma_f32_16x16x32_f16 v[34:37], v[6:9], v[142:145], v[122:125]
	v_mfma_f32_16x16x32_f16 v[122:125], v[6:9], v[146:149], v[126:129]
	v_mfma_f32_16x16x32_f16 v[126:129], v[6:9], v[150:153], v[130:133]
	v_mfma_f32_16x16x32_f16 v[6:9], v[6:9], v[154:157], v[26:29]
	v_mfma_f32_16x16x32_f16 v[26:29], v[2:5], v[142:145], v[94:97]
	v_mfma_f32_16x16x32_f16 v[94:97], v[2:5], v[146:149], v[102:105]
	v_mfma_f32_16x16x32_f16 v[102:105], v[2:5], v[150:153], v[106:109]
	v_mfma_f32_16x16x32_f16 v[0:3], v[2:5], v[154:157], v[22:25]
	s_nop 2
	global_load_dwordx4 v[22:25], v[158:159], off offset:2048
	global_load_dwordx4 v[106:109], v[158:159], off offset:3072
	global_load_dwordx4 v[130:133], v[54:55], off
	ds_read_b128 v[142:145], v74
	ds_read_b128 v[146:149], v74 offset:8192
	ds_read_b128 v[150:153], v74 offset:16384
	ds_read_b128 v[154:157], v74 offset:24576
	s_waitcnt lgkmcnt(3)
	v_mfma_f32_16x16x32_f16 v[98:101], v[18:21], v[142:145], v[98:101]
	s_waitcnt lgkmcnt(2)
	v_mfma_f32_16x16x32_f16 v[114:117], v[18:21], v[146:149], v[114:117]
	s_waitcnt lgkmcnt(1)
	v_mfma_f32_16x16x32_f16 v[118:121], v[18:21], v[150:153], v[118:121]
	s_waitcnt lgkmcnt(0)
	v_mfma_f32_16x16x32_f16 v[14:17], v[18:21], v[154:157], v[14:17]
	v_mfma_f32_16x16x32_f16 v[18:21], v[10:13], v[142:145], v[34:37]
	v_mfma_f32_16x16x32_f16 v[34:37], v[10:13], v[146:149], v[122:125]
	v_mfma_f32_16x16x32_f16 v[122:125], v[10:13], v[150:153], v[126:129]
	v_mfma_f32_16x16x32_f16 v[4:7], v[10:13], v[154:157], v[6:9]
	v_mfma_f32_16x16x32_f16 v[8:11], v[30:33], v[142:145], v[26:29]
	v_mfma_f32_16x16x32_f16 v[26:29], v[30:33], v[146:149], v[94:97]
	v_mfma_f32_16x16x32_f16 v[94:97], v[30:33], v[150:153], v[102:105]
	v_mfma_f32_16x16x32_f16 v[0:3], v[30:33], v[154:157], v[0:3]
	global_load_dwordx4 v[30:33], v[54:55], off offset:1024
	s_nop 0
	global_load_dwordx4 v[102:105], v[54:55], off offset:2048
	global_load_dwordx4 v[126:129], v[54:55], off offset:3072
	ds_read_b128 v[142:145], v75
	ds_read_b128 v[146:149], v75 offset:8192
	ds_read_b128 v[150:153], v75 offset:16384
	ds_read_b128 v[154:157], v75 offset:24576
	s_waitcnt lgkmcnt(3)
	v_mfma_f32_16x16x32_f16 v[98:101], v[46:49], v[142:145], v[98:101]
	s_waitcnt lgkmcnt(2)
	v_mfma_f32_16x16x32_f16 v[114:117], v[46:49], v[146:149], v[114:117]
	s_waitcnt lgkmcnt(1)
	v_mfma_f32_16x16x32_f16 v[118:121], v[46:49], v[150:153], v[118:121]
	s_waitcnt lgkmcnt(0)
	v_mfma_f32_16x16x32_f16 v[12:15], v[46:49], v[154:157], v[14:17]
	v_mfma_f32_16x16x32_f16 v[16:19], v[42:45], v[142:145], v[18:21]
	v_mfma_f32_16x16x32_f16 v[34:37], v[42:45], v[146:149], v[34:37]
	v_mfma_f32_16x16x32_f16 v[46:49], v[42:45], v[150:153], v[122:125]
	v_mfma_f32_16x16x32_f16 v[4:7], v[42:45], v[154:157], v[4:7]
	v_mfma_f32_16x16x32_f16 v[8:11], v[38:41], v[142:145], v[8:11]
	v_mfma_f32_16x16x32_f16 v[26:29], v[38:41], v[146:149], v[26:29]
	v_mfma_f32_16x16x32_f16 v[42:45], v[38:41], v[150:153], v[94:97]
	v_mfma_f32_16x16x32_f16 v[0:3], v[38:41], v[154:157], v[0:3]
	ds_read_b128 v[38:41], v76
	s_nop 0
	ds_read_b128 v[94:97], v76 offset:8192
	ds_read_b128 v[122:125], v76 offset:16384
	ds_read_b128 v[142:145], v76 offset:24576
	s_waitcnt vmcnt(17) lgkmcnt(3)
	v_mfma_f32_16x16x32_f16 v[98:101], v[82:85], v[38:41], v[98:101]
	s_waitcnt lgkmcnt(2)
	v_mfma_f32_16x16x32_f16 v[114:117], v[82:85], v[94:97], v[114:117]
	s_waitcnt lgkmcnt(1)
	v_mfma_f32_16x16x32_f16 v[118:121], v[82:85], v[122:125], v[118:121]
	s_waitcnt lgkmcnt(0)
	v_mfma_f32_16x16x32_f16 v[12:15], v[82:85], v[142:145], v[12:15]
	s_waitcnt vmcnt(16)
	v_mfma_f32_16x16x32_f16 v[16:19], v[86:89], v[38:41], v[16:19]
	v_mfma_f32_16x16x32_f16 v[34:37], v[86:89], v[94:97], v[34:37]
	v_mfma_f32_16x16x32_f16 v[46:49], v[86:89], v[122:125], v[46:49]
	v_mfma_f32_16x16x32_f16 v[4:7], v[86:89], v[142:145], v[4:7]
	s_waitcnt vmcnt(15)
	v_mfma_f32_16x16x32_f16 v[8:11], v[90:93], v[38:41], v[8:11]
	v_mfma_f32_16x16x32_f16 v[26:29], v[90:93], v[94:97], v[26:29]
	v_mfma_f32_16x16x32_f16 v[38:41], v[90:93], v[122:125], v[42:45]
	v_mfma_f32_16x16x32_f16 v[0:3], v[90:93], v[142:145], v[0:3]
	s_nop 1
	ds_read_b128 v[42:45], v77
	ds_read_b128 v[82:85], v77 offset:8192
	ds_read_b128 v[86:89], v77 offset:16384
	ds_read_b128 v[74:77], v77 offset:24576
	s_waitcnt vmcnt(7) lgkmcnt(3)
	v_mfma_f32_16x16x32_f16 v[90:93], v[134:137], v[42:45], v[98:101]
	s_waitcnt lgkmcnt(2)
	v_mfma_f32_16x16x32_f16 v[94:97], v[134:137], v[82:85], v[114:117]
	s_waitcnt lgkmcnt(1)
	v_mfma_f32_16x16x32_f16 v[98:101], v[134:137], v[86:89], v[118:121]
	s_waitcnt lgkmcnt(0)
	v_mfma_f32_16x16x32_f16 v[12:15], v[134:137], v[74:77], v[12:15]
	v_mfma_f32_16x16x32_f16 v[16:19], v[110:113], v[42:45], v[16:19]
	v_mfma_f32_16x16x32_f16 v[34:37], v[110:113], v[82:85], v[34:37]
	v_mfma_f32_16x16x32_f16 v[46:49], v[110:113], v[86:89], v[46:49]
	v_mfma_f32_16x16x32_f16 v[4:7], v[110:113], v[74:77], v[4:7]
	s_waitcnt vmcnt(6)
	v_mfma_f32_16x16x32_f16 v[8:11], v[138:141], v[42:45], v[8:11]
	v_mfma_f32_16x16x32_f16 v[26:29], v[138:141], v[82:85], v[26:29]
	v_mfma_f32_16x16x32_f16 v[38:41], v[138:141], v[86:89], v[38:41]
	v_mfma_f32_16x16x32_f16 v[0:3], v[138:141], v[74:77], v[0:3]
	ds_read_b128 v[42:45], v78
	ds_read_b128 v[74:77], v78 offset:8192
	ds_read_b128 v[82:85], v78 offset:16384
	ds_read_b128 v[86:89], v78 offset:24576
	s_waitcnt vmcnt(5) lgkmcnt(3)
	v_mfma_f32_16x16x32_f16 v[90:93], v[22:25], v[42:45], v[90:93]
	s_waitcnt lgkmcnt(2)
	v_mfma_f32_16x16x32_f16 v[94:97], v[22:25], v[74:77], v[94:97]
	s_waitcnt lgkmcnt(1)
	v_mfma_f32_16x16x32_f16 v[98:101], v[22:25], v[82:85], v[98:101]
	s_waitcnt lgkmcnt(0)
	v_mfma_f32_16x16x32_f16 v[12:15], v[22:25], v[86:89], v[12:15]
	s_waitcnt vmcnt(4)
	v_mfma_f32_16x16x32_f16 v[16:19], v[106:109], v[42:45], v[16:19]
	v_mfma_f32_16x16x32_f16 v[20:23], v[106:109], v[74:77], v[34:37]
	v_mfma_f32_16x16x32_f16 v[34:37], v[106:109], v[82:85], v[46:49]
	v_mfma_f32_16x16x32_f16 v[4:7], v[106:109], v[86:89], v[4:7]
	s_waitcnt vmcnt(3)
	v_mfma_f32_16x16x32_f16 v[8:11], v[130:133], v[42:45], v[8:11]
	v_mfma_f32_16x16x32_f16 v[24:27], v[130:133], v[74:77], v[26:29]
	v_mfma_f32_16x16x32_f16 v[38:41], v[130:133], v[82:85], v[38:41]
	v_mfma_f32_16x16x32_f16 v[0:3], v[130:133], v[86:89], v[0:3]
	ds_read_b128 v[42:45], v79
	ds_read_b128 v[46:49], v79 offset:8192
	ds_read_b128 v[74:77], v79 offset:16384
	ds_read_b128 v[82:85], v79 offset:24576
	s_waitcnt vmcnt(2) lgkmcnt(3)
	v_mfma_f32_16x16x32_f16 v[86:89], v[30:33], v[42:45], v[90:93]
	s_waitcnt lgkmcnt(2)
	v_mfma_f32_16x16x32_f16 v[90:93], v[30:33], v[46:49], v[94:97]
	s_waitcnt lgkmcnt(1)
	v_mfma_f32_16x16x32_f16 v[94:97], v[30:33], v[74:77], v[98:101]
	s_waitcnt lgkmcnt(0)
	v_mfma_f32_16x16x32_f16 v[12:15], v[30:33], v[82:85], v[12:15]
	s_waitcnt vmcnt(1)
	v_mfma_f32_16x16x32_f16 v[16:19], v[102:105], v[42:45], v[16:19]
	v_mfma_f32_16x16x32_f16 v[20:23], v[102:105], v[46:49], v[20:23]
	v_mfma_f32_16x16x32_f16 v[28:31], v[102:105], v[74:77], v[34:37]
	v_mfma_f32_16x16x32_f16 v[4:7], v[102:105], v[82:85], v[4:7]
	s_waitcnt vmcnt(0)
	v_mfma_f32_16x16x32_f16 v[8:11], v[126:129], v[42:45], v[8:11]
	v_mfma_f32_16x16x32_f16 v[24:27], v[126:129], v[46:49], v[24:27]
	v_mfma_f32_16x16x32_f16 v[32:35], v[126:129], v[74:77], v[38:41]
	v_mfma_f32_16x16x32_f16 v[0:3], v[126:129], v[82:85], v[0:3]
	s_nop 1
	global_load_dwordx4 v[36:39], v[56:57], off offset:1536
	global_load_dwordx4 v[40:43], v[56:57], off offset:1600
	global_load_dwordx4 v[44:47], v[56:57], off offset:1664
	v_mov_b32_e32 v58, v21
	v_mov_b32_e32 v59, v22
	v_mov_b32_e32 v74, v29
	v_mov_b32_e32 v56, v13
	v_mov_b32_e32 v57, v14
	v_mov_b32_e32 v75, v30
	v_mov_b32_e32 v48, v91
	v_mov_b32_e32 v49, v92
	v_mov_b32_e32 v54, v95
	v_mov_b32_e32 v55, v96
	v_mov_b32_e32 v76, v5
	v_mov_b32_e32 v77, v6
	s_barrier
	s_waitcnt vmcnt(2)
	v_pk_add_f32 v[78:79], v[86:87], v[36:37]
	v_pk_add_f32 v[82:83], v[88:89], v[38:39]
	v_add_f32_e32 v21, v90, v36
	v_pk_mov_b32 v[84:85], v[36:37], v[38:39] op_sel:[1,0]
	v_add_f32_e32 v22, v93, v39
	v_add_f32_e32 v29, v94, v36
	v_add_f32_e32 v36, v12, v36
	v_add_f32_e32 v37, v15, v39
	s_waitcnt vmcnt(1)
	v_add_f32_e32 v38, v20, v40
	v_add_f32_e32 v23, v23, v43
	v_add_f32_e32 v30, v97, v39
	v_pk_add_f32 v[12:13], v[16:17], v[40:41]
	v_pk_add_f32 v[14:15], v[18:19], v[42:43]
	v_pk_mov_b32 v[16:17], v[40:41], v[42:43] op_sel:[1,0]
	v_add_f32_e32 v28, v28, v40
	v_add_f32_e32 v31, v31, v43
	v_add_f32_e32 v39, v4, v40
	v_add_f32_e32 v40, v7, v43
	v_cvt_f16_f32_e32 v41, v21
	v_cvt_f16_f32_e32 v42, v22
	v_cvt_f16_f32_e32 v36, v36
	v_cvt_f16_f32_e32 v37, v37
	v_cvt_f16_f32_e32 v38, v38
	v_cvt_f16_f32_e32 v43, v23
	v_cvt_f16_f32_e32 v29, v29
	v_cvt_f16_f32_e32 v30, v30
	v_cvt_f16_f32_e32 v28, v28
	v_cvt_f16_f32_e32 v31, v31
	v_cvt_f16_f32_e32 v39, v39
	v_cvt_f16_f32_e32 v40, v40
	s_waitcnt vmcnt(0)
	v_pk_add_f32 v[4:5], v[8:9], v[44:45]
	v_pk_add_f32 v[6:7], v[10:11], v[46:47]
	v_pk_add_f32 v[10:11], v[48:49], v[84:85]
	v_pk_add_f32 v[20:21], v[56:57], v[84:85]
	v_cvt_pk_f16_f32 v12, v12, v13
	v_cvt_pk_f16_f32 v13, v14, v15
	v_pk_add_f32 v[14:15], v[58:59], v[16:17]
	v_cvt_pk_f16_f32 v8, v78, v79
	v_cvt_pk_f16_f32 v9, v82, v83
	v_pk_add_f32 v[18:19], v[54:55], v[84:85]
	v_pk_add_f32 v[22:23], v[74:75], v[16:17]
	v_pk_add_f32 v[16:17], v[76:77], v[16:17]
	v_cvt_pk_f16_f32 v4, v4, v5
	v_cvt_pk_f16_f32 v5, v6, v7
	v_cvt_pk_f16_f32 v6, v10, v11
	v_cvt_pk_f16_f32 v10, v20, v21
	v_cvt_pk_f16_f32 v11, v14, v15
	v_cvt_pk_f16_f32 v7, v18, v19
	v_cvt_pk_f16_f32 v14, v22, v23
	v_cvt_pk_f16_f32 v15, v16, v17
	ds_write2_b64 v73, v[8:9], v[12:13] offset1:4
	ds_write_b64 v69, v[4:5] offset:32832
	v_pack_b32_f16 v4, v41, v6
	v_alignbit_b32 v5, v42, v6, 16
	v_pack_b32_f16 v8, v36, v10
	v_alignbit_b32 v9, v37, v10, 16
	v_pack_b32_f16 v10, v38, v11
	v_alignbit_b32 v11, v43, v11, 16
	v_add_f32_e32 v24, v24, v44
	v_pack_b32_f16 v6, v29, v7
	v_alignbit_b32 v7, v30, v7, 16
	v_pack_b32_f16 v12, v28, v14
	v_alignbit_b32 v13, v31, v14, 16
	v_pack_b32_f16 v14, v39, v15
	v_alignbit_b32 v15, v40, v15, 16
	ds_write2_b64 v70, v[4:5], v[10:11] offset0:32 offset1:36
	ds_write2_b64 v71, v[6:7], v[12:13] offset0:64 offset1:68
	ds_write2_b64 v80, v[8:9], v[14:15] offset1:4
	v_add_f32_e32 v8, v27, v47
	v_cvt_f16_f32_e32 v24, v24
	v_cvt_f16_f32_e32 v8, v8
	v_mov_b32_e32 v4, v25
	v_mov_b32_e32 v5, v26
	v_pk_mov_b32 v[6:7], v[44:45], v[46:47] op_sel:[1,0]
	v_add_f32_e32 v9, v35, v47
	v_pk_add_f32 v[4:5], v[4:5], v[6:7]
	v_cvt_f16_f32_e32 v9, v9
	v_cvt_pk_f16_f32 v5, v4, v5
	v_pack_b32_f16 v4, v24, v5
	v_alignbit_b32 v5, v8, v5, 16
	ds_write_b64 v69, v[4:5] offset:45376
	v_add_f32_e32 v4, v32, v44
	v_cvt_f16_f32_e32 v8, v4
	v_mov_b32_e32 v4, v33
	v_mov_b32_e32 v5, v34
	v_pk_add_f32 v[4:5], v[4:5], v[6:7]
	v_add_f32_e32 v0, v0, v44
	v_cvt_pk_f16_f32 v5, v4, v5
	v_pack_b32_f16 v4, v8, v5
	v_alignbit_b32 v5, v9, v5, 16
	ds_write_b64 v69, v[4:5] offset:57920
	v_cvt_f16_f32_e32 v4, v0
	v_mov_b32_e32 v0, v1
	v_mov_b32_e32 v1, v2
	v_add_f32_e32 v2, v3, v47
	v_cvt_f16_f32_e32 v2, v2
	v_pk_add_f32 v[0:1], v[0:1], v[6:7]
	s_nop 0
	v_cvt_pk_f16_f32 v1, v0, v1
	v_pack_b32_f16 v0, v4, v1
	v_alignbit_b32 v1, v2, v1, 16
	ds_write_b64 v68, v[0:1] offset:32832
	s_waitcnt lgkmcnt(0)
	s_barrier
	ds_read_b128 v[0:3], v51 offset:32768
	ds_read_b128 v[4:7], v81 offset:32768
	s_waitcnt lgkmcnt(1)
	buffer_store_dwordx4 v[0:3], v50, s[0:3], 0 offen offset:768 sc1
	ds_read_b128 v[0:3], v53 offset:32768
	ds_read_b128 v[8:11], v160 offset:32768
	ds_read_b128 v[12:15], v61 offset:32768
	ds_read_b128 v[16:19], v63 offset:32768
	s_waitcnt lgkmcnt(4)
	buffer_store_dwordx4 v[4:7], v52, s[0:3], 0 offen offset:768 sc1
	s_waitcnt lgkmcnt(3)
	buffer_store_dwordx4 v[0:3], v60, s[0:3], 0 offen offset:768 sc1
	s_waitcnt lgkmcnt(2)
	buffer_store_dwordx4 v[8:11], v62, s[0:3], 0 offen offset:768 sc1
	s_waitcnt lgkmcnt(1)
	buffer_store_dwordx4 v[12:15], v64, s[0:3], 0 offen offset:768 sc1
	s_waitcnt lgkmcnt(0)
	buffer_store_dwordx4 v[16:19], v66, s[0:3], 0 offen offset:768 sc1
	s_endpgm
	.p2alignl 8, 3212836864
